# replaced serialized ds_bpermute reduction/shuffle chains (LN statistics, RMSNorm, rope partner) by exact DPP moves and permlane swaps; batched table-copy loads
# speedup vs baseline: 1.0092x; 1.0004x over previous
.LBB0_106:
	s_ashr_i32 s7, s6, 31
	s_lshl_b64 s[8:9], s[6:7], 12
	v_lshl_add_u64 v[34:35], v[70:71], 0, s[8:9]
	global_load_dwordx4 v[54:57], v[34:35], off
	global_load_dwordx4 v[50:53], v[34:35], off offset:16
	global_load_dwordx4 v[62:65], v[34:35], off offset:2048
	global_load_dwordx4 v[58:61], v[34:35], off offset:2064
	s_add_i32 s8, s89, s6
	s_ashr_i32 s9, s8, 31
	s_lshl_b64 s[10:11], s[8:9], 12
	v_lshl_add_u64 v[78:79], v[70:71], 0, s[10:11]
	global_load_dwordx4 v[46:49], v[78:79], off
	global_load_dwordx4 v[38:41], v[78:79], off offset:16
	global_load_dwordx4 v[42:45], v[78:79], off offset:2048
	global_load_dwordx4 v[34:37], v[78:79], off offset:2064
	s_lshl_b64 s[14:15], s[6:7], 11
	s_lshl_b64 s[10:11], s[6:7], 10
	s_add_i32 s6, s6, s3
	s_waitcnt vmcnt(7)
	v_mov_b32_e32 v78, v55
	v_mov_b32_e32 v79, v56
	v_mov_b32_e32 v80, v54
	v_mov_b32_e32 v81, v57
	s_waitcnt vmcnt(6)
	v_mov_b32_e32 v82, v51
	v_mov_b32_e32 v83, v52
	v_mov_b32_e32 v84, v50
	v_mov_b32_e32 v85, v53
	v_pk_add_f32 v[78:79], v[78:79], v[80:81]
	v_pk_add_f32 v[80:81], v[82:83], v[84:85]
	v_add_f32_e32 v90, v78, v79
	v_pk_add_f32 v[78:79], v[80:81], v[80:81] op_sel:[0,1] op_sel_hi:[1,0]
	s_waitcnt vmcnt(5)
	v_add_f32_e32 v86, v62, v63
	v_add_f32_e32 v88, v64, v65
	s_waitcnt vmcnt(4)
	v_mov_b32_e32 v91, v58
	v_mov_b32_e32 v87, v60
	v_mov_b32_e32 v89, v61
	v_add_f32_e32 v90, 0, v90
	v_mov_b32_e32 v79, v59
	v_pk_add_f32 v[82:83], v[86:87], v[88:89]
	v_pk_add_f32 v[78:79], v[90:91], v[78:79]
	s_waitcnt vmcnt(3)
	v_mov_b32_e32 v84, v47
	v_pk_add_f32 v[78:79], v[78:79], v[82:83]
	v_mov_b32_e32 v85, v48
	v_add_f32_e32 v82, v78, v79
	s_nop 1
	v_mov_b32_dpp v83, v82 quad_perm:[1,0,3,2] row_mask:0xf bank_mask:0xf
	v_mov_b32_e32 v86, v46
	v_mov_b32_e32 v87, v49
	v_pk_add_f32 v[80:81], v[84:85], v[86:87]
	s_waitcnt vmcnt(2)
	v_mov_b32_e32 v88, v39
	v_add_f32_e32 v80, v80, v81
	v_mov_b32_e32 v89, v40
	v_mov_b32_e32 v92, v38
	v_mov_b32_e32 v93, v41
	v_add_f32_e32 v98, 0, v80
	s_waitcnt lgkmcnt(0)
	v_add_f32_e32 v80, v82, v83
	v_pk_add_f32 v[84:85], v[88:89], v[92:93]
	s_nop 1
	v_mov_b32_dpp v81, v80 quad_perm:[2,3,0,1] row_mask:0xf bank_mask:0xf
	v_pk_add_f32 v[78:79], v[84:85], v[84:85] op_sel:[0,1] op_sel_hi:[1,0]
	s_waitcnt vmcnt(1)
	v_add_f32_e32 v94, v42, v43
	v_add_f32_e32 v96, v44, v45
	s_waitcnt vmcnt(0)
	v_mov_b32_e32 v99, v34
	v_mov_b32_e32 v95, v36
	v_mov_b32_e32 v97, v37
	v_mov_b32_e32 v79, v35
	v_pk_add_f32 v[86:87], v[94:95], v[96:97]
	v_pk_add_f32 v[78:79], v[98:99], v[78:79]
	s_waitcnt lgkmcnt(0)
	v_add_f32_e32 v80, v80, v81
	v_pk_add_f32 v[78:79], v[78:79], v[86:87]
	s_nop 1
	v_mov_b32_dpp v81, v80 row_shl:4 row_mask:0xf bank_mask:0x5
	v_mov_b32_dpp v81, v80 row_shr:4 row_mask:0xf bank_mask:0xa
	v_add_f32_e32 v78, v78, v79
	s_nop 1
	v_mov_b32_dpp v79, v78 quad_perm:[1,0,3,2] row_mask:0xf bank_mask:0xf
	s_waitcnt lgkmcnt(0)
	v_add_f32_e32 v80, v80, v81
	s_nop 1
	v_mov_b32_dpp v81, v80 row_shl:8 row_mask:0xf bank_mask:0x3
	v_mov_b32_dpp v81, v80 row_shr:8 row_mask:0xf bank_mask:0xc
	s_waitcnt lgkmcnt(0)
	v_add_f32_e32 v78, v78, v79
	s_nop 1
	v_mov_b32_dpp v79, v78 quad_perm:[2,3,0,1] row_mask:0xf bank_mask:0xf
	s_waitcnt lgkmcnt(0)
	v_add_f32_e32 v80, v80, v81
	ds_bpermute_b32 v81, v76, v80
	s_waitcnt lgkmcnt(1)
	v_add_f32_e32 v78, v78, v79
	s_nop 1
	v_mov_b32_dpp v79, v78 row_shl:4 row_mask:0xf bank_mask:0x5
	v_mov_b32_dpp v79, v78 row_shr:4 row_mask:0xf bank_mask:0xa
	s_waitcnt lgkmcnt(0)
	v_add_f32_e32 v80, v80, v81
	ds_bpermute_b32 v81, v77, v80
	s_waitcnt lgkmcnt(1)
	v_add_f32_e32 v78, v78, v79
	s_nop 1
	v_mov_b32_dpp v79, v78 row_shl:8 row_mask:0xf bank_mask:0x3
	v_mov_b32_dpp v79, v78 row_shr:8 row_mask:0xf bank_mask:0xc
	s_waitcnt lgkmcnt(0)
	v_add_f32_e32 v89, v78, v79
	v_add_f32_e32 v78, v80, v81
	v_fmamk_f32 v55, v78, 0xba800000, v55
	v_fmamk_f32 v54, v78, 0xba800000, v54
	v_fmamk_f32 v57, v78, 0xba800000, v57
	v_fmac_f32_e32 v56, 0xba800000, v78
	v_fmamk_f32 v51, v78, 0xba800000, v51
	v_fmamk_f32 v50, v78, 0xba800000, v50
	v_fmamk_f32 v53, v78, 0xba800000, v53
	v_fmac_f32_e32 v52, 0xba800000, v78
	v_fmamk_f32 v63, v78, 0xba800000, v63
	v_fmamk_f32 v62, v78, 0xba800000, v62
	v_fmamk_f32 v65, v78, 0xba800000, v65
	v_fmac_f32_e32 v64, 0xba800000, v78
	v_fmamk_f32 v61, v78, 0xba800000, v61
	v_fmamk_f32 v60, v78, 0xba800000, v60
	v_fmamk_f32 v59, v78, 0xba800000, v59
	v_fmac_f32_e32 v58, 0xba800000, v78
	v_pk_mul_f32 v[78:79], v[56:57], v[56:57]
	v_pk_mul_f32 v[80:81], v[54:55], v[54:55]
	v_pk_mul_f32 v[82:83], v[52:53], v[52:53]
	v_pk_mul_f32 v[84:85], v[50:51], v[50:51]
	v_pk_mov_b32 v[90:91], v[80:81], v[78:79] op_sel:[1,0]
	v_mov_b32_e32 v81, v79
	v_pk_mov_b32 v[78:79], v[84:85], v[82:83] op_sel:[1,0]
	v_mov_b32_e32 v85, v83
	v_mul_f32_e32 v86, v62, v62
	v_mul_f32_e32 v88, v64, v64
	v_pk_add_f32 v[80:81], v[90:91], v[80:81]
	v_pk_add_f32 v[78:79], v[78:79], v[84:85]
	v_pk_fma_f32 v[82:83], v[62:63], v[62:63], v[86:87] op_sel_hi:[1,1,0]
	v_pk_fma_f32 v[86:87], v[64:65], v[64:65], v[88:89] op_sel_hi:[1,1,0]
	v_pk_add_f32 v[80:81], v[80:81], v[80:81] op_sel_hi:[0,1]
	v_pk_add_f32 v[78:79], v[78:79], v[78:79] op_sel_hi:[0,1]
	v_mul_f32_e32 v82, v58, v58
	v_mul_f32_e32 v86, v59, v59
	v_mul_f32_e32 v80, v60, v60
	v_mul_f32_e32 v78, v61, v61
	v_pk_add_f32 v[82:83], v[82:83], v[86:87]
	v_pk_add_f32 v[78:79], v[80:81], v[78:79]
	ds_bpermute_b32 v92, v76, v89
	v_pk_add_f32 v[78:79], v[82:83], v[78:79]
	s_waitcnt lgkmcnt(0)
	v_add_f32_e32 v80, v89, v92
	v_add_f32_e32 v78, v78, v79
	s_nop 1
	v_mov_b32_dpp v79, v78 quad_perm:[1,0,3,2] row_mask:0xf bank_mask:0xf
	ds_bpermute_b32 v81, v77, v80
	s_waitcnt lgkmcnt(1)
	v_add_f32_e32 v78, v78, v79
	s_nop 1
	v_mov_b32_dpp v79, v78 quad_perm:[2,3,0,1] row_mask:0xf bank_mask:0xf
	s_waitcnt lgkmcnt(0)
	v_add_f32_e32 v88, v80, v81
	v_fmamk_f32 v47, v88, 0xba800000, v47
	v_fmamk_f32 v46, v88, 0xba800000, v46
	v_fmamk_f32 v49, v88, 0xba800000, v49
	s_waitcnt lgkmcnt(0)
	v_add_f32_e32 v80, v78, v79
	s_nop 1
	v_mov_b32_dpp v81, v80 row_shl:4 row_mask:0xf bank_mask:0x5
	v_mov_b32_dpp v81, v80 row_shr:4 row_mask:0xf bank_mask:0xa
	v_fmac_f32_e32 v48, 0xba800000, v88
	v_fmamk_f32 v79, v88, 0xba800000, v39
	v_fmamk_f32 v78, v88, 0xba800000, v38
	v_fmamk_f32 v41, v88, 0xba800000, v41
	s_waitcnt lgkmcnt(0)
	v_add_f32_e32 v80, v80, v81
	s_nop 1
	v_mov_b32_dpp v81, v80 row_shl:8 row_mask:0xf bank_mask:0x3
	v_mov_b32_dpp v81, v80 row_shr:8 row_mask:0xf bank_mask:0xc
	v_fmac_f32_e32 v40, 0xba800000, v88
	v_pk_mul_f32 v[38:39], v[48:49], v[48:49]
	v_pk_mul_f32 v[82:83], v[40:41], v[40:41]
	v_pk_mul_f32 v[84:85], v[78:79], v[78:79]
	s_waitcnt lgkmcnt(0)
	v_add_f32_e32 v89, v80, v81
	ds_bpermute_b32 v90, v76, v89
	v_pk_mul_f32 v[80:81], v[46:47], v[46:47]
	v_fmamk_f32 v42, v88, 0xba800000, v42
	v_pk_mov_b32 v[86:87], v[80:81], v[38:39] op_sel:[1,0]
	v_mov_b32_e32 v81, v39
	s_waitcnt lgkmcnt(0)
	v_add_f32_e32 v89, v89, v90
	ds_bpermute_b32 v90, v77, v89
	v_pk_mov_b32 v[38:39], v[84:85], v[82:83] op_sel:[1,0]
	v_mov_b32_e32 v85, v83
	v_pk_add_f32 v[38:39], v[38:39], v[84:85]
	v_fmamk_f32 v43, v88, 0xba800000, v43
	s_waitcnt lgkmcnt(0)
	v_add_f32_e32 v82, v89, v90
	v_fmamk_f32 v82, v82, 0x3a800000, v1
	v_rsq_f32_e32 v82, v82
	v_pk_add_f32 v[38:39], v[38:39], v[38:39] op_sel_hi:[0,1]
	v_fmac_f32_e32 v44, 0xba800000, v88
	v_mul_f32_e32 v38, v42, v42
	v_pk_add_f32 v[80:81], v[86:87], v[80:81]
	v_pk_mul_f32 v[54:55], v[54:55], v[82:83] op_sel_hi:[1,0]
	v_pk_mul_f32 v[56:57], v[56:57], v[82:83] op_sel_hi:[1,0]
	v_pk_mul_f32 v[50:51], v[50:51], v[82:83] op_sel_hi:[1,0]
	v_pk_mul_f32 v[52:53], v[52:53], v[82:83] op_sel_hi:[1,0]
	v_pk_mul_f32 v[62:63], v[62:63], v[82:83] op_sel_hi:[1,0]
	v_pk_mul_f32 v[64:65], v[64:65], v[82:83] op_sel_hi:[1,0]
	v_pk_mul_f32 v[58:59], v[58:59], v[82:83] op_sel_hi:[1,0]
	v_pk_mul_f32 v[60:61], v[60:61], v[82:83] op_sel_hi:[1,0]
	v_fmamk_f32 v45, v88, 0xba800000, v45
	v_pk_fma_f32 v[82:83], v[42:43], v[42:43], v[38:39] op_sel_hi:[1,1,0]
	v_mul_f32_e32 v38, v44, v44
	v_pk_add_f32 v[80:81], v[80:81], v[80:81] op_sel_hi:[0,1]
	v_pk_fma_f32 v[84:85], v[44:45], v[44:45], v[38:39] op_sel_hi:[1,1,0]
	v_fmamk_f32 v87, v88, 0xba800000, v37
	v_fmamk_f32 v86, v88, 0xba800000, v36
	v_fmamk_f32 v35, v88, 0xba800000, v35
	v_fmac_f32_e32 v34, 0xba800000, v88
	v_mul_f32_e32 v82, v34, v34
	v_mul_f32_e32 v84, v35, v35
	v_mul_f32_e32 v80, v86, v86
	v_mul_f32_e32 v38, v87, v87
	v_pk_add_f32 v[36:37], v[82:83], v[84:85]
	v_pk_add_f32 v[38:39], v[80:81], v[38:39]
	v_pk_fma_f32 v[56:57], v[8:9], v[56:57], v[16:17]
	v_pk_add_f32 v[36:37], v[36:37], v[38:39]
	v_pk_fma_f32 v[54:55], v[6:7], v[54:55], v[14:15]
	v_add_f32_e32 v38, v36, v37
	s_nop 1
	v_mov_b32_dpp v39, v38 quad_perm:[1,0,3,2] row_mask:0xf bank_mask:0xf
	v_pk_fma_f32 v[52:53], v[4:5], v[52:53], v[12:13]
	v_pk_fma_f32 v[50:51], v[2:3], v[50:51], v[10:11]
	v_pk_fma_f32 v[64:65], v[24:25], v[64:65], v[32:33]
	v_pk_fma_f32 v[62:63], v[22:23], v[62:63], v[30:31]
	s_waitcnt lgkmcnt(0)
	v_add_f32_e32 v82, v38, v39
	s_nop 1
	v_mov_b32_dpp v83, v82 quad_perm:[2,3,0,1] row_mask:0xf bank_mask:0xf
	v_pk_fma_f32 v[60:61], v[20:21], v[60:61], v[28:29]
	v_pk_fma_f32 v[58:59], v[18:19], v[58:59], v[26:27]
	v_lshl_add_u64 v[80:81], v[66:67], 0, s[14:15]
	v_cvt_pk_bf16_f32 v36, v54, v55
	s_waitcnt lgkmcnt(0)
	v_add_f32_e32 v82, v82, v83
	s_nop 1
	v_mov_b32_dpp v83, v82 row_shl:4 row_mask:0xf bank_mask:0x5
	v_mov_b32_dpp v83, v82 row_shr:4 row_mask:0xf bank_mask:0xa
	v_cvt_pk_bf16_f32 v37, v56, v57
	v_cvt_pk_bf16_f32 v38, v50, v51
	v_cvt_pk_bf16_f32 v39, v52, v53
	global_store_dwordx4 v[80:81], v[36:39], off
	s_nop 1
	v_cvt_pk_bf16_f32 v36, v62, v63
	v_cvt_pk_bf16_f32 v37, v64, v65
	v_cvt_pk_bf16_f32 v38, v58, v59
	v_cvt_pk_bf16_f32 v39, v60, v61
	global_store_dwordx4 v[80:81], v[36:39], off offset:1024
	s_waitcnt lgkmcnt(0)
	s_nop 0
	v_add_f32_e32 v38, v82, v83
	s_nop 1
	v_mov_b32_dpp v39, v38 row_shl:8 row_mask:0xf bank_mask:0x3
	v_mov_b32_dpp v39, v38 row_shr:8 row_mask:0xf bank_mask:0xc
	v_mov_b32_e32 v37, 0
	v_cvt_pk_fp8_f32 v37, v50, v51
	v_mov_b32_e32 v36, 0
	v_cvt_pk_fp8_f32 v36, v54, v55
	s_waitcnt lgkmcnt(0)
	v_add_f32_e32 v50, v38, v39
	ds_bpermute_b32 v51, v76, v50
	v_mov_b32_e32 v38, 0
	v_mov_b32_e32 v39, 0
	v_cvt_pk_fp8_f32 v38, v62, v63
	v_cvt_pk_fp8_f32 v39, v58, v59
	s_waitcnt lgkmcnt(0)
	v_add_f32_e32 v50, v50, v51
	ds_bpermute_b32 v51, v77, v50
	v_cvt_pk_fp8_f32 v36, v56, v57 op_sel:[0,0,1]
	v_cvt_pk_fp8_f32 v37, v52, v53 op_sel:[0,0,1]
	v_cvt_pk_fp8_f32 v38, v64, v65 op_sel:[0,0,1]
	v_cvt_pk_fp8_f32 v39, v60, v61 op_sel:[0,0,1]
	s_waitcnt lgkmcnt(0)
	v_add_f32_e32 v50, v50, v51
	v_fmamk_f32 v50, v50, 0x3a800000, v1
	v_rsq_f32_e32 v50, v50
	v_lshl_add_u64 v[52:53], v[68:69], 0, s[10:11]
	global_store_dwordx2 v[52:53], v[36:37], off
	global_store_dwordx2 v[52:53], v[38:39], off offset:512
	s_lshl_b64 s[10:11], s[8:9], 10
	v_pk_mul_f32 v[36:37], v[46:47], v[50:51] op_sel_hi:[1,0]
	v_pk_mul_f32 v[38:39], v[48:49], v[50:51] op_sel_hi:[1,0]
	v_pk_fma_f32 v[46:47], v[6:7], v[36:37], v[14:15]
	v_pk_mul_f32 v[36:37], v[78:79], v[50:51] op_sel_hi:[1,0]
	v_pk_mul_f32 v[40:41], v[40:41], v[50:51] op_sel_hi:[1,0]
	v_pk_fma_f32 v[48:49], v[2:3], v[36:37], v[10:11]
	v_pk_mul_f32 v[36:37], v[42:43], v[50:51] op_sel_hi:[1,0]
	v_pk_fma_f32 v[38:39], v[8:9], v[38:39], v[16:17]
	v_pk_fma_f32 v[40:41], v[4:5], v[40:41], v[12:13]
	v_pk_mul_f32 v[42:43], v[44:45], v[50:51] op_sel_hi:[1,0]
	v_pk_fma_f32 v[44:45], v[22:23], v[36:37], v[30:31]
	v_pk_mul_f32 v[34:35], v[34:35], v[50:51] op_sel_hi:[1,0]
	v_pk_mul_f32 v[36:37], v[86:87], v[50:51] op_sel_hi:[1,0]
	s_lshl_b64 s[8:9], s[8:9], 11
	v_pk_fma_f32 v[42:43], v[24:25], v[42:43], v[32:33]
	v_pk_fma_f32 v[50:51], v[20:21], v[36:37], v[28:29]
	v_pk_fma_f32 v[52:53], v[18:19], v[34:35], v[26:27]
	v_lshl_add_u64 v[54:55], v[66:67], 0, s[8:9]
	v_cvt_pk_bf16_f32 v34, v46, v47
	v_cvt_pk_bf16_f32 v35, v38, v39
	v_cvt_pk_bf16_f32 v36, v48, v49
	v_cvt_pk_bf16_f32 v37, v40, v41
	global_store_dwordx4 v[54:55], v[34:37], off
	v_mov_b32_e32 v56, 0
	v_mov_b32_e32 v57, 0
	v_cvt_pk_bf16_f32 v34, v44, v45
	v_cvt_pk_bf16_f32 v35, v42, v43
	v_cvt_pk_bf16_f32 v36, v52, v53
	v_cvt_pk_bf16_f32 v37, v50, v51
	global_store_dwordx4 v[54:55], v[34:37], off offset:1024
	v_cvt_pk_fp8_f32 v56, v46, v47
	v_cvt_pk_fp8_f32 v57, v48, v49
	v_mov_b32_e32 v34, 0
	v_mov_b32_e32 v35, 0
	v_cvt_pk_fp8_f32 v34, v44, v45
	v_cvt_pk_fp8_f32 v35, v52, v53
	v_cvt_pk_fp8_f32 v56, v38, v39 op_sel:[0,0,1]
	v_cvt_pk_fp8_f32 v57, v40, v41 op_sel:[0,0,1]
	v_cvt_pk_fp8_f32 v34, v42, v43 op_sel:[0,0,1]
	v_cvt_pk_fp8_f32 v35, v50, v51 op_sel:[0,0,1]
	v_lshl_add_u64 v[36:37], v[68:69], 0, s[10:11]
	s_cmp_lt_i32 s6, 0x8000
	global_store_dwordx2 v[36:37], v[56:57], off
	global_store_dwordx2 v[36:37], v[34:35], off offset:512
	s_cbranch_scc1 .LBB0_106

.LBB0_270:
	s_ashr_i32 s19, s18, 31
	s_lshl_b64 s[20:21], s[18:19], 12
	v_lshl_add_u64 v[12:13], v[42:43], 0, s[20:21]
	global_load_dwordx4 v[28:31], v[12:13], off
	v_add_u32_e32 v74, s18, v124
	v_ashrrev_i32_e32 v75, 31, v74
	v_lshlrev_b64 v[12:13], 12, v[74:75]
	v_add_u32_e32 v72, s18, v122
	v_lshl_add_u64 v[12:13], v[46:47], 0, v[12:13]
	v_ashrrev_i32_e32 v73, 31, v72
	global_load_dwordx4 v[24:27], v[12:13], off
	v_lshlrev_b64 v[12:13], 12, v[72:73]
	v_add_u32_e32 v70, s18, v120
	v_lshl_add_u64 v[12:13], v[48:49], 0, v[12:13]
	v_ashrrev_i32_e32 v71, 31, v70
	s_add_i32 s20, s27, s18
	global_load_dwordx4 v[20:23], v[12:13], off
	v_lshlrev_b64 v[12:13], 12, v[70:71]
	s_ashr_i32 s21, s20, 31
	v_lshl_add_u64 v[12:13], v[50:51], 0, v[12:13]
	s_lshl_b64 s[22:23], s[20:21], 12
	global_load_dwordx4 v[16:19], v[12:13], off
	v_lshl_add_u64 v[12:13], v[52:53], 0, s[22:23]
	s_lshr_b32 s22, s18, 6
	global_load_dwordx4 v[12:15], v[12:13], off
	s_waitcnt vmcnt(4)
	v_and_b32_e32 v125, 0xffff0000, v28
	v_lshlrev_b32_e32 v38, 16, v28
	v_mul_f32_e32 v2, v125, v125
	v_lshlrev_b32_e32 v134, 16, v29
	v_fmac_f32_e32 v2, v38, v38
	v_and_b32_e32 v135, 0xffff0000, v29
	v_fmac_f32_e32 v2, v134, v134
	v_lshlrev_b32_e32 v136, 16, v30
	v_fmac_f32_e32 v2, v135, v135
	v_and_b32_e32 v137, 0xffff0000, v30
	v_fmac_f32_e32 v2, v136, v136
	v_lshlrev_b32_e32 v36, 16, v31
	v_and_b32_e32 v37, 0xffff0000, v31
	v_fmac_f32_e32 v2, v137, v137
	v_pk_mul_f32 v[28:29], v[36:37], v[36:37]
	s_waitcnt vmcnt(3)
	v_and_b32_e32 v141, 0xffff0000, v27
	v_add_f32_e32 v2, v2, v28
	v_add_f32_e32 v2, v2, v29
	s_nop 1
	v_mov_b32_dpp v28, v2 quad_perm:[1,0,3,2] row_mask:0xf bank_mask:0xf
	v_mov_b32_e32 v29, s22
	s_lshl_b64 s[22:23], s[18:19], 9
	s_waitcnt lgkmcnt(0)
	v_add_f32_e32 v2, v2, v28
	s_nop 1
	v_mov_b32_dpp v28, v2 quad_perm:[2,3,0,1] row_mask:0xf bank_mask:0xf
	s_waitcnt lgkmcnt(0)
	v_add_f32_e32 v2, v2, v28
	s_nop 1
	v_mov_b32_dpp v28, v2 row_shl:4 row_mask:0xf bank_mask:0x5
	v_mov_b32_dpp v28, v2 row_shr:4 row_mask:0xf bank_mask:0xa
	s_waitcnt lgkmcnt(0)
	v_add_f32_e32 v2, v2, v28
	v_fmamk_f32 v2, v2, 0x3c800000, v248
	v_rsq_f32_e32 v2, v2
	v_mov_b32_e32 v28, s18
	v_cndmask_b32_e64 v28, v28, v29, s[40:41]
	v_lshlrev_b32_e32 v28, 6, v28
	v_mul_f32_e32 v38, v2, v38
	v_and_b32_e32 v28, 0xfc0, v28
	v_mul_f32_e32 v38, v38, v4
	v_add_u32_e32 v32, v82, v28
	s_nop 1
	v_mov_b32_dpp v39, v38 quad_perm:[2,3,0,1] row_mask:0xf bank_mask:0xf
	ds_read_b128 v[126:129], v32
	ds_read_b128 v[28:31], v32 offset:16
	ds_read_b128 v[130:133], v32 offset:4096
	ds_read_b128 v[32:35], v32 offset:4112
	s_waitcnt lgkmcnt(3)
	v_mov_b32_e32 v76, v126
	v_cndmask_b32_e64 v39, v39, -v39, vcc
	s_waitcnt lgkmcnt(1)
	v_mov_b32_e32 v77, v130
	v_pk_mul_f32 v[38:39], v[38:39], v[76:77]
	v_mov_b32_e32 v130, v127
	v_add_f32_e32 v38, v38, v39
	v_mul_f32_e32 v126, 0x3fb8aa3b, v38
	v_mul_f32_e32 v38, v2, v125
	v_mul_f32_e32 v38, v38, v5
	s_nop 1
	v_mov_b32_dpp v39, v38 quad_perm:[2,3,0,1] row_mask:0xf bank_mask:0xf
	v_mov_b32_e32 v76, v128
	v_mov_b32_e32 v77, v132
	v_mov_b32_e32 v132, v129
	s_waitcnt lgkmcnt(0)
	v_cndmask_b32_e64 v39, v39, -v39, vcc
	v_pk_mul_f32 v[38:39], v[38:39], v[130:131]
	v_lshlrev_b32_e32 v130, 16, v27
	v_add_f32_e32 v38, v38, v39
	v_mul_f32_e32 v125, 0x3fb8aa3b, v38
	v_mul_f32_e32 v38, v2, v134
	v_mul_f32_e32 v38, v38, v6
	s_nop 1
	v_mov_b32_dpp v39, v38 quad_perm:[2,3,0,1] row_mask:0xf bank_mask:0xf
	s_waitcnt lgkmcnt(0)
	v_cndmask_b32_e64 v39, v39, -v39, vcc
	v_pk_mul_f32 v[38:39], v[38:39], v[76:77]
	v_mov_b32_e32 v76, v28
	v_add_f32_e32 v38, v38, v39
	v_mul_f32_e32 v127, 0x3fb8aa3b, v38
	v_mul_f32_e32 v38, v2, v135
	v_mul_f32_e32 v38, v38, v7
	s_nop 1
	v_mov_b32_dpp v39, v38 quad_perm:[2,3,0,1] row_mask:0xf bank_mask:0xf
	v_mov_b32_e32 v77, v32
	v_mov_b32_e32 v32, v29
	s_waitcnt lgkmcnt(0)
	v_cndmask_b32_e64 v39, v39, -v39, vcc
	v_pk_mul_f32 v[38:39], v[38:39], v[132:133]
	s_nop 0
	v_add_f32_e32 v38, v38, v39
	v_mul_f32_e32 v128, 0x3fb8aa3b, v38
	v_mul_f32_e32 v38, v2, v136
	v_mul_f32_e32 v38, v38, v8
	s_nop 1
	v_mov_b32_dpp v39, v38 quad_perm:[2,3,0,1] row_mask:0xf bank_mask:0xf
	s_waitcnt lgkmcnt(0)
	v_cndmask_b32_e64 v39, v39, -v39, vcc
	v_pk_mul_f32 v[38:39], v[38:39], v[76:77]
	v_lshlrev_b32_e32 v77, 16, v25
	v_add_f32_e32 v28, v38, v39
	v_mul_f32_e32 v76, 0x3fb8aa3b, v28
	v_mul_f32_e32 v28, v2, v137
	v_mul_f32_e32 v38, v28, v9
	s_nop 1
	v_mov_b32_dpp v28, v38 quad_perm:[2,3,0,1] row_mask:0xf bank_mask:0xf
	s_waitcnt lgkmcnt(0)
	v_cndmask_b32_e64 v39, v28, -v28, vcc
	v_pk_mul_f32 v[28:29], v[38:39], v[32:33]
	v_mov_b32_e32 v32, v30
	v_add_f32_e32 v28, v28, v29
	v_mul_f32_e32 v38, 0x3fb8aa3b, v28
	v_mul_f32_e32 v28, v2, v36
	v_mul_f32_e32 v28, v28, v10
	s_nop 1
	v_mov_b32_dpp v29, v28 quad_perm:[2,3,0,1] row_mask:0xf bank_mask:0xf
	v_mov_b32_e32 v33, v34
	v_mul_f32_e32 v2, v2, v37
	v_mov_b32_e32 v34, v31
	s_waitcnt lgkmcnt(0)
	v_cndmask_b32_e64 v29, v29, -v29, vcc
	v_pk_mul_f32 v[28:29], v[28:29], v[32:33]
	s_nop 0
	v_add_f32_e32 v28, v28, v29
	v_mul_f32_e32 v30, 0x3fb8aa3b, v28
	v_mul_f32_e32 v28, v2, v11
	s_nop 1
	v_mov_b32_dpp v2, v28 quad_perm:[2,3,0,1] row_mask:0xf bank_mask:0xf
	s_waitcnt lgkmcnt(0)
	v_cndmask_b32_e64 v29, v2, -v2, vcc
	v_pk_mul_f32 v[28:29], v[28:29], v[34:35]
	s_nop 0
	v_add_f32_e32 v2, v28, v29
	v_mov_b32_e32 v29, v3
	v_cvt_pk_fp8_f32 v29, v76, v38
	v_mul_f32_e32 v2, 0x3fb8aa3b, v2
	v_mov_b32_e32 v28, v3
	v_and_b32_e32 v76, 0xffff0000, v24
	v_cvt_pk_fp8_f32 v28, v126, v125
	v_cvt_pk_fp8_f32 v29, v30, v2 op_sel:[0,0,1]
	v_lshlrev_b32_e32 v2, 16, v24
	v_mul_f32_e32 v24, v76, v76
	v_fmac_f32_e32 v24, v2, v2
	v_and_b32_e32 v125, 0xffff0000, v25
	v_fmac_f32_e32 v24, v77, v77
	v_lshlrev_b32_e32 v126, 16, v26
	v_fmac_f32_e32 v24, v125, v125
	v_cvt_pk_fp8_f32 v28, v127, v128 op_sel:[0,0,1]
	v_and_b32_e32 v127, 0xffff0000, v26
	v_fmac_f32_e32 v24, v126, v126
	v_fmac_f32_e32 v24, v127, v127
	v_fmac_f32_e32 v24, v130, v130
	v_fmac_f32_e32 v24, v141, v141
	s_nop 1
	v_mov_b32_dpp v25, v24 quad_perm:[1,0,3,2] row_mask:0xf bank_mask:0xf
	v_lshl_add_u64 v[30:31], v[44:45], 0, s[22:23]
	global_store_dwordx2 v[30:31], v[28:29], off
	s_waitcnt lgkmcnt(0)
	v_add_f32_e32 v24, v24, v25
	s_nop 1
	v_mov_b32_dpp v25, v24 quad_perm:[2,3,0,1] row_mask:0xf bank_mask:0xf
	s_waitcnt lgkmcnt(0)
	v_add_f32_e32 v24, v24, v25
	s_nop 1
	v_mov_b32_dpp v25, v24 row_shl:4 row_mask:0xf bank_mask:0x5
	v_mov_b32_dpp v25, v24 row_shr:4 row_mask:0xf bank_mask:0xa
	s_waitcnt lgkmcnt(0)
	v_add_f32_e32 v24, v24, v25
	v_fmamk_f32 v24, v24, 0x3c800000, v248
	v_rsq_f32_e32 v142, v24
	v_and_b32_e32 v24, 63, v74
	v_bfe_u32 v25, v74, 6, 6
	v_cndmask_b32_e64 v24, v24, v25, s[40:41]
	v_mul_f32_e32 v2, v142, v2
	v_mul_f32_e32 v137, v2, v83
	v_mul_f32_e32 v2, v142, v76
	v_mul_f32_e32 v135, v2, v84
	v_mul_f32_e32 v2, v142, v77
	v_mul_f32_e32 v133, v2, v85
	v_mul_f32_e32 v2, v142, v125
	v_mul_f32_e32 v131, v2, v86
	v_mul_f32_e32 v2, v142, v126
	v_mul_f32_e32 v129, v2, v87
	v_mul_f32_e32 v2, v142, v127
	v_lshl_add_u32 v28, v24, 6, v82
	v_mul_f32_e32 v128, v2, v88
	v_mul_f32_e32 v2, v142, v130
	ds_read_b128 v[32:35], v28
	ds_read_b128 v[24:27], v28 offset:16
	ds_read_b128 v[36:39], v28 offset:4096
	ds_read_b128 v[28:31], v28 offset:4112
	v_mul_f32_e32 v126, v2, v89
	v_mul_f32_e32 v2, v142, v141
	v_mul_f32_e32 v125, v2, v90
	ds_bpermute_b32 v140, v80, v137
	ds_bpermute_b32 v139, v80, v135
	ds_bpermute_b32 v138, v80, v133
	ds_bpermute_b32 v136, v80, v131
	ds_bpermute_b32 v134, v80, v129
	ds_bpermute_b32 v132, v80, v128
	ds_bpermute_b32 v130, v80, v126
	ds_bpermute_b32 v127, v80, v125
	s_and_saveexec_b64 s[22:23], s[42:43]
	s_xor_b64 s[22:23], exec, s[22:23]
	s_cbranch_execz .LBB0_272
	v_alignbit_b32 v76, v75, v74, 11
	v_and_b32_e32 v76, -2, v76
	v_and_b32_e32 v77, 0x3fff, v75
	v_and_b32_e32 v2, 0xfff, v74
	v_lshl_add_u64 v[76:77], v[76:77], 0, v[54:55]
	v_lshlrev_b64 v[76:77], 18, v[76:77]
	v_lshlrev_b32_e32 v2, 6, v2
	v_and_b32_e32 v2, 0x3f000, v2
	v_lshl_add_u64 v[76:77], s[16:17], 0, v[76:77]
	v_lshl_add_u64 v[76:77], v[76:77], 0, v[2:3]
	v_add_u32_e32 v2, s31, v123
	v_and_b32_e32 v2, 0xfc0, v2
	v_lshl_add_u64 v[76:77], v[76:77], 0, v[2:3]
	v_lshrrev_b32_e32 v2, 2, v74
	v_bitop3_b32 v2, v2, v78, 3 bitop3:0x6c
	v_lshlrev_b32_e32 v2, 4, v2
	v_lshl_add_u64 v[74:75], v[76:77], 0, v[2:3]
	v_lshl_add_u64 v[76:77], v[74:75], 0, v[40:41]
.LBB0_272:
	s_andn2_saveexec_b64 s[22:23], s[22:23]
	v_lshlrev_b64 v[74:75], 9, v[74:75]
	v_lshl_add_u64 v[76:77], v[56:57], 0, v[74:75]
	s_or_b64 exec, exec, s[22:23]
	s_waitcnt lgkmcnt(7)
	v_cndmask_b32_e64 v2, v140, -v140, vcc
	v_mul_f32_e32 v2, v2, v36
	v_fmac_f32_e32 v2, v137, v32
	s_waitcnt lgkmcnt(6)
	v_cndmask_b32_e64 v32, v139, -v139, vcc
	v_mul_f32_e32 v32, v32, v37
	v_fmac_f32_e32 v32, v135, v33
	s_waitcnt lgkmcnt(5)
	v_cndmask_b32_e64 v33, v138, -v138, vcc
	v_mul_f32_e32 v33, v33, v38
	v_fmac_f32_e32 v33, v133, v34
	s_waitcnt lgkmcnt(4)
	v_cndmask_b32_e64 v34, v136, -v136, vcc
	v_mul_f32_e32 v34, v34, v39
	v_fmac_f32_e32 v34, v131, v35
	s_waitcnt lgkmcnt(3)
	v_cndmask_b32_e64 v35, v134, -v134, vcc
	v_mul_f32_e32 v28, v35, v28
	s_waitcnt vmcnt(3)
	v_and_b32_e32 v39, 0xffff0000, v20
	v_fmac_f32_e32 v28, v129, v24
	v_lshlrev_b32_e32 v38, 16, v20
	v_mul_f32_e32 v20, v39, v39
	v_mul_f32_e32 v24, v91, v28
	s_waitcnt lgkmcnt(2)
	v_cndmask_b32_e64 v28, v132, -v132, vcc
	v_lshlrev_b32_e32 v74, 16, v21
	v_fmac_f32_e32 v20, v38, v38
	v_mul_f32_e32 v28, v28, v29
	v_and_b32_e32 v75, 0xffff0000, v21
	v_fmac_f32_e32 v20, v74, v74
	v_fmac_f32_e32 v28, v128, v25
	v_lshlrev_b32_e32 v128, 16, v22
	v_fmac_f32_e32 v20, v75, v75
	v_and_b32_e32 v137, 0xffff0000, v22
	v_fmac_f32_e32 v20, v128, v128
	v_lshlrev_b32_e32 v138, 16, v23
	v_fmac_f32_e32 v20, v137, v137
	v_and_b32_e32 v139, 0xffff0000, v23
	v_fmac_f32_e32 v20, v138, v138
	v_fmac_f32_e32 v20, v139, v139
	s_nop 1
	v_mov_b32_dpp v21, v20 quad_perm:[1,0,3,2] row_mask:0xf bank_mask:0xf
	v_mul_f32_e32 v2, v91, v2
	v_mul_f32_e32 v32, v91, v32
	v_mov_b32_e32 v36, v3
	v_cvt_pk_fp8_f32 v36, v2, v32
	s_waitcnt lgkmcnt(0)
	v_add_f32_e32 v20, v20, v21
	s_nop 1
	v_mov_b32_dpp v21, v20 quad_perm:[2,3,0,1] row_mask:0xf bank_mask:0xf
	v_mul_f32_e32 v25, v91, v28
	v_mov_b32_e32 v37, v3
	v_cndmask_b32_e64 v28, v130, -v130, vcc
	v_cndmask_b32_e64 v23, v127, -v127, vcc
	s_waitcnt lgkmcnt(0)
	v_add_f32_e32 v2, v20, v21
	s_nop 1
	v_mov_b32_dpp v20, v2 row_shl:4 row_mask:0xf bank_mask:0x5
	v_mov_b32_dpp v20, v2 row_shr:4 row_mask:0xf bank_mask:0xa
	v_cvt_pk_fp8_f32 v37, v24, v25
	v_mul_f32_e32 v28, v28, v30
	v_mul_f32_e32 v23, v23, v31
	v_fmac_f32_e32 v28, v126, v26
	s_waitcnt lgkmcnt(0)
	v_add_f32_e32 v2, v2, v20
	v_fmamk_f32 v2, v2, 0x3c800000, v248
	v_rsq_f32_e32 v2, v2
	v_fmac_f32_e32 v23, v125, v27
	v_mul_f32_e32 v22, v91, v28
	v_mul_f32_e32 v21, v91, v23
	v_mul_f32_e32 v38, v2, v38
	v_mul_f32_e32 v133, v38, v92
	v_mul_f32_e32 v38, v2, v39
	v_mul_f32_e32 v131, v38, v93
	v_mul_f32_e32 v38, v2, v74
	v_cvt_pk_fp8_f32 v37, v22, v21 op_sel:[0,0,1]
	v_and_b32_e32 v20, 63, v72
	v_bfe_u32 v21, v72, 6, 6
	v_mul_f32_e32 v129, v38, v94
	v_mul_f32_e32 v38, v2, v75
	v_cndmask_b32_e64 v20, v20, v21, s[40:41]
	v_mul_f32_e32 v127, v38, v95
	v_mul_f32_e32 v38, v2, v128
	v_mul_f32_e32 v33, v91, v33
	v_mul_f32_e32 v34, v91, v34
	v_lshl_add_u32 v24, v20, 6, v82
	v_mul_f32_e32 v125, v38, v96
	v_mul_f32_e32 v38, v2, v137
	v_cvt_pk_fp8_f32 v36, v33, v34 op_sel:[0,0,1]
	ds_read_b128 v[28:31], v24
	ds_read_b128 v[20:23], v24 offset:16
	ds_read_b128 v[32:35], v24 offset:4096
	ds_read_b128 v[24:27], v24 offset:4112
	v_mul_f32_e32 v75, v38, v97
	v_mul_f32_e32 v38, v2, v138
	v_mul_f32_e32 v2, v2, v139
	v_mul_f32_e32 v39, v38, v98
	v_mul_f32_e32 v38, v2, v99
	ds_bpermute_b32 v136, v80, v133
	ds_bpermute_b32 v135, v80, v131
	ds_bpermute_b32 v134, v80, v129
	ds_bpermute_b32 v132, v80, v127
	ds_bpermute_b32 v130, v80, v125
	ds_bpermute_b32 v128, v80, v75
	ds_bpermute_b32 v126, v80, v39
	ds_bpermute_b32 v74, v80, v38
	global_store_dwordx2 v[76:77], v[36:37], off
	s_and_saveexec_b64 s[22:23], s[44:45]
	s_xor_b64 s[22:23], exec, s[22:23]
	s_cbranch_execz .LBB0_276
	v_alignbit_b32 v36, v73, v72, 11
	v_and_b32_e32 v36, -2, v36
	v_and_b32_e32 v37, 0x3fff, v73
	v_and_b32_e32 v2, 0xfff, v72
	v_lshl_add_u64 v[36:37], v[36:37], 0, v[58:59]
	v_lshlrev_b64 v[36:37], 18, v[36:37]
	v_lshlrev_b32_e32 v2, 6, v2
	v_and_b32_e32 v2, 0x3f000, v2
	v_lshl_add_u64 v[36:37], s[16:17], 0, v[36:37]
	v_lshl_add_u64 v[36:37], v[36:37], 0, v[2:3]
	v_add_u32_e32 v2, s31, v121
	v_and_b32_e32 v2, 0xfc0, v2
	v_lshl_add_u64 v[36:37], v[36:37], 0, v[2:3]
	v_lshrrev_b32_e32 v2, 2, v72
	v_bitop3_b32 v2, v2, v78, 3 bitop3:0x6c
	v_lshlrev_b32_e32 v2, 4, v2
	v_lshl_add_u64 v[36:37], v[36:37], 0, v[2:3]
	v_lshl_add_u64 v[36:37], v[36:37], 0, v[40:41]
.LBB0_276:
	s_andn2_saveexec_b64 s[22:23], s[22:23]
	v_lshlrev_b64 v[36:37], 9, v[72:73]
	v_lshl_add_u64 v[36:37], v[60:61], 0, v[36:37]
	s_or_b64 exec, exec, s[22:23]
	s_waitcnt lgkmcnt(7)
	v_cndmask_b32_e64 v2, v136, -v136, vcc
	v_mul_f32_e32 v2, v2, v32
	v_fmac_f32_e32 v2, v133, v28
	s_waitcnt lgkmcnt(6)
	v_cndmask_b32_e64 v28, v135, -v135, vcc
	v_mul_f32_e32 v28, v28, v33
	v_fmac_f32_e32 v28, v131, v29
	s_waitcnt lgkmcnt(5)
	v_cndmask_b32_e64 v29, v134, -v134, vcc
	v_mul_f32_e32 v29, v29, v34
	v_fmac_f32_e32 v29, v129, v30
	s_waitcnt lgkmcnt(4)
	v_cndmask_b32_e64 v30, v132, -v132, vcc
	v_mul_f32_e32 v30, v30, v35
	v_fmac_f32_e32 v30, v127, v31
	s_waitcnt lgkmcnt(3)
	v_cndmask_b32_e64 v31, v130, -v130, vcc
	v_mul_f32_e32 v24, v31, v24
	s_waitcnt vmcnt(3)
	v_and_b32_e32 v35, 0xffff0000, v16
	v_fmac_f32_e32 v24, v125, v20
	v_lshlrev_b32_e32 v34, 16, v16
	v_mul_f32_e32 v16, v35, v35
	v_mul_f32_e32 v20, v100, v24
	s_waitcnt lgkmcnt(2)
	v_cndmask_b32_e64 v24, v128, -v128, vcc
	v_lshlrev_b32_e32 v72, 16, v17
	v_fmac_f32_e32 v16, v34, v34
	v_mul_f32_e32 v24, v24, v25
	v_and_b32_e32 v73, 0xffff0000, v17
	v_fmac_f32_e32 v16, v72, v72
	v_fmac_f32_e32 v24, v75, v21
	v_lshlrev_b32_e32 v75, 16, v18
	v_fmac_f32_e32 v16, v73, v73
	v_and_b32_e32 v131, 0xffff0000, v18
	v_fmac_f32_e32 v16, v75, v75
	v_lshlrev_b32_e32 v132, 16, v19
	v_fmac_f32_e32 v16, v131, v131
	v_and_b32_e32 v133, 0xffff0000, v19
	v_fmac_f32_e32 v16, v132, v132
	v_fmac_f32_e32 v16, v133, v133
	s_nop 1
	v_mov_b32_dpp v17, v16 quad_perm:[1,0,3,2] row_mask:0xf bank_mask:0xf
	v_mul_f32_e32 v2, v100, v2
	v_mul_f32_e32 v28, v100, v28
	v_mov_b32_e32 v32, v3
	v_cvt_pk_fp8_f32 v32, v2, v28
	s_waitcnt lgkmcnt(0)
	v_add_f32_e32 v16, v16, v17
	s_nop 1
	v_mov_b32_dpp v17, v16 quad_perm:[2,3,0,1] row_mask:0xf bank_mask:0xf
	v_mul_f32_e32 v21, v100, v24
	v_mov_b32_e32 v33, v3
	v_cndmask_b32_e64 v24, v126, -v126, vcc
	v_cndmask_b32_e64 v19, v74, -v74, vcc
	s_waitcnt lgkmcnt(0)
	v_add_f32_e32 v2, v16, v17
	s_nop 1
	v_mov_b32_dpp v16, v2 row_shl:4 row_mask:0xf bank_mask:0x5
	v_mov_b32_dpp v16, v2 row_shr:4 row_mask:0xf bank_mask:0xa
	v_cvt_pk_fp8_f32 v33, v20, v21
	v_mul_f32_e32 v24, v24, v26
	v_mul_f32_e32 v19, v19, v27
	v_fmac_f32_e32 v24, v39, v22
	s_waitcnt lgkmcnt(0)
	v_add_f32_e32 v2, v2, v16
	v_fmamk_f32 v2, v2, 0x3c800000, v248
	v_rsq_f32_e32 v2, v2
	v_fmac_f32_e32 v19, v38, v23
	v_mul_f32_e32 v18, v100, v24
	v_mul_f32_e32 v17, v100, v19
	v_mul_f32_e32 v34, v2, v34
	v_mul_f32_e32 v127, v34, v101
	v_mul_f32_e32 v34, v2, v35
	v_mul_f32_e32 v125, v34, v102
	v_mul_f32_e32 v34, v2, v72
	v_cvt_pk_fp8_f32 v33, v18, v17 op_sel:[0,0,1]
	v_and_b32_e32 v16, 63, v70
	v_bfe_u32 v17, v70, 6, 6
	v_mul_f32_e32 v76, v34, v103
	v_mul_f32_e32 v34, v2, v73
	v_cndmask_b32_e64 v16, v16, v17, s[40:41]
	v_mul_f32_e32 v74, v34, v104
	v_mul_f32_e32 v34, v2, v75
	v_mul_f32_e32 v29, v100, v29
	v_mul_f32_e32 v30, v100, v30
	v_lshl_add_u32 v20, v16, 6, v82
	v_mul_f32_e32 v72, v34, v105
	v_mul_f32_e32 v34, v2, v131
	v_cvt_pk_fp8_f32 v32, v29, v30 op_sel:[0,0,1]
	ds_read_b128 v[24:27], v20
	ds_read_b128 v[16:19], v20 offset:16
	ds_read_b128 v[28:31], v20 offset:4096
	ds_read_b128 v[20:23], v20 offset:4112
	v_mul_f32_e32 v39, v34, v106
	v_mul_f32_e32 v34, v2, v132
	v_mul_f32_e32 v2, v2, v133
	v_mul_f32_e32 v35, v34, v107
	v_mul_f32_e32 v34, v2, v108
	ds_bpermute_b32 v130, v80, v127
	ds_bpermute_b32 v129, v80, v125
	ds_bpermute_b32 v128, v80, v76
	ds_bpermute_b32 v126, v80, v74
	ds_bpermute_b32 v77, v80, v72
	ds_bpermute_b32 v75, v80, v39
	ds_bpermute_b32 v73, v80, v35
	ds_bpermute_b32 v38, v80, v34
	global_store_dwordx2 v[36:37], v[32:33], off
	s_and_saveexec_b64 s[22:23], s[46:47]
	s_xor_b64 s[22:23], exec, s[22:23]
	s_cbranch_execz .LBB0_280
	v_alignbit_b32 v32, v71, v70, 11
	v_and_b32_e32 v32, -2, v32
	v_and_b32_e32 v33, 0x3fff, v71
	v_and_b32_e32 v2, 0xfff, v70
	v_lshl_add_u64 v[32:33], v[32:33], 0, v[62:63]
	v_lshlrev_b64 v[32:33], 18, v[32:33]
	v_lshlrev_b32_e32 v2, 6, v2
	v_and_b32_e32 v2, 0x3f000, v2
	v_lshl_add_u64 v[32:33], s[16:17], 0, v[32:33]
	v_lshl_add_u64 v[32:33], v[32:33], 0, v[2:3]
	v_add_u32_e32 v2, s31, v119
	v_and_b32_e32 v2, 0xfc0, v2
	v_lshl_add_u64 v[32:33], v[32:33], 0, v[2:3]
	v_lshrrev_b32_e32 v2, 2, v70
	v_bitop3_b32 v2, v2, v78, 3 bitop3:0x6c
	v_lshlrev_b32_e32 v2, 4, v2
	v_lshl_add_u64 v[32:33], v[32:33], 0, v[2:3]
	v_lshl_add_u64 v[32:33], v[32:33], 0, v[40:41]
.LBB0_280:
	s_andn2_saveexec_b64 s[22:23], s[22:23]
	v_lshlrev_b64 v[32:33], 9, v[70:71]
	v_lshl_add_u64 v[32:33], v[64:65], 0, v[32:33]
	s_or_b64 exec, exec, s[22:23]
	s_waitcnt lgkmcnt(7)
	v_cndmask_b32_e64 v2, v130, -v130, vcc
	v_mul_f32_e32 v2, v2, v28
	v_fmac_f32_e32 v2, v127, v24
	s_waitcnt lgkmcnt(6)
	v_cndmask_b32_e64 v24, v129, -v129, vcc
	v_mul_f32_e32 v24, v24, v29
	v_fmac_f32_e32 v24, v125, v25
	s_waitcnt lgkmcnt(5)
	v_cndmask_b32_e64 v25, v128, -v128, vcc
	v_mul_f32_e32 v25, v25, v30
	v_fmac_f32_e32 v25, v76, v26
	s_waitcnt lgkmcnt(4)
	v_cndmask_b32_e64 v26, v126, -v126, vcc
	v_mul_f32_e32 v26, v26, v31
	v_fmac_f32_e32 v26, v74, v27
	s_waitcnt lgkmcnt(3)
	v_cndmask_b32_e64 v27, v77, -v77, vcc
	v_mul_f32_e32 v20, v27, v20
	s_waitcnt vmcnt(3)
	v_and_b32_e32 v31, 0xffff0000, v12
	v_fmac_f32_e32 v20, v72, v16
	v_lshlrev_b32_e32 v30, 16, v12
	v_mul_f32_e32 v12, v31, v31
	v_mul_f32_e32 v16, v109, v20
	s_waitcnt lgkmcnt(2)
	v_cndmask_b32_e64 v20, v75, -v75, vcc
	v_lshlrev_b32_e32 v36, 16, v13
	v_fmac_f32_e32 v12, v30, v30
	v_mul_f32_e32 v20, v20, v21
	v_and_b32_e32 v37, 0xffff0000, v13
	v_fmac_f32_e32 v12, v36, v36
	v_fmac_f32_e32 v20, v39, v17
	v_lshlrev_b32_e32 v39, 16, v14
	v_fmac_f32_e32 v12, v37, v37
	v_and_b32_e32 v125, 0xffff0000, v14
	v_fmac_f32_e32 v12, v39, v39
	v_lshlrev_b32_e32 v126, 16, v15
	v_fmac_f32_e32 v12, v125, v125
	v_and_b32_e32 v127, 0xffff0000, v15
	v_fmac_f32_e32 v12, v126, v126
	v_fmac_f32_e32 v12, v127, v127
	s_nop 1
	v_mov_b32_dpp v13, v12 quad_perm:[1,0,3,2] row_mask:0xf bank_mask:0xf
	v_mul_f32_e32 v2, v109, v2
	v_mul_f32_e32 v24, v109, v24
	v_mov_b32_e32 v28, v3
	v_cvt_pk_fp8_f32 v28, v2, v24
	s_waitcnt lgkmcnt(0)
	v_add_f32_e32 v12, v12, v13
	s_nop 1
	v_mov_b32_dpp v13, v12 quad_perm:[2,3,0,1] row_mask:0xf bank_mask:0xf
	v_mul_f32_e32 v17, v109, v20
	v_mov_b32_e32 v29, v3
	v_cndmask_b32_e64 v20, v73, -v73, vcc
	v_cndmask_b32_e64 v15, v38, -v38, vcc
	s_waitcnt lgkmcnt(0)
	v_add_f32_e32 v2, v12, v13
	s_nop 1
	v_mov_b32_dpp v12, v2 row_shl:4 row_mask:0xf bank_mask:0x5
	v_mov_b32_dpp v12, v2 row_shr:4 row_mask:0xf bank_mask:0xa
	v_cvt_pk_fp8_f32 v29, v16, v17
	v_mul_f32_e32 v20, v20, v22
	v_mul_f32_e32 v15, v15, v23
	v_fmac_f32_e32 v20, v35, v18
	s_waitcnt lgkmcnt(0)
	v_add_f32_e32 v2, v2, v12
	v_fmamk_f32 v2, v2, 0x3c800000, v248
	v_rsq_f32_e32 v2, v2
	v_fmac_f32_e32 v15, v34, v19
	v_mul_f32_e32 v14, v109, v20
	v_mul_f32_e32 v13, v109, v15
	v_mul_f32_e32 v30, v2, v30
	v_mul_f32_e32 v74, v30, v110
	v_mul_f32_e32 v30, v2, v31
	s_and_b32 s19, s20, 63
	s_bfe_u32 s22, s20, 0x60006
	v_mul_f32_e32 v72, v30, v111
	v_mul_f32_e32 v30, v2, v36
	v_cvt_pk_fp8_f32 v29, v14, v13 op_sel:[0,0,1]
	v_mov_b32_e32 v12, s19
	v_mov_b32_e32 v13, s22
	v_mul_f32_e32 v70, v30, v112
	v_mul_f32_e32 v30, v2, v37
	v_cndmask_b32_e64 v12, v12, v13, s[40:41]
	v_mul_f32_e32 v38, v30, v113
	v_mul_f32_e32 v30, v2, v39
	v_mul_f32_e32 v25, v109, v25
	v_mul_f32_e32 v26, v109, v26
	v_lshl_add_u32 v16, v12, 6, v82
	v_mul_f32_e32 v36, v30, v114
	v_mul_f32_e32 v30, v2, v125
	v_cvt_pk_fp8_f32 v28, v25, v26 op_sel:[0,0,1]
	ds_read_b128 v[20:23], v16
	ds_read_b128 v[12:15], v16 offset:16
	ds_read_b128 v[24:27], v16 offset:4096
	ds_read_b128 v[16:19], v16 offset:4112
	v_mul_f32_e32 v34, v30, v115
	v_mul_f32_e32 v30, v2, v126
	v_mul_f32_e32 v2, v2, v127
	v_mul_f32_e32 v31, v30, v116
	v_mul_f32_e32 v30, v2, v117
	ds_bpermute_b32 v77, v80, v74
	ds_bpermute_b32 v76, v80, v72
	ds_bpermute_b32 v75, v80, v70
	ds_bpermute_b32 v73, v80, v38
	ds_bpermute_b32 v71, v80, v36
	ds_bpermute_b32 v39, v80, v34
	ds_bpermute_b32 v37, v80, v31
	ds_bpermute_b32 v35, v80, v30
	global_store_dwordx2 v[32:33], v[28:29], off
	s_and_saveexec_b64 s[22:23], s[48:49]
	s_xor_b64 s[22:23], exec, s[22:23]
	s_cbranch_execz .LBB0_284
	s_lshr_b64 s[50:51], s[20:21], 11
	s_and_b32 s19, s20, 0xfff
	s_and_b32 s51, s21, 0x3fff
	s_and_b32 s50, s50, -2
	v_lshl_add_u64 v[28:29], s[50:51], 0, v[66:67]
	s_lshl_b32 s19, s19, 6
	v_lshlrev_b64 v[28:29], 18, v[28:29]
	s_and_b32 s34, s19, 0x3f000
	s_mul_i32 s19, s33, 0x600
	v_lshl_add_u64 v[28:29], s[16:17], 0, v[28:29]
	s_add_i32 s19, s19, s31
	v_lshl_add_u64 v[28:29], v[28:29], 0, s[34:35]
	s_and_b32 s34, s19, 0xfc0
	s_lshr_b32 s19, s20, 2
	v_bitop3_b32 v2, s19, v78, 3 bitop3:0x6c
	v_lshl_add_u64 v[28:29], v[28:29], 0, s[34:35]
	v_lshlrev_b32_e32 v2, 4, v2
	v_lshl_add_u64 v[28:29], v[28:29], 0, v[2:3]
	v_readlane_b32 s34, v254, 43
	s_mul_i32 s27, s33, 24
	v_lshl_add_u64 v[28:29], v[28:29], 0, v[40:41]

.LBB0_741:
	s_and_saveexec_b64 s[10:11], s[40:41]
	ds_write_b32 v144, v3
	s_or_b64 exec, exec, s[10:11]
	s_ashr_i32 s55, s54, 31
	s_add_u32 s10, s54, s12
	s_addc_u32 s11, s55, s13
	s_lshl_b64 s[10:11], s[10:11], 11
	v_lshl_add_u64 v[12:13], v[126:127], 0, s[10:11]
	s_waitcnt vmcnt(0) lgkmcnt(0)
	s_barrier
	global_load_dwordx4 v[4:7], v[12:13], off offset:1024
	global_load_dwordx4 v[8:11], v[12:13], off
	global_load_dwordx4 v[112:115], v[12:13], off offset:2048
	global_load_dwordx4 v[116:119], v[12:13], off offset:3072
	s_movk_i32 s3, 0x1000
	v_add_co_u32_e64 v120, s[46:47], s93, v12
	v_add_co_u32_e32 v14, vcc, s3, v12
	s_nop 0
	v_addc_co_u32_e64 v121, s[46:47], 0, v13, s[46:47]
	s_movk_i32 s3, 0x4000
	v_add_co_u32_e64 v16, s[46:47], s3, v12
	s_movk_i32 s3, 0x6000
	s_nop 0
	v_addc_co_u32_e64 v17, s[46:47], 0, v13, s[46:47]
	v_add_co_u32_e64 v20, s[46:47], s3, v12
	v_addc_co_u32_e32 v15, vcc, 0, v13, vcc
	s_nop 0
	v_addc_co_u32_e64 v21, s[46:47], 0, v13, s[46:47]
	global_load_dwordx4 v[92:95], v[120:121], off
	global_load_dwordx4 v[96:99], v[120:121], off offset:1024
	global_load_dwordx4 v[80:83], v[120:121], off offset:2048
	global_load_dwordx4 v[84:87], v[120:121], off offset:3072
	global_load_dwordx4 v[76:79], v[16:17], off offset:-4096
	global_load_dwordx4 v[60:63], v[16:17], off
	global_load_dwordx4 v[64:67], v[16:17], off offset:1024
	global_load_dwordx4 v[48:51], v[16:17], off offset:2048
	global_load_dwordx4 v[56:59], v[16:17], off offset:3072
	global_load_dwordx4 v[40:43], v[20:21], off offset:-4096
	global_load_dwordx4 v[28:31], v[20:21], off
	global_load_dwordx4 v[32:35], v[20:21], off offset:1024
	s_nop 0
	global_load_dwordx4 v[16:19], v[20:21], off offset:2048
	global_load_dwordx4 v[24:27], v[20:21], off offset:3072
	global_load_dwordx4 v[108:111], v[14:15], off offset:1024
	global_load_dwordx4 v[100:103], v[14:15], off offset:2048
	s_movk_i32 s3, 0x3000
	v_add_co_u32_e32 v22, vcc, s3, v12
	s_movk_i32 s3, 0x7000
	s_nop 0
	v_addc_co_u32_e32 v23, vcc, 0, v13, vcc
	global_load_dwordx4 v[104:107], v[14:15], off offset:3072
	global_load_dwordx4 v[88:91], v[22:23], off offset:1024
	global_load_dwordx4 v[68:71], v[22:23], off offset:2048
	global_load_dwordx4 v[72:75], v[22:23], off offset:3072
	s_waitcnt vmcnt(23)
	v_lshlrev_b32_e32 v2, 16, v4
	s_waitcnt vmcnt(22)
	v_lshlrev_b32_e32 v173, 16, v9
	v_lshlrev_b32_e32 v172, 16, v8
	v_and_b32_e32 v175, 0xffff0000, v9
	v_and_b32_e32 v174, 0xffff0000, v8
	v_lshlrev_b32_e32 v177, 16, v11
	v_lshlrev_b32_e32 v176, 16, v10
	v_and_b32_e32 v179, 0xffff0000, v11
	v_and_b32_e32 v178, 0xffff0000, v10
	v_and_b32_e32 v171, 0xffff0000, v4
	v_lshlrev_b32_e32 v180, 16, v5
	v_and_b32_e32 v181, 0xffff0000, v5
	v_lshlrev_b32_e32 v141, 16, v6
	v_and_b32_e32 v182, 0xffff0000, v6
	v_lshlrev_b32_e32 v139, 16, v7
	v_and_b32_e32 v143, 0xffff0000, v7
	v_pk_add_f32 v[4:5], v[172:173], v[174:175]
	v_pk_add_f32 v[6:7], v[176:177], v[178:179]
	v_add_f32_e32 v1, v4, v5
	v_pk_add_f32 v[4:5], v[6:7], v[6:7] op_sel:[0,1] op_sel_hi:[1,0]
	v_add_f32_e32 v138, v2, v171
	v_add_f32_e32 v142, v180, v181
	v_add_f32_e32 v140, 0, v1
	v_mov_b32_e32 v5, v182
	v_pk_add_f32 v[6:7], v[138:139], v[142:143]
	v_pk_add_f32 v[4:5], v[140:141], v[4:5]
	s_nop 0
	v_pk_add_f32 v[4:5], v[4:5], v[6:7]
	s_nop 0
	v_add_f32_e32 v1, v4, v5
	s_nop 1
	v_mov_b32_dpp v5, v1 quad_perm:[1,0,3,2] row_mask:0xf bank_mask:0xf
	v_add_co_u32_e32 v4, vcc, s18, v12
	s_waitcnt lgkmcnt(0)
	v_add_f32_e32 v1, v1, v5
	s_nop 1
	v_mov_b32_dpp v6, v1 quad_perm:[2,3,0,1] row_mask:0xf bank_mask:0xf
	v_addc_co_u32_e32 v5, vcc, 0, v13, vcc
	v_add_co_u32_e32 v8, vcc, s3, v12
	s_waitcnt lgkmcnt(0)
	v_add_f32_e32 v1, v1, v6
	s_nop 1
	v_mov_b32_dpp v6, v1 row_shl:4 row_mask:0xf bank_mask:0x5
	v_mov_b32_dpp v6, v1 row_shr:4 row_mask:0xf bank_mask:0xa
	v_addc_co_u32_e32 v9, vcc, 0, v13, vcc
	global_load_dwordx4 v[52:55], v[4:5], off offset:1024
	global_load_dwordx4 v[36:39], v[4:5], off offset:2048
	global_load_dwordx4 v[44:47], v[4:5], off offset:3072
	global_load_dwordx4 v[12:15], v[8:9], off
	s_waitcnt lgkmcnt(0)
	v_add_f32_e32 v1, v1, v6
	s_nop 1
	v_mov_b32_dpp v6, v1 row_shl:8 row_mask:0xf bank_mask:0x3
	v_mov_b32_dpp v6, v1 row_shr:8 row_mask:0xf bank_mask:0xc
	s_waitcnt lgkmcnt(0)
	v_add_f32_e32 v1, v1, v6
	global_load_dwordx4 v[20:23], v[8:9], off offset:1024
	global_load_dwordx4 v[4:7], v[8:9], off offset:2048
	s_nop 0
	global_load_dwordx4 v[120:123], v[120:121], off offset:-4096
	s_nop 0
	global_load_dwordx4 v[8:11], v[8:9], off offset:3072
	v_mov_b32_e32 v138, v1
	s_nop 1
	v_permlane16_swap_b32_e32 v138, v1
	s_waitcnt lgkmcnt(0)
	v_add_f32_e32 v1, v1, v138
	v_mov_b32_e32 v138, v1
	s_nop 1
	v_permlane32_swap_b32_e32 v138, v1
	s_waitcnt lgkmcnt(0)
	v_add_f32_e32 v1, v1, v138
	v_fmac_f32_e32 v175, 0xba800000, v1
	v_fmac_f32_e32 v174, 0xba800000, v1
	v_fmac_f32_e32 v179, 0xba800000, v1
	v_fmac_f32_e32 v178, 0xba800000, v1
	v_fmac_f32_e32 v173, 0xba800000, v1
	v_fmac_f32_e32 v172, 0xba800000, v1
	v_fmac_f32_e32 v177, 0xba800000, v1
	v_fmac_f32_e32 v176, 0xba800000, v1
	v_mul_f32_e32 v138, v174, v174
	v_mul_f32_e32 v140, v175, v175
	v_mul_f32_e32 v142, v178, v178
	v_mul_f32_e32 v174, v179, v179
	v_fmac_f32_e32 v138, v172, v172
	v_fmac_f32_e32 v140, v173, v173
	v_fmac_f32_e32 v142, v176, v176
	v_fmac_f32_e32 v174, v177, v177
	v_add_f32_e32 v138, v138, v140
	v_add_f32_e32 v140, v142, v174
	v_fmac_f32_e32 v171, 0xba800000, v1
	v_fmac_f32_e32 v181, 0xba800000, v1
	v_add_f32_e32 v138, v138, v140
	v_fmac_f32_e32 v2, 0xba800000, v1
	v_mul_f32_e32 v140, v171, v171
	v_fmac_f32_e32 v180, 0xba800000, v1
	v_fmac_f32_e32 v140, v2, v2
	v_mul_f32_e32 v2, v181, v181
	v_fmac_f32_e32 v2, v180, v180
	v_add_f32_e32 v2, v140, v2
	v_fmac_f32_e32 v143, 0xba800000, v1
	v_fmac_f32_e32 v182, 0xba800000, v1
	v_add_f32_e32 v2, v138, v2
	v_fmac_f32_e32 v139, 0xba800000, v1
	v_fmac_f32_e32 v141, 0xba800000, v1
	v_mul_f32_e32 v138, v182, v182
	v_mul_f32_e32 v140, v143, v143
	v_fmac_f32_e32 v138, v141, v141
	v_fmac_f32_e32 v140, v139, v139
	v_add_f32_e32 v138, v138, v140
	v_add_f32_e32 v2, v2, v138
	s_nop 1
	v_mov_b32_dpp v138, v2 quad_perm:[1,0,3,2] row_mask:0xf bank_mask:0xf
	s_waitcnt lgkmcnt(0)
	v_add_f32_e32 v2, v2, v138
	s_nop 1
	v_mov_b32_dpp v138, v2 quad_perm:[2,3,0,1] row_mask:0xf bank_mask:0xf
	s_waitcnt lgkmcnt(0)
	v_add_f32_e32 v2, v2, v138
	s_nop 1
	v_mov_b32_dpp v138, v2 row_shl:4 row_mask:0xf bank_mask:0x5
	v_mov_b32_dpp v138, v2 row_shr:4 row_mask:0xf bank_mask:0xa
	s_waitcnt lgkmcnt(0)
	v_add_f32_e32 v2, v2, v138
	s_nop 1
	v_mov_b32_dpp v138, v2 row_shl:8 row_mask:0xf bank_mask:0x3
	v_mov_b32_dpp v138, v2 row_shr:8 row_mask:0xf bank_mask:0xc
	s_waitcnt lgkmcnt(0)
	v_add_f32_e32 v2, v2, v138
	v_mov_b32_e32 v138, v2
	s_nop 1
	v_permlane16_swap_b32_e32 v138, v2
	s_waitcnt lgkmcnt(0)
	v_add_f32_e32 v2, v2, v138
	ds_bpermute_b32 v138, v151, v2
	s_and_saveexec_b64 s[10:11], s[42:43]
	s_cbranch_execz .LBB0_745
	v_mul_f32_e32 v140, 0x3a800000, v1
	s_waitcnt lgkmcnt(0)
	v_add_f32_e32 v1, v2, v138
	v_fmamk_f32 v1, v1, 0x3a800000, v241
	v_rsq_f32_e32 v141, v1
	s_add_i32 s3, s14, 0
	s_add_i32 s3, s3, 0x23800
	v_mov_b32_e32 v1, s3
	ds_write_b64 v1, v[140:141]
.LBB0_745:
	s_or_b64 exec, exec, s[10:11]
	s_waitcnt vmcnt(29)
	v_lshlrev_b32_e32 v141, 16, v113
	v_lshlrev_b32_e32 v140, 16, v112
	v_and_b32_e32 v113, 0xffff0000, v113
	v_and_b32_e32 v112, 0xffff0000, v112
	v_pk_add_f32 v[142:143], v[140:141], v[112:113]
	s_waitcnt vmcnt(28)
	v_lshlrev_b32_e32 v2, 16, v116
	v_add_f32_e32 v1, v142, v143
	v_lshlrev_b32_e32 v143, 16, v115
	v_lshlrev_b32_e32 v142, 16, v114
	v_and_b32_e32 v115, 0xffff0000, v115
	v_and_b32_e32 v114, 0xffff0000, v114
	v_pk_add_f32 v[172:173], v[142:143], v[114:115]
	v_and_b32_e32 v171, 0xffff0000, v116
	v_lshlrev_b32_e32 v176, 16, v117
	v_and_b32_e32 v177, 0xffff0000, v117
	v_and_b32_e32 v178, 0xffff0000, v118
	v_pk_add_f32 v[172:173], v[172:173], v[172:173] op_sel:[0,1] op_sel_hi:[1,0]
	v_lshlrev_b32_e32 v117, 16, v118
	v_lshlrev_b32_e32 v139, 16, v119
	v_and_b32_e32 v119, 0xffff0000, v119
	v_add_f32_e32 v116, 0, v1
	s_waitcnt lgkmcnt(0)
	v_add_f32_e32 v138, v2, v171
	v_add_f32_e32 v118, v176, v177
	v_mov_b32_e32 v173, v178
	v_pk_add_f32 v[172:173], v[116:117], v[172:173]
	v_pk_add_f32 v[174:175], v[138:139], v[118:119]
	s_nop 0
	v_pk_add_f32 v[172:173], v[172:173], v[174:175]
	s_nop 0
	v_add_f32_e32 v1, v172, v173
	s_nop 1
	v_mov_b32_dpp v116, v1 quad_perm:[1,0,3,2] row_mask:0xf bank_mask:0xf
	s_waitcnt lgkmcnt(0)
	v_add_f32_e32 v1, v1, v116
	s_nop 1
	v_mov_b32_dpp v116, v1 quad_perm:[2,3,0,1] row_mask:0xf bank_mask:0xf
	s_waitcnt lgkmcnt(0)
	v_add_f32_e32 v1, v1, v116
	s_nop 1
	v_mov_b32_dpp v116, v1 row_shl:4 row_mask:0xf bank_mask:0x5
	v_mov_b32_dpp v116, v1 row_shr:4 row_mask:0xf bank_mask:0xa
	s_waitcnt lgkmcnt(0)
	v_add_f32_e32 v1, v1, v116
	s_nop 1
	v_mov_b32_dpp v116, v1 row_shl:8 row_mask:0xf bank_mask:0x3
	v_mov_b32_dpp v116, v1 row_shr:8 row_mask:0xf bank_mask:0xc
	s_waitcnt lgkmcnt(0)
	v_add_f32_e32 v1, v1, v116
	v_mov_b32_e32 v116, v1
	s_nop 1
	v_permlane16_swap_b32_e32 v116, v1
	s_waitcnt lgkmcnt(0)
	v_add_f32_e32 v1, v1, v116
	v_mov_b32_e32 v116, v1
	s_nop 1
	v_permlane32_swap_b32_e32 v116, v1
	s_waitcnt lgkmcnt(0)
	v_add_f32_e32 v1, v1, v116
	v_fmac_f32_e32 v113, 0xba800000, v1
	v_fmac_f32_e32 v112, 0xba800000, v1
	v_fmac_f32_e32 v141, 0xba800000, v1
	v_fmac_f32_e32 v140, 0xba800000, v1
	v_mul_f32_e32 v112, v112, v112
	v_mul_f32_e32 v113, v113, v113
	v_fmac_f32_e32 v112, v140, v140
	v_fmac_f32_e32 v113, v141, v141
	v_fmac_f32_e32 v115, 0xba800000, v1
	v_fmac_f32_e32 v114, 0xba800000, v1
	v_add_f32_e32 v112, v112, v113
	v_fmac_f32_e32 v143, 0xba800000, v1
	v_fmac_f32_e32 v142, 0xba800000, v1
	v_mul_f32_e32 v113, v114, v114
	v_mul_f32_e32 v114, v115, v115
	v_fmac_f32_e32 v113, v142, v142
	v_fmac_f32_e32 v114, v143, v143
	v_add_f32_e32 v113, v113, v114
	v_fmac_f32_e32 v171, 0xba800000, v1
	v_add_f32_e32 v112, v112, v113
	v_fmac_f32_e32 v177, 0xba800000, v1
	v_fmac_f32_e32 v2, 0xba800000, v1
	v_mul_f32_e32 v113, v171, v171
	v_fmac_f32_e32 v176, 0xba800000, v1
	v_fmac_f32_e32 v113, v2, v2
	v_mul_f32_e32 v2, v177, v177
	v_fmac_f32_e32 v2, v176, v176
	v_add_f32_e32 v2, v113, v2
	v_fmac_f32_e32 v119, 0xba800000, v1
	v_fmac_f32_e32 v178, 0xba800000, v1
	v_add_f32_e32 v2, v112, v2
	v_fmac_f32_e32 v139, 0xba800000, v1
	v_fmac_f32_e32 v117, 0xba800000, v1
	v_mul_f32_e32 v112, v178, v178
	v_mul_f32_e32 v113, v119, v119
	v_fmac_f32_e32 v112, v117, v117
	v_fmac_f32_e32 v113, v139, v139
	v_add_f32_e32 v112, v112, v113
	v_add_f32_e32 v2, v2, v112
	s_nop 1
	v_mov_b32_dpp v112, v2 quad_perm:[1,0,3,2] row_mask:0xf bank_mask:0xf
	s_waitcnt lgkmcnt(0)
	v_add_f32_e32 v2, v2, v112
	s_nop 1
	v_mov_b32_dpp v112, v2 quad_perm:[2,3,0,1] row_mask:0xf bank_mask:0xf
	s_waitcnt lgkmcnt(0)
	v_add_f32_e32 v2, v2, v112
	s_nop 1
	v_mov_b32_dpp v112, v2 row_shl:4 row_mask:0xf bank_mask:0x5
	v_mov_b32_dpp v112, v2 row_shr:4 row_mask:0xf bank_mask:0xa
	s_waitcnt lgkmcnt(0)
	v_add_f32_e32 v2, v2, v112
	s_nop 1
	v_mov_b32_dpp v112, v2 row_shl:8 row_mask:0xf bank_mask:0x3
	v_mov_b32_dpp v112, v2 row_shr:8 row_mask:0xf bank_mask:0xc
	s_waitcnt lgkmcnt(0)
	v_add_f32_e32 v2, v2, v112
	v_mov_b32_e32 v112, v2
	s_nop 1
	v_permlane16_swap_b32_e32 v112, v2
	s_waitcnt lgkmcnt(0)
	v_add_f32_e32 v2, v2, v112
	ds_bpermute_b32 v112, v151, v2
	s_and_saveexec_b64 s[10:11], s[42:43]
	s_cbranch_execz .LBB0_747
	v_mul_f32_e32 v114, 0x3a800000, v1
	s_waitcnt lgkmcnt(0)
	v_add_f32_e32 v1, v2, v112
	v_fmamk_f32 v1, v1, 0x3a800000, v241
	v_rsq_f32_e32 v115, v1
	s_add_i32 s3, s14, 0
	s_add_i32 s3, s3, 0x23808
	v_mov_b32_e32 v1, s3
	ds_write_b64 v1, v[114:115]
.LBB0_747:
	s_or_b64 exec, exec, s[10:11]
	s_waitcnt vmcnt(1)
	v_lshlrev_b32_e32 v115, 16, v121
	v_lshlrev_b32_e32 v114, 16, v120
	v_and_b32_e32 v117, 0xffff0000, v121
	v_and_b32_e32 v116, 0xffff0000, v120
	v_pk_add_f32 v[118:119], v[114:115], v[116:117]
	v_and_b32_e32 v121, 0xffff0000, v123
	v_add_f32_e32 v1, v118, v119
	v_lshlrev_b32_e32 v119, 16, v123
	v_lshlrev_b32_e32 v118, 16, v122
	v_and_b32_e32 v120, 0xffff0000, v122
	v_pk_add_f32 v[122:123], v[118:119], v[120:121]
	v_lshlrev_b32_e32 v2, 16, v108
	v_and_b32_e32 v140, 0xffff0000, v108
	v_lshlrev_b32_e32 v141, 16, v109
	v_and_b32_e32 v142, 0xffff0000, v109
	v_and_b32_e32 v143, 0xffff0000, v110
	v_pk_add_f32 v[122:123], v[122:123], v[122:123] op_sel:[0,1] op_sel_hi:[1,0]
	v_lshlrev_b32_e32 v109, 16, v110
	v_lshlrev_b32_e32 v113, 16, v111
	v_and_b32_e32 v111, 0xffff0000, v111
	v_add_f32_e32 v108, 0, v1
	s_waitcnt lgkmcnt(0)
	v_add_f32_e32 v112, v2, v140
	v_add_f32_e32 v110, v141, v142
	v_mov_b32_e32 v123, v143
	v_pk_add_f32 v[122:123], v[108:109], v[122:123]
	v_pk_add_f32 v[138:139], v[112:113], v[110:111]
	s_nop 0
	v_pk_add_f32 v[122:123], v[122:123], v[138:139]
	s_nop 0
	v_add_f32_e32 v1, v122, v123
	s_nop 1
	v_mov_b32_dpp v108, v1 quad_perm:[1,0,3,2] row_mask:0xf bank_mask:0xf
	s_waitcnt lgkmcnt(0)
	v_add_f32_e32 v1, v1, v108
	s_nop 1
	v_mov_b32_dpp v108, v1 quad_perm:[2,3,0,1] row_mask:0xf bank_mask:0xf
	s_waitcnt lgkmcnt(0)
	v_add_f32_e32 v1, v1, v108
	s_nop 1
	v_mov_b32_dpp v108, v1 row_shl:4 row_mask:0xf bank_mask:0x5
	v_mov_b32_dpp v108, v1 row_shr:4 row_mask:0xf bank_mask:0xa
	s_waitcnt lgkmcnt(0)
	v_add_f32_e32 v1, v1, v108
	s_nop 1
	v_mov_b32_dpp v108, v1 row_shl:8 row_mask:0xf bank_mask:0x3
	v_mov_b32_dpp v108, v1 row_shr:8 row_mask:0xf bank_mask:0xc
	s_waitcnt lgkmcnt(0)
	v_add_f32_e32 v1, v1, v108
	v_mov_b32_e32 v108, v1
	s_nop 1
	v_permlane16_swap_b32_e32 v108, v1
	s_waitcnt lgkmcnt(0)
	v_add_f32_e32 v1, v1, v108
	v_mov_b32_e32 v108, v1
	s_nop 1
	v_permlane32_swap_b32_e32 v108, v1
	s_waitcnt lgkmcnt(0)
	v_add_f32_e32 v1, v1, v108
	v_fmac_f32_e32 v117, 0xba800000, v1
	v_fmac_f32_e32 v116, 0xba800000, v1
	v_fmac_f32_e32 v115, 0xba800000, v1
	v_fmac_f32_e32 v114, 0xba800000, v1
	v_mul_f32_e32 v108, v116, v116
	v_mul_f32_e32 v110, v117, v117
	v_fmac_f32_e32 v108, v114, v114
	v_fmac_f32_e32 v110, v115, v115
	v_fmac_f32_e32 v121, 0xba800000, v1
	v_fmac_f32_e32 v120, 0xba800000, v1
	v_add_f32_e32 v108, v108, v110
	v_fmac_f32_e32 v119, 0xba800000, v1
	v_fmac_f32_e32 v118, 0xba800000, v1
	v_mul_f32_e32 v110, v120, v120
	v_mul_f32_e32 v112, v121, v121
	v_fmac_f32_e32 v110, v118, v118
	v_fmac_f32_e32 v112, v119, v119
	v_add_f32_e32 v110, v110, v112
	v_fmac_f32_e32 v140, 0xba800000, v1
	v_add_f32_e32 v108, v108, v110
	v_fmac_f32_e32 v142, 0xba800000, v1
	v_fmac_f32_e32 v2, 0xba800000, v1
	v_mul_f32_e32 v110, v140, v140
	v_fmac_f32_e32 v141, 0xba800000, v1
	v_fmac_f32_e32 v110, v2, v2
	v_mul_f32_e32 v2, v142, v142
	v_fmac_f32_e32 v2, v141, v141
	v_add_f32_e32 v2, v110, v2
	v_fmac_f32_e32 v143, 0xba800000, v1
	v_add_f32_e32 v2, v108, v2
	v_fmac_f32_e32 v111, 0xba800000, v1
	v_fmac_f32_e32 v109, 0xba800000, v1
	v_mul_f32_e32 v108, v143, v143
	v_fmac_f32_e32 v113, 0xba800000, v1
	v_fmac_f32_e32 v108, v109, v109
	v_mul_f32_e32 v109, v111, v111
	v_fmac_f32_e32 v109, v113, v113
	v_add_f32_e32 v108, v108, v109
	v_add_f32_e32 v2, v2, v108
	s_nop 1
	v_mov_b32_dpp v108, v2 quad_perm:[1,0,3,2] row_mask:0xf bank_mask:0xf
	s_waitcnt lgkmcnt(0)
	v_add_f32_e32 v2, v2, v108
	s_nop 1
	v_mov_b32_dpp v108, v2 quad_perm:[2,3,0,1] row_mask:0xf bank_mask:0xf
	s_waitcnt lgkmcnt(0)
	v_add_f32_e32 v2, v2, v108
	s_nop 1
	v_mov_b32_dpp v108, v2 row_shl:4 row_mask:0xf bank_mask:0x5
	v_mov_b32_dpp v108, v2 row_shr:4 row_mask:0xf bank_mask:0xa
	s_waitcnt lgkmcnt(0)
	v_add_f32_e32 v2, v2, v108
	s_nop 1
	v_mov_b32_dpp v108, v2 row_shl:8 row_mask:0xf bank_mask:0x3
	v_mov_b32_dpp v108, v2 row_shr:8 row_mask:0xf bank_mask:0xc
	s_waitcnt lgkmcnt(0)
	v_add_f32_e32 v2, v2, v108
	v_mov_b32_e32 v108, v2
	s_nop 1
	v_permlane16_swap_b32_e32 v108, v2
	s_waitcnt lgkmcnt(0)
	v_add_f32_e32 v2, v2, v108
	ds_bpermute_b32 v108, v151, v2
	s_and_saveexec_b64 s[10:11], s[42:43]
	s_cbranch_execz .LBB0_749
	v_mul_f32_e32 v110, 0x3a800000, v1
	s_waitcnt lgkmcnt(0)
	v_add_f32_e32 v1, v2, v108
	v_fmamk_f32 v1, v1, 0x3a800000, v241
	v_rsq_f32_e32 v111, v1
	s_add_i32 s3, s14, 0
	s_add_i32 s3, s3, 0x23810
	v_mov_b32_e32 v1, s3
	ds_write_b64 v1, v[110:111]
.LBB0_749:
	s_or_b64 exec, exec, s[10:11]
	v_lshlrev_b32_e32 v111, 16, v101
	v_lshlrev_b32_e32 v110, 16, v100
	v_and_b32_e32 v101, 0xffff0000, v101
	v_and_b32_e32 v100, 0xffff0000, v100
	v_pk_add_f32 v[112:113], v[110:111], v[100:101]
	v_lshlrev_b32_e32 v2, 16, v104
	v_add_f32_e32 v1, v112, v113
	v_lshlrev_b32_e32 v113, 16, v103
	v_lshlrev_b32_e32 v112, 16, v102
	v_and_b32_e32 v103, 0xffff0000, v103
	v_and_b32_e32 v102, 0xffff0000, v102
	v_pk_add_f32 v[114:115], v[112:113], v[102:103]
	v_and_b32_e32 v118, 0xffff0000, v104
	v_lshlrev_b32_e32 v119, 16, v105
	v_and_b32_e32 v120, 0xffff0000, v105
	v_and_b32_e32 v121, 0xffff0000, v106
	v_pk_add_f32 v[114:115], v[114:115], v[114:115] op_sel:[0,1] op_sel_hi:[1,0]
	v_lshlrev_b32_e32 v105, 16, v106
	v_lshlrev_b32_e32 v109, 16, v107
	v_and_b32_e32 v107, 0xffff0000, v107
	v_add_f32_e32 v104, 0, v1
	s_waitcnt lgkmcnt(0)
	v_add_f32_e32 v108, v2, v118
	v_add_f32_e32 v106, v119, v120
	v_mov_b32_e32 v115, v121
	v_pk_add_f32 v[114:115], v[104:105], v[114:115]
	v_pk_add_f32 v[116:117], v[108:109], v[106:107]
	s_nop 0
	v_pk_add_f32 v[114:115], v[114:115], v[116:117]
	s_nop 0
	v_add_f32_e32 v1, v114, v115
	s_nop 1
	v_mov_b32_dpp v104, v1 quad_perm:[1,0,3,2] row_mask:0xf bank_mask:0xf
	s_waitcnt lgkmcnt(0)
	v_add_f32_e32 v1, v1, v104
	s_nop 1
	v_mov_b32_dpp v104, v1 quad_perm:[2,3,0,1] row_mask:0xf bank_mask:0xf
	s_waitcnt lgkmcnt(0)
	v_add_f32_e32 v1, v1, v104
	s_nop 1
	v_mov_b32_dpp v104, v1 row_shl:4 row_mask:0xf bank_mask:0x5
	v_mov_b32_dpp v104, v1 row_shr:4 row_mask:0xf bank_mask:0xa
	s_waitcnt lgkmcnt(0)
	v_add_f32_e32 v1, v1, v104
	s_nop 1
	v_mov_b32_dpp v104, v1 row_shl:8 row_mask:0xf bank_mask:0x3
	v_mov_b32_dpp v104, v1 row_shr:8 row_mask:0xf bank_mask:0xc
	s_waitcnt lgkmcnt(0)
	v_add_f32_e32 v1, v1, v104
	v_mov_b32_e32 v104, v1
	s_nop 1
	v_permlane16_swap_b32_e32 v104, v1
	s_waitcnt lgkmcnt(0)
	v_add_f32_e32 v1, v1, v104
	v_mov_b32_e32 v104, v1
	s_nop 1
	v_permlane32_swap_b32_e32 v104, v1
	s_waitcnt lgkmcnt(0)
	v_add_f32_e32 v1, v1, v104
	v_fmac_f32_e32 v101, 0xba800000, v1
	v_fmac_f32_e32 v100, 0xba800000, v1
	v_fmac_f32_e32 v111, 0xba800000, v1
	v_fmac_f32_e32 v110, 0xba800000, v1
	v_mul_f32_e32 v100, v100, v100
	v_mul_f32_e32 v101, v101, v101
	v_fmac_f32_e32 v100, v110, v110
	v_fmac_f32_e32 v101, v111, v111
	v_fmac_f32_e32 v103, 0xba800000, v1
	v_fmac_f32_e32 v102, 0xba800000, v1
	v_add_f32_e32 v100, v100, v101
	v_fmac_f32_e32 v113, 0xba800000, v1
	v_fmac_f32_e32 v112, 0xba800000, v1
	v_mul_f32_e32 v101, v102, v102
	v_mul_f32_e32 v102, v103, v103
	v_fmac_f32_e32 v101, v112, v112
	v_fmac_f32_e32 v102, v113, v113
	v_add_f32_e32 v101, v101, v102
	v_fmac_f32_e32 v118, 0xba800000, v1
	v_add_f32_e32 v100, v100, v101
	v_fmac_f32_e32 v120, 0xba800000, v1
	v_fmac_f32_e32 v2, 0xba800000, v1
	v_mul_f32_e32 v101, v118, v118
	v_fmac_f32_e32 v119, 0xba800000, v1
	v_fmac_f32_e32 v101, v2, v2
	v_mul_f32_e32 v2, v120, v120
	v_fmac_f32_e32 v2, v119, v119
	v_add_f32_e32 v2, v101, v2
	v_fmac_f32_e32 v107, 0xba800000, v1
	v_fmac_f32_e32 v121, 0xba800000, v1
	v_add_f32_e32 v2, v100, v2
	v_fmac_f32_e32 v109, 0xba800000, v1
	v_fmac_f32_e32 v105, 0xba800000, v1
	v_mul_f32_e32 v100, v121, v121
	v_mul_f32_e32 v101, v107, v107
	v_fmac_f32_e32 v100, v105, v105
	v_fmac_f32_e32 v101, v109, v109
	v_add_f32_e32 v100, v100, v101
	v_add_f32_e32 v2, v2, v100
	s_nop 1
	v_mov_b32_dpp v100, v2 quad_perm:[1,0,3,2] row_mask:0xf bank_mask:0xf
	s_waitcnt lgkmcnt(0)
	v_add_f32_e32 v2, v2, v100
	s_nop 1
	v_mov_b32_dpp v100, v2 quad_perm:[2,3,0,1] row_mask:0xf bank_mask:0xf
	s_waitcnt lgkmcnt(0)
	v_add_f32_e32 v2, v2, v100
	s_nop 1
	v_mov_b32_dpp v100, v2 row_shl:4 row_mask:0xf bank_mask:0x5
	v_mov_b32_dpp v100, v2 row_shr:4 row_mask:0xf bank_mask:0xa
	s_waitcnt lgkmcnt(0)
	v_add_f32_e32 v2, v2, v100
	s_nop 1
	v_mov_b32_dpp v100, v2 row_shl:8 row_mask:0xf bank_mask:0x3
	v_mov_b32_dpp v100, v2 row_shr:8 row_mask:0xf bank_mask:0xc
	s_waitcnt lgkmcnt(0)
	v_add_f32_e32 v2, v2, v100
	v_mov_b32_e32 v100, v2
	s_nop 1
	v_permlane16_swap_b32_e32 v100, v2
	s_waitcnt lgkmcnt(0)
	v_add_f32_e32 v2, v2, v100
	ds_bpermute_b32 v100, v151, v2
	s_and_saveexec_b64 s[10:11], s[42:43]
	s_cbranch_execz .LBB0_751
	v_mul_f32_e32 v102, 0x3a800000, v1
	s_waitcnt lgkmcnt(0)
	v_add_f32_e32 v1, v2, v100
	v_fmamk_f32 v1, v1, 0x3a800000, v241
	v_rsq_f32_e32 v103, v1
	s_add_i32 s3, s14, 0
	s_add_i32 s3, s3, 0x23818
	v_mov_b32_e32 v1, s3
	ds_write_b64 v1, v[102:103]
.LBB0_751:
	s_or_b64 exec, exec, s[10:11]
	v_lshlrev_b32_e32 v103, 16, v93
	v_lshlrev_b32_e32 v102, 16, v92
	v_and_b32_e32 v93, 0xffff0000, v93
	v_and_b32_e32 v92, 0xffff0000, v92
	v_pk_add_f32 v[104:105], v[102:103], v[92:93]
	v_lshlrev_b32_e32 v2, 16, v96
	v_add_f32_e32 v1, v104, v105
	v_lshlrev_b32_e32 v105, 16, v95
	v_lshlrev_b32_e32 v104, 16, v94
	v_and_b32_e32 v95, 0xffff0000, v95
	v_and_b32_e32 v94, 0xffff0000, v94
	v_pk_add_f32 v[106:107], v[104:105], v[94:95]
	v_and_b32_e32 v110, 0xffff0000, v96
	v_lshlrev_b32_e32 v111, 16, v97
	v_and_b32_e32 v112, 0xffff0000, v97
	v_and_b32_e32 v113, 0xffff0000, v98
	v_pk_add_f32 v[106:107], v[106:107], v[106:107] op_sel:[0,1] op_sel_hi:[1,0]
	v_lshlrev_b32_e32 v97, 16, v98
	v_lshlrev_b32_e32 v101, 16, v99
	v_and_b32_e32 v99, 0xffff0000, v99
	v_add_f32_e32 v96, 0, v1
	s_waitcnt lgkmcnt(0)
	v_add_f32_e32 v100, v2, v110
	v_add_f32_e32 v98, v111, v112
	v_mov_b32_e32 v107, v113
	v_pk_add_f32 v[106:107], v[96:97], v[106:107]
	v_pk_add_f32 v[108:109], v[100:101], v[98:99]
	s_nop 0
	v_pk_add_f32 v[106:107], v[106:107], v[108:109]
	s_nop 0
	v_add_f32_e32 v1, v106, v107
	s_nop 1
	v_mov_b32_dpp v96, v1 quad_perm:[1,0,3,2] row_mask:0xf bank_mask:0xf
	s_waitcnt lgkmcnt(0)
	v_add_f32_e32 v1, v1, v96
	s_nop 1
	v_mov_b32_dpp v96, v1 quad_perm:[2,3,0,1] row_mask:0xf bank_mask:0xf
	s_waitcnt lgkmcnt(0)
	v_add_f32_e32 v1, v1, v96
	s_nop 1
	v_mov_b32_dpp v96, v1 row_shl:4 row_mask:0xf bank_mask:0x5
	v_mov_b32_dpp v96, v1 row_shr:4 row_mask:0xf bank_mask:0xa
	s_waitcnt lgkmcnt(0)
	v_add_f32_e32 v1, v1, v96
	s_nop 1
	v_mov_b32_dpp v96, v1 row_shl:8 row_mask:0xf bank_mask:0x3
	v_mov_b32_dpp v96, v1 row_shr:8 row_mask:0xf bank_mask:0xc
	s_waitcnt lgkmcnt(0)
	v_add_f32_e32 v1, v1, v96
	v_mov_b32_e32 v96, v1
	s_nop 1
	v_permlane16_swap_b32_e32 v96, v1
	s_waitcnt lgkmcnt(0)
	v_add_f32_e32 v1, v1, v96
	v_mov_b32_e32 v96, v1
	s_nop 1
	v_permlane32_swap_b32_e32 v96, v1
	s_waitcnt lgkmcnt(0)
	v_add_f32_e32 v1, v1, v96
	v_fmac_f32_e32 v93, 0xba800000, v1
	v_fmac_f32_e32 v92, 0xba800000, v1
	v_fmac_f32_e32 v103, 0xba800000, v1
	v_fmac_f32_e32 v102, 0xba800000, v1
	v_mul_f32_e32 v92, v92, v92
	v_mul_f32_e32 v93, v93, v93
	v_fmac_f32_e32 v92, v102, v102
	v_fmac_f32_e32 v93, v103, v103
	v_fmac_f32_e32 v95, 0xba800000, v1
	v_fmac_f32_e32 v94, 0xba800000, v1
	v_add_f32_e32 v92, v92, v93
	v_fmac_f32_e32 v105, 0xba800000, v1
	v_fmac_f32_e32 v104, 0xba800000, v1
	v_mul_f32_e32 v93, v94, v94
	v_mul_f32_e32 v94, v95, v95
	v_fmac_f32_e32 v93, v104, v104
	v_fmac_f32_e32 v94, v105, v105
	v_add_f32_e32 v93, v93, v94
	v_fmac_f32_e32 v110, 0xba800000, v1
	v_add_f32_e32 v92, v92, v93
	v_fmac_f32_e32 v112, 0xba800000, v1
	v_fmac_f32_e32 v2, 0xba800000, v1
	v_mul_f32_e32 v93, v110, v110
	v_fmac_f32_e32 v111, 0xba800000, v1
	v_fmac_f32_e32 v93, v2, v2
	v_mul_f32_e32 v2, v112, v112
	v_fmac_f32_e32 v2, v111, v111
	v_add_f32_e32 v2, v93, v2
	v_fmac_f32_e32 v99, 0xba800000, v1
	v_fmac_f32_e32 v113, 0xba800000, v1
	v_add_f32_e32 v2, v92, v2
	v_fmac_f32_e32 v101, 0xba800000, v1
	v_fmac_f32_e32 v97, 0xba800000, v1
	v_mul_f32_e32 v92, v113, v113
	v_mul_f32_e32 v93, v99, v99
	v_fmac_f32_e32 v92, v97, v97
	v_fmac_f32_e32 v93, v101, v101
	v_add_f32_e32 v92, v92, v93
	v_add_f32_e32 v2, v2, v92
	s_nop 1
	v_mov_b32_dpp v92, v2 quad_perm:[1,0,3,2] row_mask:0xf bank_mask:0xf
	s_waitcnt lgkmcnt(0)
	v_add_f32_e32 v2, v2, v92
	s_nop 1
	v_mov_b32_dpp v92, v2 quad_perm:[2,3,0,1] row_mask:0xf bank_mask:0xf
	s_waitcnt lgkmcnt(0)
	v_add_f32_e32 v2, v2, v92
	s_nop 1
	v_mov_b32_dpp v92, v2 row_shl:4 row_mask:0xf bank_mask:0x5
	v_mov_b32_dpp v92, v2 row_shr:4 row_mask:0xf bank_mask:0xa
	s_waitcnt lgkmcnt(0)
	v_add_f32_e32 v2, v2, v92
	s_nop 1
	v_mov_b32_dpp v92, v2 row_shl:8 row_mask:0xf bank_mask:0x3
	v_mov_b32_dpp v92, v2 row_shr:8 row_mask:0xf bank_mask:0xc
	s_waitcnt lgkmcnt(0)
	v_add_f32_e32 v2, v2, v92
	v_mov_b32_e32 v92, v2
	s_nop 1
	v_permlane16_swap_b32_e32 v92, v2
	s_waitcnt lgkmcnt(0)
	v_add_f32_e32 v2, v2, v92
	ds_bpermute_b32 v92, v151, v2
	s_and_saveexec_b64 s[10:11], s[42:43]
	s_cbranch_execz .LBB0_753
	v_mul_f32_e32 v94, 0x3a800000, v1
	s_waitcnt lgkmcnt(0)
	v_add_f32_e32 v1, v2, v92
	v_fmamk_f32 v1, v1, 0x3a800000, v241
	v_rsq_f32_e32 v95, v1
	s_add_i32 s3, s14, 0
	s_add_i32 s3, s3, 0x23820
	v_mov_b32_e32 v1, s3
	ds_write_b64 v1, v[94:95]
.LBB0_753:
	s_or_b64 exec, exec, s[10:11]
	v_lshlrev_b32_e32 v95, 16, v81
	v_lshlrev_b32_e32 v94, 16, v80
	v_and_b32_e32 v81, 0xffff0000, v81
	v_and_b32_e32 v80, 0xffff0000, v80
	v_pk_add_f32 v[96:97], v[94:95], v[80:81]
	v_lshlrev_b32_e32 v2, 16, v84
	v_add_f32_e32 v1, v96, v97
	v_lshlrev_b32_e32 v97, 16, v83
	v_lshlrev_b32_e32 v96, 16, v82
	v_and_b32_e32 v83, 0xffff0000, v83
	v_and_b32_e32 v82, 0xffff0000, v82
	v_pk_add_f32 v[98:99], v[96:97], v[82:83]
	v_and_b32_e32 v102, 0xffff0000, v84
	v_lshlrev_b32_e32 v103, 16, v85
	v_and_b32_e32 v104, 0xffff0000, v85
	v_and_b32_e32 v105, 0xffff0000, v86
	v_pk_add_f32 v[98:99], v[98:99], v[98:99] op_sel:[0,1] op_sel_hi:[1,0]
	v_lshlrev_b32_e32 v85, 16, v86
	v_lshlrev_b32_e32 v93, 16, v87
	v_and_b32_e32 v87, 0xffff0000, v87
	v_add_f32_e32 v84, 0, v1
	s_waitcnt lgkmcnt(0)
	v_add_f32_e32 v92, v2, v102
	v_add_f32_e32 v86, v103, v104
	v_mov_b32_e32 v99, v105
	v_pk_add_f32 v[98:99], v[84:85], v[98:99]
	v_pk_add_f32 v[100:101], v[92:93], v[86:87]
	s_nop 0
	v_pk_add_f32 v[98:99], v[98:99], v[100:101]
	s_nop 0
	v_add_f32_e32 v1, v98, v99
	s_nop 1
	v_mov_b32_dpp v84, v1 quad_perm:[1,0,3,2] row_mask:0xf bank_mask:0xf
	s_waitcnt lgkmcnt(0)
	v_add_f32_e32 v1, v1, v84
	s_nop 1
	v_mov_b32_dpp v84, v1 quad_perm:[2,3,0,1] row_mask:0xf bank_mask:0xf
	s_waitcnt lgkmcnt(0)
	v_add_f32_e32 v1, v1, v84
	s_nop 1
	v_mov_b32_dpp v84, v1 row_shl:4 row_mask:0xf bank_mask:0x5
	v_mov_b32_dpp v84, v1 row_shr:4 row_mask:0xf bank_mask:0xa
	s_waitcnt lgkmcnt(0)
	v_add_f32_e32 v1, v1, v84
	s_nop 1
	v_mov_b32_dpp v84, v1 row_shl:8 row_mask:0xf bank_mask:0x3
	v_mov_b32_dpp v84, v1 row_shr:8 row_mask:0xf bank_mask:0xc
	s_waitcnt lgkmcnt(0)
	v_add_f32_e32 v1, v1, v84
	v_mov_b32_e32 v84, v1
	s_nop 1
	v_permlane16_swap_b32_e32 v84, v1
	s_waitcnt lgkmcnt(0)
	v_add_f32_e32 v1, v1, v84
	v_mov_b32_e32 v84, v1
	s_nop 1
	v_permlane32_swap_b32_e32 v84, v1
	s_waitcnt lgkmcnt(0)
	v_add_f32_e32 v1, v1, v84
	v_fmac_f32_e32 v81, 0xba800000, v1
	v_fmac_f32_e32 v80, 0xba800000, v1
	v_fmac_f32_e32 v95, 0xba800000, v1
	v_fmac_f32_e32 v94, 0xba800000, v1
	v_mul_f32_e32 v80, v80, v80
	v_mul_f32_e32 v81, v81, v81
	v_fmac_f32_e32 v80, v94, v94
	v_fmac_f32_e32 v81, v95, v95
	v_fmac_f32_e32 v83, 0xba800000, v1
	v_fmac_f32_e32 v82, 0xba800000, v1
	v_add_f32_e32 v80, v80, v81
	v_fmac_f32_e32 v97, 0xba800000, v1
	v_fmac_f32_e32 v96, 0xba800000, v1
	v_mul_f32_e32 v81, v82, v82
	v_mul_f32_e32 v82, v83, v83
	v_fmac_f32_e32 v81, v96, v96
	v_fmac_f32_e32 v82, v97, v97
	v_add_f32_e32 v81, v81, v82
	v_fmac_f32_e32 v102, 0xba800000, v1
	v_add_f32_e32 v80, v80, v81
	v_fmac_f32_e32 v104, 0xba800000, v1
	v_fmac_f32_e32 v2, 0xba800000, v1
	v_mul_f32_e32 v81, v102, v102
	v_fmac_f32_e32 v103, 0xba800000, v1
	v_fmac_f32_e32 v81, v2, v2
	v_mul_f32_e32 v2, v104, v104
	v_fmac_f32_e32 v2, v103, v103
	v_add_f32_e32 v2, v81, v2
	v_fmac_f32_e32 v87, 0xba800000, v1
	v_fmac_f32_e32 v105, 0xba800000, v1
	v_add_f32_e32 v2, v80, v2
	v_fmac_f32_e32 v93, 0xba800000, v1
	v_fmac_f32_e32 v85, 0xba800000, v1
	v_mul_f32_e32 v80, v105, v105
	v_mul_f32_e32 v81, v87, v87
	v_fmac_f32_e32 v80, v85, v85
	v_fmac_f32_e32 v81, v93, v93
	v_add_f32_e32 v80, v80, v81
	v_add_f32_e32 v2, v2, v80
	s_nop 1
	v_mov_b32_dpp v80, v2 quad_perm:[1,0,3,2] row_mask:0xf bank_mask:0xf
	s_waitcnt lgkmcnt(0)
	v_add_f32_e32 v2, v2, v80
	s_nop 1
	v_mov_b32_dpp v80, v2 quad_perm:[2,3,0,1] row_mask:0xf bank_mask:0xf
	s_waitcnt lgkmcnt(0)
	v_add_f32_e32 v2, v2, v80
	s_nop 1
	v_mov_b32_dpp v80, v2 row_shl:4 row_mask:0xf bank_mask:0x5
	v_mov_b32_dpp v80, v2 row_shr:4 row_mask:0xf bank_mask:0xa
	s_waitcnt lgkmcnt(0)
	v_add_f32_e32 v2, v2, v80
	s_nop 1
	v_mov_b32_dpp v80, v2 row_shl:8 row_mask:0xf bank_mask:0x3
	v_mov_b32_dpp v80, v2 row_shr:8 row_mask:0xf bank_mask:0xc
	s_waitcnt lgkmcnt(0)
	v_add_f32_e32 v2, v2, v80
	v_mov_b32_e32 v80, v2
	s_nop 1
	v_permlane16_swap_b32_e32 v80, v2
	s_waitcnt lgkmcnt(0)
	v_add_f32_e32 v2, v2, v80
	ds_bpermute_b32 v80, v151, v2
	s_and_saveexec_b64 s[10:11], s[42:43]
	s_cbranch_execz .LBB0_755
	v_mul_f32_e32 v82, 0x3a800000, v1
	s_waitcnt lgkmcnt(0)
	v_add_f32_e32 v1, v2, v80
	v_fmamk_f32 v1, v1, 0x3a800000, v241
	v_rsq_f32_e32 v83, v1
	s_add_i32 s3, s14, 0
	s_add_i32 s3, s3, 0x23828
	v_mov_b32_e32 v1, s3
	ds_write_b64 v1, v[82:83]
.LBB0_755:
	s_or_b64 exec, exec, s[10:11]
	v_lshlrev_b32_e32 v87, 16, v77
	v_lshlrev_b32_e32 v86, 16, v76
	v_and_b32_e32 v77, 0xffff0000, v77
	v_and_b32_e32 v76, 0xffff0000, v76
	v_lshlrev_b32_e32 v2, 16, v88
	v_and_b32_e32 v94, 0xffff0000, v88
	v_lshlrev_b32_e32 v95, 16, v89
	v_and_b32_e32 v96, 0xffff0000, v89
	v_pk_add_f32 v[88:89], v[86:87], v[76:77]
	v_lshlrev_b32_e32 v81, 16, v90
	v_add_f32_e32 v1, v88, v89
	v_lshlrev_b32_e32 v89, 16, v79
	v_lshlrev_b32_e32 v88, 16, v78
	v_and_b32_e32 v79, 0xffff0000, v79
	v_and_b32_e32 v78, 0xffff0000, v78
	v_and_b32_e32 v97, 0xffff0000, v90
	v_lshlrev_b32_e32 v83, 16, v91
	v_and_b32_e32 v85, 0xffff0000, v91
	v_pk_add_f32 v[90:91], v[88:89], v[78:79]
	s_waitcnt lgkmcnt(0)
	v_add_f32_e32 v80, 0, v1
	v_pk_add_f32 v[90:91], v[90:91], v[90:91] op_sel:[0,1] op_sel_hi:[1,0]
	v_add_f32_e32 v82, v2, v94
	v_add_f32_e32 v84, v95, v96
	v_mov_b32_e32 v91, v97
	v_pk_add_f32 v[90:91], v[80:81], v[90:91]
	v_pk_add_f32 v[92:93], v[82:83], v[84:85]
	s_nop 0
	v_pk_add_f32 v[90:91], v[90:91], v[92:93]
	s_nop 0
	v_add_f32_e32 v1, v90, v91
	s_nop 1
	v_mov_b32_dpp v80, v1 quad_perm:[1,0,3,2] row_mask:0xf bank_mask:0xf
	s_waitcnt lgkmcnt(0)
	v_add_f32_e32 v1, v1, v80
	s_nop 1
	v_mov_b32_dpp v80, v1 quad_perm:[2,3,0,1] row_mask:0xf bank_mask:0xf
	s_waitcnt lgkmcnt(0)
	v_add_f32_e32 v1, v1, v80
	s_nop 1
	v_mov_b32_dpp v80, v1 row_shl:4 row_mask:0xf bank_mask:0x5
	v_mov_b32_dpp v80, v1 row_shr:4 row_mask:0xf bank_mask:0xa
	s_waitcnt lgkmcnt(0)
	v_add_f32_e32 v1, v1, v80
	s_nop 1
	v_mov_b32_dpp v80, v1 row_shl:8 row_mask:0xf bank_mask:0x3
	v_mov_b32_dpp v80, v1 row_shr:8 row_mask:0xf bank_mask:0xc
	s_waitcnt lgkmcnt(0)
	v_add_f32_e32 v1, v1, v80
	v_mov_b32_e32 v80, v1
	s_nop 1
	v_permlane16_swap_b32_e32 v80, v1
	s_waitcnt lgkmcnt(0)
	v_add_f32_e32 v1, v1, v80
	v_mov_b32_e32 v80, v1
	s_nop 1
	v_permlane32_swap_b32_e32 v80, v1
	s_waitcnt lgkmcnt(0)
	v_add_f32_e32 v1, v1, v80
	v_fmac_f32_e32 v77, 0xba800000, v1
	v_fmac_f32_e32 v76, 0xba800000, v1
	v_fmac_f32_e32 v87, 0xba800000, v1
	v_fmac_f32_e32 v86, 0xba800000, v1
	v_mul_f32_e32 v76, v76, v76
	v_mul_f32_e32 v77, v77, v77
	v_fmac_f32_e32 v76, v86, v86
	v_fmac_f32_e32 v77, v87, v87
	v_fmac_f32_e32 v79, 0xba800000, v1
	v_fmac_f32_e32 v78, 0xba800000, v1
	v_add_f32_e32 v76, v76, v77
	v_fmac_f32_e32 v89, 0xba800000, v1
	v_fmac_f32_e32 v88, 0xba800000, v1
	v_mul_f32_e32 v77, v78, v78
	v_mul_f32_e32 v78, v79, v79
	v_fmac_f32_e32 v77, v88, v88
	v_fmac_f32_e32 v78, v89, v89
	v_add_f32_e32 v77, v77, v78
	v_fmac_f32_e32 v94, 0xba800000, v1
	v_add_f32_e32 v76, v76, v77
	v_fmac_f32_e32 v96, 0xba800000, v1
	v_fmac_f32_e32 v2, 0xba800000, v1
	v_mul_f32_e32 v77, v94, v94
	v_fmac_f32_e32 v95, 0xba800000, v1
	v_fmac_f32_e32 v77, v2, v2
	v_mul_f32_e32 v2, v96, v96
	v_fmac_f32_e32 v2, v95, v95
	v_add_f32_e32 v2, v77, v2
	v_fmac_f32_e32 v85, 0xba800000, v1
	v_fmac_f32_e32 v97, 0xba800000, v1
	v_add_f32_e32 v2, v76, v2
	v_fmac_f32_e32 v83, 0xba800000, v1
	v_fmac_f32_e32 v81, 0xba800000, v1
	v_mul_f32_e32 v76, v97, v97
	v_mul_f32_e32 v77, v85, v85
	v_fmac_f32_e32 v76, v81, v81
	v_fmac_f32_e32 v77, v83, v83
	v_add_f32_e32 v76, v76, v77
	v_add_f32_e32 v2, v2, v76
	s_nop 1
	v_mov_b32_dpp v76, v2 quad_perm:[1,0,3,2] row_mask:0xf bank_mask:0xf
	s_waitcnt lgkmcnt(0)
	v_add_f32_e32 v2, v2, v76
	s_nop 1
	v_mov_b32_dpp v76, v2 quad_perm:[2,3,0,1] row_mask:0xf bank_mask:0xf
	s_waitcnt lgkmcnt(0)
	v_add_f32_e32 v2, v2, v76
	s_nop 1
	v_mov_b32_dpp v76, v2 row_shl:4 row_mask:0xf bank_mask:0x5
	v_mov_b32_dpp v76, v2 row_shr:4 row_mask:0xf bank_mask:0xa
	s_waitcnt lgkmcnt(0)
	v_add_f32_e32 v2, v2, v76
	s_nop 1
	v_mov_b32_dpp v76, v2 row_shl:8 row_mask:0xf bank_mask:0x3
	v_mov_b32_dpp v76, v2 row_shr:8 row_mask:0xf bank_mask:0xc
	s_waitcnt lgkmcnt(0)
	v_add_f32_e32 v2, v2, v76
	v_mov_b32_e32 v76, v2
	s_nop 1
	v_permlane16_swap_b32_e32 v76, v2
	s_waitcnt lgkmcnt(0)
	v_add_f32_e32 v2, v2, v76
	ds_bpermute_b32 v76, v151, v2
	s_and_saveexec_b64 s[10:11], s[42:43]
	s_cbranch_execz .LBB0_757
	v_mul_f32_e32 v78, 0x3a800000, v1
	s_waitcnt lgkmcnt(0)
	v_add_f32_e32 v1, v2, v76
	v_fmamk_f32 v1, v1, 0x3a800000, v241
	v_rsq_f32_e32 v79, v1
	s_add_i32 s3, s14, 0
	s_add_i32 s3, s3, 0x23830
	v_mov_b32_e32 v1, s3
	ds_write_b64 v1, v[78:79]
.LBB0_757:
	s_or_b64 exec, exec, s[10:11]
	v_lshlrev_b32_e32 v79, 16, v69
	v_lshlrev_b32_e32 v78, 16, v68
	v_and_b32_e32 v69, 0xffff0000, v69
	v_and_b32_e32 v68, 0xffff0000, v68
	v_pk_add_f32 v[80:81], v[78:79], v[68:69]
	v_lshlrev_b32_e32 v2, 16, v72
	v_add_f32_e32 v1, v80, v81
	v_lshlrev_b32_e32 v81, 16, v71
	v_lshlrev_b32_e32 v80, 16, v70
	v_and_b32_e32 v71, 0xffff0000, v71
	v_and_b32_e32 v70, 0xffff0000, v70
	v_pk_add_f32 v[82:83], v[80:81], v[70:71]
	v_and_b32_e32 v86, 0xffff0000, v72
	v_lshlrev_b32_e32 v87, 16, v73
	v_and_b32_e32 v88, 0xffff0000, v73
	v_and_b32_e32 v89, 0xffff0000, v74
	v_pk_add_f32 v[82:83], v[82:83], v[82:83] op_sel:[0,1] op_sel_hi:[1,0]
	v_lshlrev_b32_e32 v73, 16, v74
	v_lshlrev_b32_e32 v77, 16, v75
	v_and_b32_e32 v75, 0xffff0000, v75
	v_add_f32_e32 v72, 0, v1
	s_waitcnt lgkmcnt(0)
	v_add_f32_e32 v76, v2, v86
	v_add_f32_e32 v74, v87, v88
	v_mov_b32_e32 v83, v89
	v_pk_add_f32 v[82:83], v[72:73], v[82:83]
	v_pk_add_f32 v[84:85], v[76:77], v[74:75]
	s_nop 0
	v_pk_add_f32 v[82:83], v[82:83], v[84:85]
	s_nop 0
	v_add_f32_e32 v1, v82, v83
	s_nop 1
	v_mov_b32_dpp v72, v1 quad_perm:[1,0,3,2] row_mask:0xf bank_mask:0xf
	s_waitcnt lgkmcnt(0)
	v_add_f32_e32 v1, v1, v72
	s_nop 1
	v_mov_b32_dpp v72, v1 quad_perm:[2,3,0,1] row_mask:0xf bank_mask:0xf
	s_waitcnt lgkmcnt(0)
	v_add_f32_e32 v1, v1, v72
	s_nop 1
	v_mov_b32_dpp v72, v1 row_shl:4 row_mask:0xf bank_mask:0x5
	v_mov_b32_dpp v72, v1 row_shr:4 row_mask:0xf bank_mask:0xa
	s_waitcnt lgkmcnt(0)
	v_add_f32_e32 v1, v1, v72
	s_nop 1
	v_mov_b32_dpp v72, v1 row_shl:8 row_mask:0xf bank_mask:0x3
	v_mov_b32_dpp v72, v1 row_shr:8 row_mask:0xf bank_mask:0xc
	s_waitcnt lgkmcnt(0)
	v_add_f32_e32 v1, v1, v72
	v_mov_b32_e32 v72, v1
	s_nop 1
	v_permlane16_swap_b32_e32 v72, v1
	s_waitcnt lgkmcnt(0)
	v_add_f32_e32 v1, v1, v72
	v_mov_b32_e32 v72, v1
	s_nop 1
	v_permlane32_swap_b32_e32 v72, v1
	s_waitcnt lgkmcnt(0)
	v_add_f32_e32 v1, v1, v72
	v_fmac_f32_e32 v69, 0xba800000, v1
	v_fmac_f32_e32 v68, 0xba800000, v1
	v_fmac_f32_e32 v79, 0xba800000, v1
	v_fmac_f32_e32 v78, 0xba800000, v1
	v_mul_f32_e32 v68, v68, v68
	v_mul_f32_e32 v69, v69, v69
	v_fmac_f32_e32 v68, v78, v78
	v_fmac_f32_e32 v69, v79, v79
	v_fmac_f32_e32 v71, 0xba800000, v1
	v_fmac_f32_e32 v70, 0xba800000, v1
	v_add_f32_e32 v68, v68, v69
	v_fmac_f32_e32 v81, 0xba800000, v1
	v_fmac_f32_e32 v80, 0xba800000, v1
	v_mul_f32_e32 v69, v70, v70
	v_mul_f32_e32 v70, v71, v71
	v_fmac_f32_e32 v69, v80, v80
	v_fmac_f32_e32 v70, v81, v81
	v_add_f32_e32 v69, v69, v70
	v_fmac_f32_e32 v86, 0xba800000, v1
	v_add_f32_e32 v68, v68, v69
	v_fmac_f32_e32 v88, 0xba800000, v1
	v_fmac_f32_e32 v2, 0xba800000, v1
	v_mul_f32_e32 v69, v86, v86
	v_fmac_f32_e32 v87, 0xba800000, v1
	v_fmac_f32_e32 v69, v2, v2
	v_mul_f32_e32 v2, v88, v88
	v_fmac_f32_e32 v2, v87, v87
	v_add_f32_e32 v2, v69, v2
	v_fmac_f32_e32 v75, 0xba800000, v1
	v_fmac_f32_e32 v89, 0xba800000, v1
	v_add_f32_e32 v2, v68, v2
	v_fmac_f32_e32 v77, 0xba800000, v1
	v_fmac_f32_e32 v73, 0xba800000, v1
	v_mul_f32_e32 v68, v89, v89
	v_mul_f32_e32 v69, v75, v75
	v_fmac_f32_e32 v68, v73, v73
	v_fmac_f32_e32 v69, v77, v77
	v_add_f32_e32 v68, v68, v69
	v_add_f32_e32 v2, v2, v68
	s_nop 1
	v_mov_b32_dpp v68, v2 quad_perm:[1,0,3,2] row_mask:0xf bank_mask:0xf
	s_waitcnt lgkmcnt(0)
	v_add_f32_e32 v2, v2, v68
	s_nop 1
	v_mov_b32_dpp v68, v2 quad_perm:[2,3,0,1] row_mask:0xf bank_mask:0xf
	s_waitcnt lgkmcnt(0)
	v_add_f32_e32 v2, v2, v68
	s_nop 1
	v_mov_b32_dpp v68, v2 row_shl:4 row_mask:0xf bank_mask:0x5
	v_mov_b32_dpp v68, v2 row_shr:4 row_mask:0xf bank_mask:0xa
	s_waitcnt lgkmcnt(0)
	v_add_f32_e32 v2, v2, v68
	s_nop 1
	v_mov_b32_dpp v68, v2 row_shl:8 row_mask:0xf bank_mask:0x3
	v_mov_b32_dpp v68, v2 row_shr:8 row_mask:0xf bank_mask:0xc
	s_waitcnt lgkmcnt(0)
	v_add_f32_e32 v2, v2, v68
	v_mov_b32_e32 v68, v2
	s_nop 1
	v_permlane16_swap_b32_e32 v68, v2
	s_waitcnt lgkmcnt(0)
	v_add_f32_e32 v2, v2, v68
	ds_bpermute_b32 v68, v151, v2
	s_and_saveexec_b64 s[10:11], s[42:43]
	s_cbranch_execz .LBB0_759
	v_mul_f32_e32 v70, 0x3a800000, v1
	s_waitcnt lgkmcnt(0)
	v_add_f32_e32 v1, v2, v68
	v_fmamk_f32 v1, v1, 0x3a800000, v241
	v_rsq_f32_e32 v71, v1
	s_add_i32 s3, s14, 0
	s_add_i32 s3, s3, 0x23838
	v_mov_b32_e32 v1, s3
	ds_write_b64 v1, v[70:71]
.LBB0_759:
	s_or_b64 exec, exec, s[10:11]
	v_lshlrev_b32_e32 v71, 16, v61
	v_lshlrev_b32_e32 v70, 16, v60
	v_and_b32_e32 v61, 0xffff0000, v61
	v_and_b32_e32 v60, 0xffff0000, v60
	v_pk_add_f32 v[72:73], v[70:71], v[60:61]
	v_lshlrev_b32_e32 v2, 16, v64
	v_add_f32_e32 v1, v72, v73
	v_lshlrev_b32_e32 v73, 16, v63
	v_lshlrev_b32_e32 v72, 16, v62
	v_and_b32_e32 v63, 0xffff0000, v63
	v_and_b32_e32 v62, 0xffff0000, v62
	v_pk_add_f32 v[74:75], v[72:73], v[62:63]
	v_and_b32_e32 v78, 0xffff0000, v64
	v_lshlrev_b32_e32 v79, 16, v65
	v_and_b32_e32 v80, 0xffff0000, v65
	v_and_b32_e32 v81, 0xffff0000, v66
	v_pk_add_f32 v[74:75], v[74:75], v[74:75] op_sel:[0,1] op_sel_hi:[1,0]
	v_lshlrev_b32_e32 v65, 16, v66
	v_lshlrev_b32_e32 v69, 16, v67
	v_and_b32_e32 v67, 0xffff0000, v67
	v_add_f32_e32 v64, 0, v1
	s_waitcnt lgkmcnt(0)
	v_add_f32_e32 v68, v2, v78
	v_add_f32_e32 v66, v79, v80
	v_mov_b32_e32 v75, v81
	v_pk_add_f32 v[74:75], v[64:65], v[74:75]
	v_pk_add_f32 v[76:77], v[68:69], v[66:67]
	s_nop 0
	v_pk_add_f32 v[74:75], v[74:75], v[76:77]
	s_nop 0
	v_add_f32_e32 v1, v74, v75
	s_nop 1
	v_mov_b32_dpp v64, v1 quad_perm:[1,0,3,2] row_mask:0xf bank_mask:0xf
	s_waitcnt lgkmcnt(0)
	v_add_f32_e32 v1, v1, v64
	s_nop 1
	v_mov_b32_dpp v64, v1 quad_perm:[2,3,0,1] row_mask:0xf bank_mask:0xf
	s_waitcnt lgkmcnt(0)
	v_add_f32_e32 v1, v1, v64
	s_nop 1
	v_mov_b32_dpp v64, v1 row_shl:4 row_mask:0xf bank_mask:0x5
	v_mov_b32_dpp v64, v1 row_shr:4 row_mask:0xf bank_mask:0xa
	s_waitcnt lgkmcnt(0)
	v_add_f32_e32 v1, v1, v64
	s_nop 1
	v_mov_b32_dpp v64, v1 row_shl:8 row_mask:0xf bank_mask:0x3
	v_mov_b32_dpp v64, v1 row_shr:8 row_mask:0xf bank_mask:0xc
	s_waitcnt lgkmcnt(0)
	v_add_f32_e32 v1, v1, v64
	v_mov_b32_e32 v64, v1
	s_nop 1
	v_permlane16_swap_b32_e32 v64, v1
	s_waitcnt lgkmcnt(0)
	v_add_f32_e32 v1, v1, v64
	v_mov_b32_e32 v64, v1
	s_nop 1
	v_permlane32_swap_b32_e32 v64, v1
	s_waitcnt lgkmcnt(0)
	v_add_f32_e32 v1, v1, v64
	v_fmac_f32_e32 v61, 0xba800000, v1
	v_fmac_f32_e32 v60, 0xba800000, v1
	v_fmac_f32_e32 v71, 0xba800000, v1
	v_fmac_f32_e32 v70, 0xba800000, v1
	v_mul_f32_e32 v60, v60, v60
	v_mul_f32_e32 v61, v61, v61
	v_fmac_f32_e32 v60, v70, v70
	v_fmac_f32_e32 v61, v71, v71
	v_fmac_f32_e32 v63, 0xba800000, v1
	v_fmac_f32_e32 v62, 0xba800000, v1
	v_add_f32_e32 v60, v60, v61
	v_fmac_f32_e32 v73, 0xba800000, v1
	v_fmac_f32_e32 v72, 0xba800000, v1
	v_mul_f32_e32 v61, v62, v62
	v_mul_f32_e32 v62, v63, v63
	v_fmac_f32_e32 v61, v72, v72
	v_fmac_f32_e32 v62, v73, v73
	v_add_f32_e32 v61, v61, v62
	v_fmac_f32_e32 v78, 0xba800000, v1
	v_add_f32_e32 v60, v60, v61
	v_fmac_f32_e32 v80, 0xba800000, v1
	v_fmac_f32_e32 v2, 0xba800000, v1
	v_mul_f32_e32 v61, v78, v78
	v_fmac_f32_e32 v79, 0xba800000, v1
	v_fmac_f32_e32 v61, v2, v2
	v_mul_f32_e32 v2, v80, v80
	v_fmac_f32_e32 v2, v79, v79
	v_add_f32_e32 v2, v61, v2
	v_fmac_f32_e32 v67, 0xba800000, v1
	v_fmac_f32_e32 v81, 0xba800000, v1
	v_add_f32_e32 v2, v60, v2
	v_fmac_f32_e32 v69, 0xba800000, v1
	v_fmac_f32_e32 v65, 0xba800000, v1
	v_mul_f32_e32 v60, v81, v81
	v_mul_f32_e32 v61, v67, v67
	v_fmac_f32_e32 v60, v65, v65
	v_fmac_f32_e32 v61, v69, v69
	v_add_f32_e32 v60, v60, v61
	v_add_f32_e32 v2, v2, v60
	s_nop 1
	v_mov_b32_dpp v60, v2 quad_perm:[1,0,3,2] row_mask:0xf bank_mask:0xf
	s_waitcnt lgkmcnt(0)
	v_add_f32_e32 v2, v2, v60
	s_nop 1
	v_mov_b32_dpp v60, v2 quad_perm:[2,3,0,1] row_mask:0xf bank_mask:0xf
	s_waitcnt lgkmcnt(0)
	v_add_f32_e32 v2, v2, v60
	s_nop 1
	v_mov_b32_dpp v60, v2 row_shl:4 row_mask:0xf bank_mask:0x5
	v_mov_b32_dpp v60, v2 row_shr:4 row_mask:0xf bank_mask:0xa
	s_waitcnt lgkmcnt(0)
	v_add_f32_e32 v2, v2, v60
	s_nop 1
	v_mov_b32_dpp v60, v2 row_shl:8 row_mask:0xf bank_mask:0x3
	v_mov_b32_dpp v60, v2 row_shr:8 row_mask:0xf bank_mask:0xc
	s_waitcnt lgkmcnt(0)
	v_add_f32_e32 v2, v2, v60
	v_mov_b32_e32 v60, v2
	s_nop 1
	v_permlane16_swap_b32_e32 v60, v2
	s_waitcnt lgkmcnt(0)
	v_add_f32_e32 v2, v2, v60
	ds_bpermute_b32 v60, v151, v2
	s_and_saveexec_b64 s[10:11], s[42:43]
	s_cbranch_execz .LBB0_761
	v_mul_f32_e32 v62, 0x3a800000, v1
	s_waitcnt lgkmcnt(0)
	v_add_f32_e32 v1, v2, v60
	v_fmamk_f32 v1, v1, 0x3a800000, v241
	v_rsq_f32_e32 v63, v1
	s_add_i32 s3, s14, 0
	s_add_i32 s3, s3, 0x23840
	v_mov_b32_e32 v1, s3
	ds_write_b64 v1, v[62:63]
.LBB0_761:
	s_or_b64 exec, exec, s[10:11]
	v_lshlrev_b32_e32 v63, 16, v49
	v_lshlrev_b32_e32 v62, 16, v48
	v_and_b32_e32 v49, 0xffff0000, v49
	v_and_b32_e32 v48, 0xffff0000, v48
	v_pk_add_f32 v[64:65], v[62:63], v[48:49]
	v_lshlrev_b32_e32 v2, 16, v56
	v_add_f32_e32 v1, v64, v65
	v_lshlrev_b32_e32 v65, 16, v51
	v_lshlrev_b32_e32 v64, 16, v50
	v_and_b32_e32 v51, 0xffff0000, v51
	v_and_b32_e32 v50, 0xffff0000, v50
	v_pk_add_f32 v[66:67], v[64:65], v[50:51]
	v_and_b32_e32 v70, 0xffff0000, v56
	v_lshlrev_b32_e32 v71, 16, v57
	v_and_b32_e32 v72, 0xffff0000, v57
	v_and_b32_e32 v73, 0xffff0000, v58
	v_pk_add_f32 v[66:67], v[66:67], v[66:67] op_sel:[0,1] op_sel_hi:[1,0]
	v_lshlrev_b32_e32 v57, 16, v58
	v_lshlrev_b32_e32 v61, 16, v59
	v_and_b32_e32 v59, 0xffff0000, v59
	v_add_f32_e32 v56, 0, v1
	s_waitcnt lgkmcnt(0)
	v_add_f32_e32 v60, v2, v70
	v_add_f32_e32 v58, v71, v72
	v_mov_b32_e32 v67, v73
	v_pk_add_f32 v[66:67], v[56:57], v[66:67]
	v_pk_add_f32 v[68:69], v[60:61], v[58:59]
	s_nop 0
	v_pk_add_f32 v[66:67], v[66:67], v[68:69]
	s_nop 0
	v_add_f32_e32 v1, v66, v67
	s_nop 1
	v_mov_b32_dpp v56, v1 quad_perm:[1,0,3,2] row_mask:0xf bank_mask:0xf
	s_waitcnt lgkmcnt(0)
	v_add_f32_e32 v1, v1, v56
	s_nop 1
	v_mov_b32_dpp v56, v1 quad_perm:[2,3,0,1] row_mask:0xf bank_mask:0xf
	s_waitcnt lgkmcnt(0)
	v_add_f32_e32 v1, v1, v56
	s_nop 1
	v_mov_b32_dpp v56, v1 row_shl:4 row_mask:0xf bank_mask:0x5
	v_mov_b32_dpp v56, v1 row_shr:4 row_mask:0xf bank_mask:0xa
	s_waitcnt lgkmcnt(0)
	v_add_f32_e32 v1, v1, v56
	s_nop 1
	v_mov_b32_dpp v56, v1 row_shl:8 row_mask:0xf bank_mask:0x3
	v_mov_b32_dpp v56, v1 row_shr:8 row_mask:0xf bank_mask:0xc
	s_waitcnt lgkmcnt(0)
	v_add_f32_e32 v1, v1, v56
	v_mov_b32_e32 v56, v1
	s_nop 1
	v_permlane16_swap_b32_e32 v56, v1
	s_waitcnt lgkmcnt(0)
	v_add_f32_e32 v1, v1, v56
	v_mov_b32_e32 v56, v1
	s_nop 1
	v_permlane32_swap_b32_e32 v56, v1
	s_waitcnt lgkmcnt(0)
	v_add_f32_e32 v1, v1, v56
	v_fmac_f32_e32 v49, 0xba800000, v1
	v_fmac_f32_e32 v48, 0xba800000, v1
	v_fmac_f32_e32 v63, 0xba800000, v1
	v_fmac_f32_e32 v62, 0xba800000, v1
	v_mul_f32_e32 v48, v48, v48
	v_mul_f32_e32 v49, v49, v49
	v_fmac_f32_e32 v48, v62, v62
	v_fmac_f32_e32 v49, v63, v63
	v_fmac_f32_e32 v51, 0xba800000, v1
	v_fmac_f32_e32 v50, 0xba800000, v1
	v_add_f32_e32 v48, v48, v49
	v_fmac_f32_e32 v65, 0xba800000, v1
	v_fmac_f32_e32 v64, 0xba800000, v1
	v_mul_f32_e32 v49, v50, v50
	v_mul_f32_e32 v50, v51, v51
	v_fmac_f32_e32 v49, v64, v64
	v_fmac_f32_e32 v50, v65, v65
	v_add_f32_e32 v49, v49, v50
	v_fmac_f32_e32 v70, 0xba800000, v1
	v_add_f32_e32 v48, v48, v49
	v_fmac_f32_e32 v72, 0xba800000, v1
	v_fmac_f32_e32 v2, 0xba800000, v1
	v_mul_f32_e32 v49, v70, v70
	v_fmac_f32_e32 v71, 0xba800000, v1
	v_fmac_f32_e32 v49, v2, v2
	v_mul_f32_e32 v2, v72, v72
	v_fmac_f32_e32 v2, v71, v71
	v_add_f32_e32 v2, v49, v2
	v_fmac_f32_e32 v59, 0xba800000, v1
	v_fmac_f32_e32 v73, 0xba800000, v1
	v_add_f32_e32 v2, v48, v2
	v_fmac_f32_e32 v61, 0xba800000, v1
	v_fmac_f32_e32 v57, 0xba800000, v1
	v_mul_f32_e32 v48, v73, v73
	v_mul_f32_e32 v49, v59, v59
	v_fmac_f32_e32 v48, v57, v57
	v_fmac_f32_e32 v49, v61, v61
	v_add_f32_e32 v48, v48, v49
	v_add_f32_e32 v2, v2, v48
	s_nop 1
	v_mov_b32_dpp v48, v2 quad_perm:[1,0,3,2] row_mask:0xf bank_mask:0xf
	s_waitcnt lgkmcnt(0)
	v_add_f32_e32 v2, v2, v48
	s_nop 1
	v_mov_b32_dpp v48, v2 quad_perm:[2,3,0,1] row_mask:0xf bank_mask:0xf
	s_waitcnt lgkmcnt(0)
	v_add_f32_e32 v2, v2, v48
	s_nop 1
	v_mov_b32_dpp v48, v2 row_shl:4 row_mask:0xf bank_mask:0x5
	v_mov_b32_dpp v48, v2 row_shr:4 row_mask:0xf bank_mask:0xa
	s_waitcnt lgkmcnt(0)
	v_add_f32_e32 v2, v2, v48
	s_nop 1
	v_mov_b32_dpp v48, v2 row_shl:8 row_mask:0xf bank_mask:0x3
	v_mov_b32_dpp v48, v2 row_shr:8 row_mask:0xf bank_mask:0xc
	s_waitcnt lgkmcnt(0)
	v_add_f32_e32 v2, v2, v48
	v_mov_b32_e32 v48, v2
	s_nop 1
	v_permlane16_swap_b32_e32 v48, v2
	s_waitcnt lgkmcnt(0)
	v_add_f32_e32 v2, v2, v48
	ds_bpermute_b32 v48, v151, v2
	s_and_saveexec_b64 s[10:11], s[42:43]
	s_cbranch_execz .LBB0_763
	v_mul_f32_e32 v50, 0x3a800000, v1
	s_waitcnt lgkmcnt(0)
	v_add_f32_e32 v1, v2, v48
	v_fmamk_f32 v1, v1, 0x3a800000, v241
	v_rsq_f32_e32 v51, v1
	s_add_i32 s3, s14, 0
	s_add_i32 s3, s3, 0x23848
	v_mov_b32_e32 v1, s3
	ds_write_b64 v1, v[50:51]
.LBB0_763:
	s_or_b64 exec, exec, s[10:11]
	v_lshlrev_b32_e32 v63, 16, v53
	v_and_b32_e32 v64, 0xffff0000, v53
	v_lshlrev_b32_e32 v49, 16, v54
	v_and_b32_e32 v65, 0xffff0000, v54
	v_lshlrev_b32_e32 v51, 16, v55
	v_and_b32_e32 v53, 0xffff0000, v55
	v_lshlrev_b32_e32 v55, 16, v41
	v_lshlrev_b32_e32 v54, 16, v40
	v_and_b32_e32 v41, 0xffff0000, v41
	v_and_b32_e32 v40, 0xffff0000, v40
	v_pk_add_f32 v[56:57], v[54:55], v[40:41]
	v_lshlrev_b32_e32 v2, 16, v52
	v_add_f32_e32 v1, v56, v57
	v_lshlrev_b32_e32 v57, 16, v43
	v_lshlrev_b32_e32 v56, 16, v42
	v_and_b32_e32 v43, 0xffff0000, v43
	v_and_b32_e32 v42, 0xffff0000, v42
	v_pk_add_f32 v[58:59], v[56:57], v[42:43]
	v_and_b32_e32 v62, 0xffff0000, v52
	v_pk_add_f32 v[58:59], v[58:59], v[58:59] op_sel:[0,1] op_sel_hi:[1,0]
	s_waitcnt lgkmcnt(0)
	v_add_f32_e32 v48, 0, v1
	v_add_f32_e32 v50, v2, v62
	v_add_f32_e32 v52, v63, v64
	v_mov_b32_e32 v59, v65
	v_pk_add_f32 v[58:59], v[48:49], v[58:59]
	v_pk_add_f32 v[60:61], v[50:51], v[52:53]
	s_nop 0
	v_pk_add_f32 v[58:59], v[58:59], v[60:61]
	s_nop 0
	v_add_f32_e32 v1, v58, v59
	s_nop 1
	v_mov_b32_dpp v48, v1 quad_perm:[1,0,3,2] row_mask:0xf bank_mask:0xf
	s_waitcnt lgkmcnt(0)
	v_add_f32_e32 v1, v1, v48
	s_nop 1
	v_mov_b32_dpp v48, v1 quad_perm:[2,3,0,1] row_mask:0xf bank_mask:0xf
	s_waitcnt lgkmcnt(0)
	v_add_f32_e32 v1, v1, v48
	s_nop 1
	v_mov_b32_dpp v48, v1 row_shl:4 row_mask:0xf bank_mask:0x5
	v_mov_b32_dpp v48, v1 row_shr:4 row_mask:0xf bank_mask:0xa
	s_waitcnt lgkmcnt(0)
	v_add_f32_e32 v1, v1, v48
	s_nop 1
	v_mov_b32_dpp v48, v1 row_shl:8 row_mask:0xf bank_mask:0x3
	v_mov_b32_dpp v48, v1 row_shr:8 row_mask:0xf bank_mask:0xc
	s_waitcnt lgkmcnt(0)
	v_add_f32_e32 v1, v1, v48
	v_mov_b32_e32 v48, v1
	s_nop 1
	v_permlane16_swap_b32_e32 v48, v1
	s_waitcnt lgkmcnt(0)
	v_add_f32_e32 v1, v1, v48
	v_mov_b32_e32 v48, v1
	s_nop 1
	v_permlane32_swap_b32_e32 v48, v1
	s_waitcnt lgkmcnt(0)
	v_add_f32_e32 v1, v1, v48
	v_fmac_f32_e32 v41, 0xba800000, v1
	v_fmac_f32_e32 v40, 0xba800000, v1
	v_fmac_f32_e32 v55, 0xba800000, v1
	v_fmac_f32_e32 v54, 0xba800000, v1
	v_mul_f32_e32 v40, v40, v40
	v_mul_f32_e32 v41, v41, v41
	v_fmac_f32_e32 v40, v54, v54
	v_fmac_f32_e32 v41, v55, v55
	v_fmac_f32_e32 v43, 0xba800000, v1
	v_fmac_f32_e32 v42, 0xba800000, v1
	v_add_f32_e32 v40, v40, v41
	v_fmac_f32_e32 v57, 0xba800000, v1
	v_fmac_f32_e32 v56, 0xba800000, v1
	v_mul_f32_e32 v41, v42, v42
	v_mul_f32_e32 v42, v43, v43
	v_fmac_f32_e32 v41, v56, v56
	v_fmac_f32_e32 v42, v57, v57
	v_add_f32_e32 v41, v41, v42
	v_fmac_f32_e32 v62, 0xba800000, v1
	v_add_f32_e32 v40, v40, v41
	v_fmac_f32_e32 v64, 0xba800000, v1
	v_fmac_f32_e32 v2, 0xba800000, v1
	v_mul_f32_e32 v41, v62, v62
	v_fmac_f32_e32 v63, 0xba800000, v1
	v_fmac_f32_e32 v41, v2, v2
	v_mul_f32_e32 v2, v64, v64
	v_fmac_f32_e32 v2, v63, v63
	v_add_f32_e32 v2, v41, v2
	v_fmac_f32_e32 v53, 0xba800000, v1
	v_fmac_f32_e32 v65, 0xba800000, v1
	v_add_f32_e32 v2, v40, v2
	v_fmac_f32_e32 v51, 0xba800000, v1
	v_fmac_f32_e32 v49, 0xba800000, v1
	v_mul_f32_e32 v40, v65, v65
	v_mul_f32_e32 v41, v53, v53
	v_fmac_f32_e32 v40, v49, v49
	v_fmac_f32_e32 v41, v51, v51
	v_add_f32_e32 v40, v40, v41
	v_add_f32_e32 v2, v2, v40
	s_nop 1
	v_mov_b32_dpp v40, v2 quad_perm:[1,0,3,2] row_mask:0xf bank_mask:0xf
	s_waitcnt lgkmcnt(0)
	v_add_f32_e32 v2, v2, v40
	s_nop 1
	v_mov_b32_dpp v40, v2 quad_perm:[2,3,0,1] row_mask:0xf bank_mask:0xf
	s_waitcnt lgkmcnt(0)
	v_add_f32_e32 v2, v2, v40
	s_nop 1
	v_mov_b32_dpp v40, v2 row_shl:4 row_mask:0xf bank_mask:0x5
	v_mov_b32_dpp v40, v2 row_shr:4 row_mask:0xf bank_mask:0xa
	s_waitcnt lgkmcnt(0)
	v_add_f32_e32 v2, v2, v40
	s_nop 1
	v_mov_b32_dpp v40, v2 row_shl:8 row_mask:0xf bank_mask:0x3
	v_mov_b32_dpp v40, v2 row_shr:8 row_mask:0xf bank_mask:0xc
	s_waitcnt lgkmcnt(0)
	v_add_f32_e32 v2, v2, v40
	v_mov_b32_e32 v40, v2
	s_nop 1
	v_permlane16_swap_b32_e32 v40, v2
	s_waitcnt lgkmcnt(0)
	v_add_f32_e32 v2, v2, v40
	ds_bpermute_b32 v40, v151, v2
	s_and_saveexec_b64 s[10:11], s[42:43]
	s_cbranch_execz .LBB0_765
	v_mul_f32_e32 v42, 0x3a800000, v1
	s_waitcnt lgkmcnt(0)
	v_add_f32_e32 v1, v2, v40
	v_fmamk_f32 v1, v1, 0x3a800000, v241
	v_rsq_f32_e32 v43, v1
	s_add_i32 s3, s14, 0
	s_add_i32 s3, s3, 0x23850
	v_mov_b32_e32 v1, s3
	ds_write_b64 v1, v[42:43]
.LBB0_765:
	s_or_b64 exec, exec, s[10:11]
	v_lshlrev_b32_e32 v55, 16, v45
	v_and_b32_e32 v56, 0xffff0000, v45
	v_lshlrev_b32_e32 v41, 16, v46
	v_and_b32_e32 v57, 0xffff0000, v46
	v_lshlrev_b32_e32 v43, 16, v47
	v_and_b32_e32 v45, 0xffff0000, v47
	v_lshlrev_b32_e32 v47, 16, v37
	v_lshlrev_b32_e32 v46, 16, v36
	v_and_b32_e32 v37, 0xffff0000, v37
	v_and_b32_e32 v36, 0xffff0000, v36
	v_pk_add_f32 v[48:49], v[46:47], v[36:37]
	v_lshlrev_b32_e32 v2, 16, v44
	v_add_f32_e32 v1, v48, v49
	v_lshlrev_b32_e32 v49, 16, v39
	v_lshlrev_b32_e32 v48, 16, v38
	v_and_b32_e32 v39, 0xffff0000, v39
	v_and_b32_e32 v38, 0xffff0000, v38
	v_pk_add_f32 v[50:51], v[48:49], v[38:39]
	v_and_b32_e32 v54, 0xffff0000, v44
	v_pk_add_f32 v[50:51], v[50:51], v[50:51] op_sel:[0,1] op_sel_hi:[1,0]
	s_waitcnt lgkmcnt(0)
	v_add_f32_e32 v40, 0, v1
	v_add_f32_e32 v42, v2, v54
	v_add_f32_e32 v44, v55, v56
	v_mov_b32_e32 v51, v57
	v_pk_add_f32 v[50:51], v[40:41], v[50:51]
	v_pk_add_f32 v[52:53], v[42:43], v[44:45]
	s_nop 0
	v_pk_add_f32 v[50:51], v[50:51], v[52:53]
	s_nop 0
	v_add_f32_e32 v1, v50, v51
	s_nop 1
	v_mov_b32_dpp v40, v1 quad_perm:[1,0,3,2] row_mask:0xf bank_mask:0xf
	s_waitcnt lgkmcnt(0)
	v_add_f32_e32 v1, v1, v40
	s_nop 1
	v_mov_b32_dpp v40, v1 quad_perm:[2,3,0,1] row_mask:0xf bank_mask:0xf
	s_waitcnt lgkmcnt(0)
	v_add_f32_e32 v1, v1, v40
	s_nop 1
	v_mov_b32_dpp v40, v1 row_shl:4 row_mask:0xf bank_mask:0x5
	v_mov_b32_dpp v40, v1 row_shr:4 row_mask:0xf bank_mask:0xa
	s_waitcnt lgkmcnt(0)
	v_add_f32_e32 v1, v1, v40
	s_nop 1
	v_mov_b32_dpp v40, v1 row_shl:8 row_mask:0xf bank_mask:0x3
	v_mov_b32_dpp v40, v1 row_shr:8 row_mask:0xf bank_mask:0xc
	s_waitcnt lgkmcnt(0)
	v_add_f32_e32 v1, v1, v40
	v_mov_b32_e32 v40, v1
	s_nop 1
	v_permlane16_swap_b32_e32 v40, v1
	s_waitcnt lgkmcnt(0)
	v_add_f32_e32 v1, v1, v40
	v_mov_b32_e32 v40, v1
	s_nop 1
	v_permlane32_swap_b32_e32 v40, v1
	s_waitcnt lgkmcnt(0)
	v_add_f32_e32 v1, v1, v40
	v_fmac_f32_e32 v37, 0xba800000, v1
	v_fmac_f32_e32 v36, 0xba800000, v1
	v_fmac_f32_e32 v47, 0xba800000, v1
	v_fmac_f32_e32 v46, 0xba800000, v1
	v_mul_f32_e32 v36, v36, v36
	v_mul_f32_e32 v37, v37, v37
	v_fmac_f32_e32 v36, v46, v46
	v_fmac_f32_e32 v37, v47, v47
	v_fmac_f32_e32 v39, 0xba800000, v1
	v_fmac_f32_e32 v38, 0xba800000, v1
	v_add_f32_e32 v36, v36, v37
	v_fmac_f32_e32 v49, 0xba800000, v1
	v_fmac_f32_e32 v48, 0xba800000, v1
	v_mul_f32_e32 v37, v38, v38
	v_mul_f32_e32 v38, v39, v39
	v_fmac_f32_e32 v37, v48, v48
	v_fmac_f32_e32 v38, v49, v49
	v_add_f32_e32 v37, v37, v38
	v_fmac_f32_e32 v54, 0xba800000, v1
	v_add_f32_e32 v36, v36, v37
	v_fmac_f32_e32 v56, 0xba800000, v1
	v_fmac_f32_e32 v2, 0xba800000, v1
	v_mul_f32_e32 v37, v54, v54
	v_fmac_f32_e32 v55, 0xba800000, v1
	v_fmac_f32_e32 v37, v2, v2
	v_mul_f32_e32 v2, v56, v56
	v_fmac_f32_e32 v2, v55, v55
	v_add_f32_e32 v2, v37, v2
	v_fmac_f32_e32 v45, 0xba800000, v1
	v_fmac_f32_e32 v57, 0xba800000, v1
	v_add_f32_e32 v2, v36, v2
	v_fmac_f32_e32 v43, 0xba800000, v1
	v_fmac_f32_e32 v41, 0xba800000, v1
	v_mul_f32_e32 v36, v57, v57
	v_mul_f32_e32 v37, v45, v45
	v_fmac_f32_e32 v36, v41, v41
	v_fmac_f32_e32 v37, v43, v43
	v_add_f32_e32 v36, v36, v37
	v_add_f32_e32 v2, v2, v36
	s_nop 1
	v_mov_b32_dpp v36, v2 quad_perm:[1,0,3,2] row_mask:0xf bank_mask:0xf
	s_waitcnt lgkmcnt(0)
	v_add_f32_e32 v2, v2, v36
	s_nop 1
	v_mov_b32_dpp v36, v2 quad_perm:[2,3,0,1] row_mask:0xf bank_mask:0xf
	s_waitcnt lgkmcnt(0)
	v_add_f32_e32 v2, v2, v36
	s_nop 1
	v_mov_b32_dpp v36, v2 row_shl:4 row_mask:0xf bank_mask:0x5
	v_mov_b32_dpp v36, v2 row_shr:4 row_mask:0xf bank_mask:0xa
	s_waitcnt lgkmcnt(0)
	v_add_f32_e32 v2, v2, v36
	s_nop 1
	v_mov_b32_dpp v36, v2 row_shl:8 row_mask:0xf bank_mask:0x3
	v_mov_b32_dpp v36, v2 row_shr:8 row_mask:0xf bank_mask:0xc
	s_waitcnt lgkmcnt(0)
	v_add_f32_e32 v2, v2, v36
	v_mov_b32_e32 v36, v2
	s_nop 1
	v_permlane16_swap_b32_e32 v36, v2
	s_waitcnt lgkmcnt(0)
	v_add_f32_e32 v2, v2, v36
	ds_bpermute_b32 v36, v151, v2
	s_and_saveexec_b64 s[10:11], s[42:43]
	s_cbranch_execz .LBB0_767
	v_mul_f32_e32 v38, 0x3a800000, v1
	s_waitcnt lgkmcnt(0)
	v_add_f32_e32 v1, v2, v36
	v_fmamk_f32 v1, v1, 0x3a800000, v241
	v_rsq_f32_e32 v39, v1
	s_add_i32 s3, s14, 0
	s_add_i32 s3, s3, 0x23858
	v_mov_b32_e32 v1, s3
	ds_write_b64 v1, v[38:39]
.LBB0_767:
	s_or_b64 exec, exec, s[10:11]
	v_lshlrev_b32_e32 v39, 16, v29
	v_lshlrev_b32_e32 v38, 16, v28
	v_and_b32_e32 v29, 0xffff0000, v29
	v_and_b32_e32 v28, 0xffff0000, v28
	v_pk_add_f32 v[40:41], v[38:39], v[28:29]
	v_lshlrev_b32_e32 v2, 16, v32
	v_add_f32_e32 v1, v40, v41
	v_lshlrev_b32_e32 v41, 16, v31
	v_lshlrev_b32_e32 v40, 16, v30
	v_and_b32_e32 v31, 0xffff0000, v31
	v_and_b32_e32 v30, 0xffff0000, v30
	v_pk_add_f32 v[42:43], v[40:41], v[30:31]
	v_and_b32_e32 v46, 0xffff0000, v32
	v_lshlrev_b32_e32 v47, 16, v33
	v_and_b32_e32 v48, 0xffff0000, v33
	v_and_b32_e32 v49, 0xffff0000, v34
	v_pk_add_f32 v[42:43], v[42:43], v[42:43] op_sel:[0,1] op_sel_hi:[1,0]
	v_lshlrev_b32_e32 v33, 16, v34
	v_lshlrev_b32_e32 v37, 16, v35
	v_and_b32_e32 v35, 0xffff0000, v35
	v_add_f32_e32 v32, 0, v1
	s_waitcnt lgkmcnt(0)
	v_add_f32_e32 v36, v2, v46
	v_add_f32_e32 v34, v47, v48
	v_mov_b32_e32 v43, v49
	v_pk_add_f32 v[42:43], v[32:33], v[42:43]
	v_pk_add_f32 v[44:45], v[36:37], v[34:35]
	s_nop 0
	v_pk_add_f32 v[42:43], v[42:43], v[44:45]
	s_nop 0
	v_add_f32_e32 v1, v42, v43
	s_nop 1
	v_mov_b32_dpp v32, v1 quad_perm:[1,0,3,2] row_mask:0xf bank_mask:0xf
	s_waitcnt lgkmcnt(0)
	v_add_f32_e32 v1, v1, v32
	s_nop 1
	v_mov_b32_dpp v32, v1 quad_perm:[2,3,0,1] row_mask:0xf bank_mask:0xf
	s_waitcnt lgkmcnt(0)
	v_add_f32_e32 v1, v1, v32
	s_nop 1
	v_mov_b32_dpp v32, v1 row_shl:4 row_mask:0xf bank_mask:0x5
	v_mov_b32_dpp v32, v1 row_shr:4 row_mask:0xf bank_mask:0xa
	s_waitcnt lgkmcnt(0)
	v_add_f32_e32 v1, v1, v32
	s_nop 1
	v_mov_b32_dpp v32, v1 row_shl:8 row_mask:0xf bank_mask:0x3
	v_mov_b32_dpp v32, v1 row_shr:8 row_mask:0xf bank_mask:0xc
	s_waitcnt lgkmcnt(0)
	v_add_f32_e32 v1, v1, v32
	v_mov_b32_e32 v32, v1
	s_nop 1
	v_permlane16_swap_b32_e32 v32, v1
	s_waitcnt lgkmcnt(0)
	v_add_f32_e32 v1, v1, v32
	v_mov_b32_e32 v32, v1
	s_nop 1
	v_permlane32_swap_b32_e32 v32, v1
	s_waitcnt lgkmcnt(0)
	v_add_f32_e32 v1, v1, v32
	v_fmac_f32_e32 v29, 0xba800000, v1
	v_fmac_f32_e32 v28, 0xba800000, v1
	v_fmac_f32_e32 v39, 0xba800000, v1
	v_fmac_f32_e32 v38, 0xba800000, v1
	v_mul_f32_e32 v28, v28, v28
	v_mul_f32_e32 v29, v29, v29
	v_fmac_f32_e32 v28, v38, v38
	v_fmac_f32_e32 v29, v39, v39
	v_fmac_f32_e32 v31, 0xba800000, v1
	v_fmac_f32_e32 v30, 0xba800000, v1
	v_add_f32_e32 v28, v28, v29
	v_fmac_f32_e32 v41, 0xba800000, v1
	v_fmac_f32_e32 v40, 0xba800000, v1
	v_mul_f32_e32 v29, v30, v30
	v_mul_f32_e32 v30, v31, v31
	v_fmac_f32_e32 v29, v40, v40
	v_fmac_f32_e32 v30, v41, v41
	v_add_f32_e32 v29, v29, v30
	v_fmac_f32_e32 v46, 0xba800000, v1
	v_add_f32_e32 v28, v28, v29
	v_fmac_f32_e32 v48, 0xba800000, v1
	v_fmac_f32_e32 v2, 0xba800000, v1
	v_mul_f32_e32 v29, v46, v46
	v_fmac_f32_e32 v47, 0xba800000, v1
	v_fmac_f32_e32 v29, v2, v2
	v_mul_f32_e32 v2, v48, v48
	v_fmac_f32_e32 v2, v47, v47
	v_add_f32_e32 v2, v29, v2
	v_fmac_f32_e32 v35, 0xba800000, v1
	v_fmac_f32_e32 v49, 0xba800000, v1
	v_add_f32_e32 v2, v28, v2
	v_fmac_f32_e32 v37, 0xba800000, v1
	v_fmac_f32_e32 v33, 0xba800000, v1
	v_mul_f32_e32 v28, v49, v49
	v_mul_f32_e32 v29, v35, v35
	v_fmac_f32_e32 v28, v33, v33
	v_fmac_f32_e32 v29, v37, v37
	v_add_f32_e32 v28, v28, v29
	v_add_f32_e32 v2, v2, v28
	s_nop 1
	v_mov_b32_dpp v28, v2 quad_perm:[1,0,3,2] row_mask:0xf bank_mask:0xf
	s_waitcnt lgkmcnt(0)
	v_add_f32_e32 v2, v2, v28
	s_nop 1
	v_mov_b32_dpp v28, v2 quad_perm:[2,3,0,1] row_mask:0xf bank_mask:0xf
	s_waitcnt lgkmcnt(0)
	v_add_f32_e32 v2, v2, v28
	s_nop 1
	v_mov_b32_dpp v28, v2 row_shl:4 row_mask:0xf bank_mask:0x5
	v_mov_b32_dpp v28, v2 row_shr:4 row_mask:0xf bank_mask:0xa
	s_waitcnt lgkmcnt(0)
	v_add_f32_e32 v2, v2, v28
	s_nop 1
	v_mov_b32_dpp v28, v2 row_shl:8 row_mask:0xf bank_mask:0x3
	v_mov_b32_dpp v28, v2 row_shr:8 row_mask:0xf bank_mask:0xc
	s_waitcnt lgkmcnt(0)
	v_add_f32_e32 v2, v2, v28
	v_mov_b32_e32 v28, v2
	s_nop 1
	v_permlane16_swap_b32_e32 v28, v2
	s_waitcnt lgkmcnt(0)
	v_add_f32_e32 v2, v2, v28
	ds_bpermute_b32 v28, v151, v2
	s_and_saveexec_b64 s[10:11], s[42:43]
	s_cbranch_execz .LBB0_769
	v_mul_f32_e32 v30, 0x3a800000, v1
	s_waitcnt lgkmcnt(0)
	v_add_f32_e32 v1, v2, v28
	v_fmamk_f32 v1, v1, 0x3a800000, v241
	v_rsq_f32_e32 v31, v1
	s_add_i32 s3, s14, 0
	s_add_i32 s3, s3, 0x23860
	v_mov_b32_e32 v1, s3
	ds_write_b64 v1, v[30:31]
.LBB0_769:
	s_or_b64 exec, exec, s[10:11]
	v_lshlrev_b32_e32 v31, 16, v17
	v_lshlrev_b32_e32 v30, 16, v16
	v_and_b32_e32 v17, 0xffff0000, v17
	v_and_b32_e32 v16, 0xffff0000, v16
	v_pk_add_f32 v[32:33], v[30:31], v[16:17]
	v_lshlrev_b32_e32 v2, 16, v24
	v_add_f32_e32 v1, v32, v33
	v_lshlrev_b32_e32 v33, 16, v19
	v_lshlrev_b32_e32 v32, 16, v18
	v_and_b32_e32 v19, 0xffff0000, v19
	v_and_b32_e32 v18, 0xffff0000, v18
	v_pk_add_f32 v[34:35], v[32:33], v[18:19]
	v_and_b32_e32 v38, 0xffff0000, v24
	v_lshlrev_b32_e32 v39, 16, v25
	v_and_b32_e32 v40, 0xffff0000, v25
	v_and_b32_e32 v41, 0xffff0000, v26
	v_pk_add_f32 v[34:35], v[34:35], v[34:35] op_sel:[0,1] op_sel_hi:[1,0]
	v_lshlrev_b32_e32 v25, 16, v26
	v_lshlrev_b32_e32 v29, 16, v27
	v_and_b32_e32 v27, 0xffff0000, v27
	v_add_f32_e32 v24, 0, v1
	s_waitcnt lgkmcnt(0)
	v_add_f32_e32 v28, v2, v38
	v_add_f32_e32 v26, v39, v40
	v_mov_b32_e32 v35, v41
	v_pk_add_f32 v[34:35], v[24:25], v[34:35]
	v_pk_add_f32 v[36:37], v[28:29], v[26:27]
	s_nop 0
	v_pk_add_f32 v[34:35], v[34:35], v[36:37]
	s_nop 0
	v_add_f32_e32 v1, v34, v35
	s_nop 1
	v_mov_b32_dpp v24, v1 quad_perm:[1,0,3,2] row_mask:0xf bank_mask:0xf
	s_waitcnt lgkmcnt(0)
	v_add_f32_e32 v1, v1, v24
	s_nop 1
	v_mov_b32_dpp v24, v1 quad_perm:[2,3,0,1] row_mask:0xf bank_mask:0xf
	s_waitcnt lgkmcnt(0)
	v_add_f32_e32 v1, v1, v24
	s_nop 1
	v_mov_b32_dpp v24, v1 row_shl:4 row_mask:0xf bank_mask:0x5
	v_mov_b32_dpp v24, v1 row_shr:4 row_mask:0xf bank_mask:0xa
	s_waitcnt lgkmcnt(0)
	v_add_f32_e32 v1, v1, v24
	s_nop 1
	v_mov_b32_dpp v24, v1 row_shl:8 row_mask:0xf bank_mask:0x3
	v_mov_b32_dpp v24, v1 row_shr:8 row_mask:0xf bank_mask:0xc
	s_waitcnt lgkmcnt(0)
	v_add_f32_e32 v1, v1, v24
	v_mov_b32_e32 v24, v1
	s_nop 1
	v_permlane16_swap_b32_e32 v24, v1
	s_waitcnt lgkmcnt(0)
	v_add_f32_e32 v1, v1, v24
	v_mov_b32_e32 v24, v1
	s_nop 1
	v_permlane32_swap_b32_e32 v24, v1
	s_waitcnt lgkmcnt(0)
	v_add_f32_e32 v1, v1, v24
	v_fmac_f32_e32 v17, 0xba800000, v1
	v_fmac_f32_e32 v16, 0xba800000, v1
	v_fmac_f32_e32 v31, 0xba800000, v1
	v_fmac_f32_e32 v30, 0xba800000, v1
	v_mul_f32_e32 v16, v16, v16
	v_mul_f32_e32 v17, v17, v17
	v_fmac_f32_e32 v16, v30, v30
	v_fmac_f32_e32 v17, v31, v31
	v_fmac_f32_e32 v19, 0xba800000, v1
	v_fmac_f32_e32 v18, 0xba800000, v1
	v_add_f32_e32 v16, v16, v17
	v_fmac_f32_e32 v33, 0xba800000, v1
	v_fmac_f32_e32 v32, 0xba800000, v1
	v_mul_f32_e32 v17, v18, v18
	v_mul_f32_e32 v18, v19, v19
	v_fmac_f32_e32 v17, v32, v32
	v_fmac_f32_e32 v18, v33, v33
	v_add_f32_e32 v17, v17, v18
	v_fmac_f32_e32 v38, 0xba800000, v1
	v_add_f32_e32 v16, v16, v17
	v_fmac_f32_e32 v40, 0xba800000, v1
	v_fmac_f32_e32 v2, 0xba800000, v1
	v_mul_f32_e32 v17, v38, v38
	v_fmac_f32_e32 v39, 0xba800000, v1
	v_fmac_f32_e32 v17, v2, v2
	v_mul_f32_e32 v2, v40, v40
	v_fmac_f32_e32 v2, v39, v39
	v_add_f32_e32 v2, v17, v2
	v_fmac_f32_e32 v27, 0xba800000, v1
	v_fmac_f32_e32 v41, 0xba800000, v1
	v_add_f32_e32 v2, v16, v2
	v_fmac_f32_e32 v29, 0xba800000, v1
	v_fmac_f32_e32 v25, 0xba800000, v1
	v_mul_f32_e32 v16, v41, v41
	v_mul_f32_e32 v17, v27, v27
	v_fmac_f32_e32 v16, v25, v25
	v_fmac_f32_e32 v17, v29, v29
	v_add_f32_e32 v16, v16, v17
	v_add_f32_e32 v2, v2, v16
	s_nop 1
	v_mov_b32_dpp v16, v2 quad_perm:[1,0,3,2] row_mask:0xf bank_mask:0xf
	s_waitcnt lgkmcnt(0)
	v_add_f32_e32 v2, v2, v16
	s_nop 1
	v_mov_b32_dpp v16, v2 quad_perm:[2,3,0,1] row_mask:0xf bank_mask:0xf
	s_waitcnt lgkmcnt(0)
	v_add_f32_e32 v2, v2, v16
	s_nop 1
	v_mov_b32_dpp v16, v2 row_shl:4 row_mask:0xf bank_mask:0x5
	v_mov_b32_dpp v16, v2 row_shr:4 row_mask:0xf bank_mask:0xa
	s_waitcnt lgkmcnt(0)
	v_add_f32_e32 v2, v2, v16
	s_nop 1
	v_mov_b32_dpp v16, v2 row_shl:8 row_mask:0xf bank_mask:0x3
	v_mov_b32_dpp v16, v2 row_shr:8 row_mask:0xf bank_mask:0xc
	s_waitcnt lgkmcnt(0)
	v_add_f32_e32 v2, v2, v16
	v_mov_b32_e32 v16, v2
	s_nop 1
	v_permlane16_swap_b32_e32 v16, v2
	s_waitcnt lgkmcnt(0)
	v_add_f32_e32 v2, v2, v16
	ds_bpermute_b32 v16, v151, v2
	s_and_saveexec_b64 s[10:11], s[42:43]
	s_cbranch_execz .LBB0_771
	v_mul_f32_e32 v18, 0x3a800000, v1
	s_waitcnt lgkmcnt(0)
	v_add_f32_e32 v1, v2, v16
	v_fmamk_f32 v1, v1, 0x3a800000, v241
	v_rsq_f32_e32 v19, v1
	s_add_i32 s3, s14, 0
	s_add_i32 s3, s3, 0x23868
	v_mov_b32_e32 v1, s3
	ds_write_b64 v1, v[18:19]
.LBB0_771:
	s_or_b64 exec, exec, s[10:11]
	v_lshlrev_b32_e32 v31, 16, v21
	v_and_b32_e32 v32, 0xffff0000, v21
	v_lshlrev_b32_e32 v17, 16, v22
	v_and_b32_e32 v33, 0xffff0000, v22
	v_lshlrev_b32_e32 v19, 16, v23
	v_and_b32_e32 v21, 0xffff0000, v23
	v_lshlrev_b32_e32 v23, 16, v13
	v_lshlrev_b32_e32 v22, 16, v12
	v_and_b32_e32 v13, 0xffff0000, v13
	v_and_b32_e32 v12, 0xffff0000, v12
	v_pk_add_f32 v[24:25], v[22:23], v[12:13]
	v_lshlrev_b32_e32 v2, 16, v20
	v_add_f32_e32 v1, v24, v25
	v_lshlrev_b32_e32 v25, 16, v15
	v_lshlrev_b32_e32 v24, 16, v14
	v_and_b32_e32 v15, 0xffff0000, v15
	v_and_b32_e32 v14, 0xffff0000, v14
	v_pk_add_f32 v[26:27], v[24:25], v[14:15]
	v_and_b32_e32 v30, 0xffff0000, v20
	v_pk_add_f32 v[26:27], v[26:27], v[26:27] op_sel:[0,1] op_sel_hi:[1,0]
	s_waitcnt lgkmcnt(0)
	v_add_f32_e32 v16, 0, v1
	v_add_f32_e32 v18, v2, v30
	v_add_f32_e32 v20, v31, v32
	v_mov_b32_e32 v27, v33
	v_pk_add_f32 v[26:27], v[16:17], v[26:27]
	v_pk_add_f32 v[28:29], v[18:19], v[20:21]
	s_nop 0
	v_pk_add_f32 v[26:27], v[26:27], v[28:29]
	s_nop 0
	v_add_f32_e32 v1, v26, v27
	s_nop 1
	v_mov_b32_dpp v16, v1 quad_perm:[1,0,3,2] row_mask:0xf bank_mask:0xf
	s_waitcnt lgkmcnt(0)
	v_add_f32_e32 v1, v1, v16
	s_nop 1
	v_mov_b32_dpp v16, v1 quad_perm:[2,3,0,1] row_mask:0xf bank_mask:0xf
	s_waitcnt lgkmcnt(0)
	v_add_f32_e32 v1, v1, v16
	s_nop 1
	v_mov_b32_dpp v16, v1 row_shl:4 row_mask:0xf bank_mask:0x5
	v_mov_b32_dpp v16, v1 row_shr:4 row_mask:0xf bank_mask:0xa
	s_waitcnt lgkmcnt(0)
	v_add_f32_e32 v1, v1, v16
	s_nop 1
	v_mov_b32_dpp v16, v1 row_shl:8 row_mask:0xf bank_mask:0x3
	v_mov_b32_dpp v16, v1 row_shr:8 row_mask:0xf bank_mask:0xc
	s_waitcnt lgkmcnt(0)
	v_add_f32_e32 v1, v1, v16
	v_mov_b32_e32 v16, v1
	s_nop 1
	v_permlane16_swap_b32_e32 v16, v1
	s_waitcnt lgkmcnt(0)
	v_add_f32_e32 v1, v1, v16
	v_mov_b32_e32 v16, v1
	s_nop 1
	v_permlane32_swap_b32_e32 v16, v1
	s_waitcnt lgkmcnt(0)
	v_add_f32_e32 v1, v1, v16
	v_fmac_f32_e32 v13, 0xba800000, v1
	v_fmac_f32_e32 v12, 0xba800000, v1
	v_fmac_f32_e32 v23, 0xba800000, v1
	v_fmac_f32_e32 v22, 0xba800000, v1
	v_mul_f32_e32 v12, v12, v12
	v_mul_f32_e32 v13, v13, v13
	v_fmac_f32_e32 v12, v22, v22
	v_fmac_f32_e32 v13, v23, v23
	v_fmac_f32_e32 v15, 0xba800000, v1
	v_fmac_f32_e32 v14, 0xba800000, v1
	v_add_f32_e32 v12, v12, v13
	v_fmac_f32_e32 v25, 0xba800000, v1
	v_fmac_f32_e32 v24, 0xba800000, v1
	v_mul_f32_e32 v13, v14, v14
	v_mul_f32_e32 v14, v15, v15
	v_fmac_f32_e32 v13, v24, v24
	v_fmac_f32_e32 v14, v25, v25
	v_add_f32_e32 v13, v13, v14
	v_fmac_f32_e32 v30, 0xba800000, v1
	v_add_f32_e32 v12, v12, v13
	v_fmac_f32_e32 v32, 0xba800000, v1
	v_fmac_f32_e32 v2, 0xba800000, v1
	v_mul_f32_e32 v13, v30, v30
	v_fmac_f32_e32 v31, 0xba800000, v1
	v_fmac_f32_e32 v13, v2, v2
	v_mul_f32_e32 v2, v32, v32
	v_fmac_f32_e32 v2, v31, v31
	v_add_f32_e32 v2, v13, v2
	v_fmac_f32_e32 v21, 0xba800000, v1
	v_fmac_f32_e32 v33, 0xba800000, v1
	v_add_f32_e32 v2, v12, v2
	v_fmac_f32_e32 v19, 0xba800000, v1
	v_fmac_f32_e32 v17, 0xba800000, v1
	v_mul_f32_e32 v12, v33, v33
	v_mul_f32_e32 v13, v21, v21
	v_fmac_f32_e32 v12, v17, v17
	v_fmac_f32_e32 v13, v19, v19
	v_add_f32_e32 v12, v12, v13
	v_add_f32_e32 v2, v2, v12
	s_nop 1
	v_mov_b32_dpp v12, v2 quad_perm:[1,0,3,2] row_mask:0xf bank_mask:0xf
	s_waitcnt lgkmcnt(0)
	v_add_f32_e32 v2, v2, v12
	s_nop 1
	v_mov_b32_dpp v12, v2 quad_perm:[2,3,0,1] row_mask:0xf bank_mask:0xf
	s_waitcnt lgkmcnt(0)
	v_add_f32_e32 v2, v2, v12
	s_nop 1
	v_mov_b32_dpp v12, v2 row_shl:4 row_mask:0xf bank_mask:0x5
	v_mov_b32_dpp v12, v2 row_shr:4 row_mask:0xf bank_mask:0xa
	s_waitcnt lgkmcnt(0)
	v_add_f32_e32 v2, v2, v12
	s_nop 1
	v_mov_b32_dpp v12, v2 row_shl:8 row_mask:0xf bank_mask:0x3
	v_mov_b32_dpp v12, v2 row_shr:8 row_mask:0xf bank_mask:0xc
	s_waitcnt lgkmcnt(0)
	v_add_f32_e32 v2, v2, v12
	v_mov_b32_e32 v12, v2
	s_nop 1
	v_permlane16_swap_b32_e32 v12, v2
	s_waitcnt lgkmcnt(0)
	v_add_f32_e32 v2, v2, v12
	ds_bpermute_b32 v12, v151, v2
	s_and_saveexec_b64 s[10:11], s[42:43]
	s_cbranch_execz .LBB0_773
	v_mul_f32_e32 v14, 0x3a800000, v1
	s_waitcnt lgkmcnt(0)
	v_add_f32_e32 v1, v2, v12
	v_fmamk_f32 v1, v1, 0x3a800000, v241
	v_rsq_f32_e32 v15, v1
	s_add_i32 s3, s14, 0
	s_add_i32 s3, s3, 0x23870
	v_mov_b32_e32 v1, s3
	ds_write_b64 v1, v[14:15]
.LBB0_773:
	s_or_b64 exec, exec, s[10:11]
	v_lshlrev_b32_e32 v15, 16, v5
	v_lshlrev_b32_e32 v14, 16, v4
	v_and_b32_e32 v5, 0xffff0000, v5
	v_and_b32_e32 v4, 0xffff0000, v4
	v_pk_add_f32 v[16:17], v[14:15], v[4:5]
	s_waitcnt vmcnt(0)
	v_lshlrev_b32_e32 v2, 16, v8
	v_add_f32_e32 v1, v16, v17
	v_lshlrev_b32_e32 v17, 16, v7
	v_lshlrev_b32_e32 v16, 16, v6
	v_and_b32_e32 v7, 0xffff0000, v7
	v_and_b32_e32 v6, 0xffff0000, v6
	v_pk_add_f32 v[18:19], v[16:17], v[6:7]
	v_and_b32_e32 v22, 0xffff0000, v8
	v_lshlrev_b32_e32 v23, 16, v9
	v_and_b32_e32 v24, 0xffff0000, v9
	v_and_b32_e32 v25, 0xffff0000, v10
	v_pk_add_f32 v[18:19], v[18:19], v[18:19] op_sel:[0,1] op_sel_hi:[1,0]
	v_lshlrev_b32_e32 v9, 16, v10
	v_lshlrev_b32_e32 v13, 16, v11
	v_and_b32_e32 v11, 0xffff0000, v11
	v_add_f32_e32 v8, 0, v1
	s_waitcnt lgkmcnt(0)
	v_add_f32_e32 v12, v2, v22
	v_add_f32_e32 v10, v23, v24
	v_mov_b32_e32 v19, v25
	v_pk_add_f32 v[18:19], v[8:9], v[18:19]
	v_pk_add_f32 v[20:21], v[12:13], v[10:11]
	s_nop 0
	v_pk_add_f32 v[18:19], v[18:19], v[20:21]
	s_nop 0
	v_add_f32_e32 v1, v18, v19
	s_nop 1
	v_mov_b32_dpp v8, v1 quad_perm:[1,0,3,2] row_mask:0xf bank_mask:0xf
	s_waitcnt lgkmcnt(0)
	v_add_f32_e32 v1, v1, v8
	s_nop 1
	v_mov_b32_dpp v8, v1 quad_perm:[2,3,0,1] row_mask:0xf bank_mask:0xf
	s_waitcnt lgkmcnt(0)
	v_add_f32_e32 v1, v1, v8
	s_nop 1
	v_mov_b32_dpp v8, v1 row_shl:4 row_mask:0xf bank_mask:0x5
	v_mov_b32_dpp v8, v1 row_shr:4 row_mask:0xf bank_mask:0xa
	s_waitcnt lgkmcnt(0)
	v_add_f32_e32 v1, v1, v8
	s_nop 1
	v_mov_b32_dpp v8, v1 row_shl:8 row_mask:0xf bank_mask:0x3
	v_mov_b32_dpp v8, v1 row_shr:8 row_mask:0xf bank_mask:0xc
	s_waitcnt lgkmcnt(0)
	v_add_f32_e32 v1, v1, v8
	v_mov_b32_e32 v8, v1
	s_nop 1
	v_permlane16_swap_b32_e32 v8, v1
	s_waitcnt lgkmcnt(0)
	v_add_f32_e32 v1, v1, v8
	v_mov_b32_e32 v8, v1
	s_nop 1
	v_permlane32_swap_b32_e32 v8, v1
	s_waitcnt lgkmcnt(0)
	v_add_f32_e32 v1, v1, v8
	v_fmac_f32_e32 v5, 0xba800000, v1
	v_fmac_f32_e32 v4, 0xba800000, v1
	v_fmac_f32_e32 v15, 0xba800000, v1
	v_fmac_f32_e32 v14, 0xba800000, v1
	v_mul_f32_e32 v4, v4, v4
	v_mul_f32_e32 v5, v5, v5
	v_fmac_f32_e32 v4, v14, v14
	v_fmac_f32_e32 v5, v15, v15
	v_fmac_f32_e32 v7, 0xba800000, v1
	v_fmac_f32_e32 v6, 0xba800000, v1
	v_add_f32_e32 v4, v4, v5
	v_fmac_f32_e32 v17, 0xba800000, v1
	v_fmac_f32_e32 v16, 0xba800000, v1
	v_mul_f32_e32 v5, v6, v6
	v_mul_f32_e32 v6, v7, v7
	v_fmac_f32_e32 v5, v16, v16
	v_fmac_f32_e32 v6, v17, v17
	v_add_f32_e32 v5, v5, v6
	v_fmac_f32_e32 v22, 0xba800000, v1
	v_add_f32_e32 v4, v4, v5
	v_fmac_f32_e32 v24, 0xba800000, v1
	v_fmac_f32_e32 v2, 0xba800000, v1
	v_mul_f32_e32 v5, v22, v22
	v_fmac_f32_e32 v23, 0xba800000, v1
	v_fmac_f32_e32 v5, v2, v2
	v_mul_f32_e32 v2, v24, v24
	v_fmac_f32_e32 v2, v23, v23
	v_add_f32_e32 v2, v5, v2
	v_fmac_f32_e32 v11, 0xba800000, v1
	v_fmac_f32_e32 v25, 0xba800000, v1
	v_add_f32_e32 v2, v4, v2
	v_fmac_f32_e32 v13, 0xba800000, v1
	v_fmac_f32_e32 v9, 0xba800000, v1
	v_mul_f32_e32 v4, v25, v25
	v_mul_f32_e32 v5, v11, v11
	v_fmac_f32_e32 v4, v9, v9
	v_fmac_f32_e32 v5, v13, v13
	v_add_f32_e32 v4, v4, v5
	v_add_f32_e32 v2, v2, v4
	s_nop 1
	v_mov_b32_dpp v4, v2 quad_perm:[1,0,3,2] row_mask:0xf bank_mask:0xf
	s_waitcnt lgkmcnt(0)
	v_add_f32_e32 v2, v2, v4
	s_nop 1
	v_mov_b32_dpp v4, v2 quad_perm:[2,3,0,1] row_mask:0xf bank_mask:0xf
	s_waitcnt lgkmcnt(0)
	v_add_f32_e32 v2, v2, v4
	s_nop 1
	v_mov_b32_dpp v4, v2 row_shl:4 row_mask:0xf bank_mask:0x5
	v_mov_b32_dpp v4, v2 row_shr:4 row_mask:0xf bank_mask:0xa
	s_waitcnt lgkmcnt(0)
	v_add_f32_e32 v2, v2, v4
	s_nop 1
	v_mov_b32_dpp v4, v2 row_shl:8 row_mask:0xf bank_mask:0x3
	v_mov_b32_dpp v4, v2 row_shr:8 row_mask:0xf bank_mask:0xc
	s_waitcnt lgkmcnt(0)
	v_add_f32_e32 v2, v2, v4
	v_mov_b32_e32 v4, v2
	s_nop 1
	v_permlane16_swap_b32_e32 v4, v2
	s_waitcnt lgkmcnt(0)
	v_add_f32_e32 v2, v2, v4
	ds_bpermute_b32 v4, v151, v2
	s_and_saveexec_b64 s[10:11], s[42:43]
	s_cbranch_execz .LBB0_775
	v_mul_f32_e32 v6, 0x3a800000, v1
	s_waitcnt lgkmcnt(0)
	v_add_f32_e32 v1, v2, v4
	v_fmamk_f32 v1, v1, 0x3a800000, v241
	v_rsq_f32_e32 v7, v1
	s_add_i32 s3, s14, 0
	s_add_i32 s3, s3, 0x23878
	v_mov_b32_e32 v1, s3
	ds_write_b64 v1, v[6:7]

.LBB0_1060:
	s_add_i32 s3, s14, -1
	v_and_or_b32 v2, s3, 62, v98
	v_lshlrev_b32_e32 v65, 2, v2
	ds_bpermute_b32 v2, v65, v1
	s_ashr_i32 s7, s6, 31
	ds_bpermute_b32 v52, v65, v93
	s_lshl_b64 s[10:11], s[6:7], 11
	v_lshl_add_u64 v[90:91], v[82:83], 0, s[10:11]
	s_waitcnt lgkmcnt(1)
	v_readfirstlane_b32 s10, v2
	s_ashr_i32 s11, s10, 31
	s_lshl_b64 s[10:11], s[10:11], 10
	ds_bpermute_b32 v2, v65, v95
	v_lshl_add_u64 v[48:49], v[80:81], 0, s[10:11]
	s_waitcnt lgkmcnt(1)
	v_readfirstlane_b32 s10, v52
	s_ashr_i32 s11, s10, 31
	global_load_dwordx4 v[48:51], v[48:49], off
	s_lshl_b64 s[10:11], s[10:11], 10
	v_lshl_add_u64 v[52:53], v[80:81], 0, s[10:11]
	global_load_dwordx4 v[52:55], v[52:53], off
	s_waitcnt lgkmcnt(0)
	v_readfirstlane_b32 s10, v2
	s_ashr_i32 s11, s10, 31
	global_load_dwordx4 v[40:43], v[90:91], off
	global_load_dwordx4 v[44:47], v[90:91], off offset:16
	s_lshl_b64 s[10:11], s[10:11], 10
	v_lshl_add_u64 v[56:57], v[80:81], 0, s[10:11]
	ds_bpermute_b32 v60, v65, v97
	global_load_dwordx4 v[56:59], v[56:57], off
	v_and_or_b32 v2, s14, 63, v98
	v_lshlrev_b32_e32 v105, 2, v2
	s_waitcnt vmcnt(5)
	ds_bpermute_b32 v2, v65, v36
	s_waitcnt lgkmcnt(1)
	v_readfirstlane_b32 s10, v60
	s_ashr_i32 s11, s10, 31
	s_lshl_b64 s[10:11], s[10:11], 10
	v_lshl_add_u64 v[60:61], v[80:81], 0, s[10:11]
	global_load_dwordx4 v[60:63], v[60:61], off
	ds_bpermute_b32 v64, v65, v37
	ds_bpermute_b32 v67, v105, v1
	ds_bpermute_b32 v66, v65, v38
	ds_bpermute_b32 v68, v65, v39
	ds_bpermute_b32 v69, v105, v93
	ds_bpermute_b32 v96, v105, v36
	s_waitcnt lgkmcnt(4)
	v_readfirstlane_b32 s10, v67
	s_ashr_i32 s11, s10, 31
	s_lshl_b64 s[10:11], s[10:11], 10
	v_lshl_add_u64 v[70:71], v[80:81], 0, s[10:11]
	s_waitcnt lgkmcnt(1)
	v_readfirstlane_b32 s10, v69
	s_ashr_i32 s11, s10, 31
	s_lshl_b64 s[10:11], s[10:11], 10
	ds_bpermute_b32 v94, v105, v37
	s_and_b64 vcc, exec, s[8:9]
	s_waitcnt vmcnt(5)
	v_cvt_pk_f32_fp8_e32 v[88:89], v48
	v_cvt_pk_f32_fp8_sdwa v[106:107], v48 src0_sel:WORD_1
	v_cvt_pk_f32_fp8_e32 v[108:109], v49
	v_cvt_pk_f32_fp8_sdwa v[48:49], v49 src0_sel:WORD_1
	v_cvt_pk_f32_fp8_e32 v[110:111], v50
	v_cvt_pk_f32_fp8_sdwa v[112:113], v50 src0_sel:WORD_1
	v_cvt_pk_f32_fp8_e32 v[114:115], v51
	v_cvt_pk_f32_fp8_sdwa v[50:51], v51 src0_sel:WORD_1
	s_waitcnt vmcnt(4)
	v_cvt_pk_f32_fp8_e32 v[116:117], v52
	v_cvt_pk_f32_fp8_sdwa v[118:119], v52 src0_sel:WORD_1
	v_cvt_pk_f32_fp8_e32 v[120:121], v53
	v_cvt_pk_f32_fp8_sdwa v[52:53], v53 src0_sel:WORD_1
	v_cvt_pk_f32_fp8_e32 v[122:123], v54
	v_cvt_pk_f32_fp8_sdwa v[124:125], v54 src0_sel:WORD_1
	v_cvt_pk_f32_fp8_e32 v[126:127], v55
	v_cvt_pk_f32_fp8_sdwa v[54:55], v55 src0_sel:WORD_1
	s_waitcnt vmcnt(3)
	v_lshlrev_b32_e32 v72, 16, v40
	v_and_b32_e32 v73, 0xffff0000, v40
	v_lshlrev_b32_e32 v40, 16, v41
	v_and_b32_e32 v41, 0xffff0000, v41
	v_lshlrev_b32_e32 v74, 16, v42
	v_and_b32_e32 v75, 0xffff0000, v42
	v_lshlrev_b32_e32 v42, 16, v43
	v_and_b32_e32 v43, 0xffff0000, v43
	s_waitcnt vmcnt(2)
	v_lshlrev_b32_e32 v76, 16, v44
	v_and_b32_e32 v77, 0xffff0000, v44
	v_lshlrev_b32_e32 v44, 16, v45
	v_and_b32_e32 v45, 0xffff0000, v45
	v_lshlrev_b32_e32 v78, 16, v46
	v_and_b32_e32 v79, 0xffff0000, v46
	v_lshlrev_b32_e32 v46, 16, v47
	v_and_b32_e32 v47, 0xffff0000, v47
	v_pk_mul_f32 v[106:107], v[2:3], v[106:107] op_sel_hi:[0,1]
	v_pk_mul_f32 v[88:89], v[2:3], v[88:89] op_sel_hi:[0,1]
	v_pk_mul_f32 v[48:49], v[2:3], v[48:49] op_sel_hi:[0,1]
	v_pk_mul_f32 v[108:109], v[2:3], v[108:109] op_sel_hi:[0,1]
	v_pk_mul_f32 v[112:113], v[2:3], v[112:113] op_sel_hi:[0,1]
	v_pk_mul_f32 v[110:111], v[2:3], v[110:111] op_sel_hi:[0,1]
	v_pk_mul_f32 v[50:51], v[2:3], v[50:51] op_sel_hi:[0,1]
	v_pk_mul_f32 v[114:115], v[2:3], v[114:115] op_sel_hi:[0,1]
	v_pk_fma_f32 v[72:73], v[72:73], s[92:93], v[88:89] op_sel_hi:[1,0,1]
	v_pk_fma_f32 v[40:41], v[40:41], s[92:93], v[106:107] op_sel_hi:[1,0,1]
	v_pk_fma_f32 v[74:75], v[74:75], s[92:93], v[108:109] op_sel_hi:[1,0,1]
	v_pk_fma_f32 v[42:43], v[42:43], s[92:93], v[48:49] op_sel_hi:[1,0,1]
	v_pk_fma_f32 v[48:49], v[76:77], s[92:93], v[110:111] op_sel_hi:[1,0,1]
	v_pk_fma_f32 v[44:45], v[44:45], s[92:93], v[112:113] op_sel_hi:[1,0,1]
	v_pk_fma_f32 v[76:77], v[78:79], s[92:93], v[114:115] op_sel_hi:[1,0,1]
	v_pk_fma_f32 v[46:47], v[46:47], s[92:93], v[50:51] op_sel_hi:[1,0,1]
	v_pk_fma_f32 v[40:41], v[64:65], v[118:119], v[40:41] op_sel_hi:[0,1,1]
	v_pk_fma_f32 v[50:51], v[64:65], v[116:117], v[72:73] op_sel_hi:[0,1,1]
	v_pk_fma_f32 v[42:43], v[64:65], v[52:53], v[42:43] op_sel_hi:[0,1,1]
	v_pk_fma_f32 v[52:53], v[64:65], v[120:121], v[74:75] op_sel_hi:[0,1,1]
	v_pk_fma_f32 v[44:45], v[64:65], v[124:125], v[44:45] op_sel_hi:[0,1,1]
	v_pk_fma_f32 v[48:49], v[64:65], v[122:123], v[48:49] op_sel_hi:[0,1,1]
	v_pk_fma_f32 v[46:47], v[64:65], v[54:55], v[46:47] op_sel_hi:[0,1,1]
	v_pk_fma_f32 v[54:55], v[64:65], v[126:127], v[76:77] op_sel_hi:[0,1,1]
	s_waitcnt vmcnt(1)
	v_cvt_pk_f32_fp8_e32 v[64:65], v56
	v_cvt_pk_f32_fp8_sdwa v[72:73], v56 src0_sel:WORD_1
	v_cvt_pk_f32_fp8_e32 v[74:75], v57
	v_cvt_pk_f32_fp8_sdwa v[56:57], v57 src0_sel:WORD_1
	v_pk_fma_f32 v[50:51], v[66:67], v[64:65], v[50:51] op_sel_hi:[0,1,1]
	v_cvt_pk_f32_fp8_sdwa v[64:65], v58 src0_sel:WORD_1
	v_pk_fma_f32 v[40:41], v[66:67], v[72:73], v[40:41] op_sel_hi:[0,1,1]
	v_pk_fma_f32 v[42:43], v[66:67], v[56:57], v[42:43] op_sel_hi:[0,1,1]
	v_cvt_pk_f32_fp8_e32 v[56:57], v58
	v_cvt_pk_f32_fp8_e32 v[72:73], v59
	v_cvt_pk_f32_fp8_sdwa v[58:59], v59 src0_sel:WORD_1
	v_pk_fma_f32 v[44:45], v[66:67], v[64:65], v[44:45] op_sel_hi:[0,1,1]
	v_pk_fma_f32 v[48:49], v[66:67], v[56:57], v[48:49] op_sel_hi:[0,1,1]
	s_waitcnt vmcnt(0)
	v_cvt_pk_f32_fp8_sdwa v[56:57], v60 src0_sel:WORD_1
	v_cvt_pk_f32_fp8_sdwa v[64:65], v61 src0_sel:WORD_1
	v_pk_fma_f32 v[46:47], v[66:67], v[58:59], v[46:47] op_sel_hi:[0,1,1]
	v_cvt_pk_f32_fp8_e32 v[58:59], v60
	v_cvt_pk_f32_fp8_e32 v[60:61], v61
	v_pk_fma_f32 v[52:53], v[66:67], v[74:75], v[52:53] op_sel_hi:[0,1,1]
	v_pk_fma_f32 v[54:55], v[66:67], v[72:73], v[54:55] op_sel_hi:[0,1,1]
	v_pk_fma_f32 v[66:67], v[68:69], v[56:57], v[40:41] op_sel_hi:[0,1,1]
	v_pk_fma_f32 v[74:75], v[68:69], v[64:65], v[42:43] op_sel_hi:[0,1,1]
	v_cvt_pk_f32_fp8_sdwa v[40:41], v62 src0_sel:WORD_1
	v_cvt_pk_f32_fp8_e32 v[42:43], v62
	v_pk_fma_f32 v[72:73], v[68:69], v[58:59], v[50:51] op_sel_hi:[0,1,1]
	v_pk_fma_f32 v[76:77], v[68:69], v[60:61], v[52:53] op_sel_hi:[0,1,1]
	v_cvt_pk_f32_fp8_sdwa v[50:51], v63 src0_sel:WORD_1
	v_cvt_pk_f32_fp8_e32 v[52:53], v63
	v_pk_fma_f32 v[78:79], v[68:69], v[40:41], v[44:45] op_sel_hi:[0,1,1]
	v_pk_fma_f32 v[106:107], v[68:69], v[42:43], v[48:49] op_sel_hi:[0,1,1]
	v_pk_mov_b32 v[40:41], v[72:73], v[66:67] op_sel:[1,0]
	v_mov_b32_e32 v42, v72
	v_mov_b32_e32 v43, v67
	v_pk_add_f32 v[40:41], v[40:41], v[42:43]
	v_pk_mov_b32 v[42:43], v[76:77], v[74:75] op_sel:[1,0]
	v_mov_b32_e32 v44, v76
	v_mov_b32_e32 v45, v75
	v_pk_add_f32 v[42:43], v[42:43], v[44:45]
	v_pk_fma_f32 v[108:109], v[68:69], v[50:51], v[46:47] op_sel_hi:[0,1,1]
	v_pk_fma_f32 v[110:111], v[68:69], v[52:53], v[54:55] op_sel_hi:[0,1,1]
	v_add_f32_e32 v2, v40, v41
	v_pk_add_f32 v[42:43], v[42:43], v[42:43] op_sel:[0,1] op_sel_hi:[1,0]
	v_add_f32_e32 v40, 0, v2
	v_add_f32_e32 v44, v106, v107
	v_add_f32_e32 v46, v78, v79
	v_mov_b32_e32 v41, v110
	v_mov_b32_e32 v43, v111
	v_mov_b32_e32 v45, v108
	v_mov_b32_e32 v47, v109
	v_pk_add_f32 v[40:41], v[40:41], v[42:43]
	v_pk_add_f32 v[42:43], v[44:45], v[46:47]
	s_nop 0
	v_pk_add_f32 v[40:41], v[40:41], v[42:43]
	ds_bpermute_b32 v42, v105, v95
	v_add_f32_e32 v2, v40, v41
	s_nop 1
	v_mov_b32_dpp v40, v2 quad_perm:[1,0,3,2] row_mask:0xf bank_mask:0xf
	s_waitcnt lgkmcnt(0)
	v_add_f32_e32 v2, v2, v40
	s_nop 1
	v_mov_b32_dpp v43, v2 quad_perm:[2,3,0,1] row_mask:0xf bank_mask:0xf
	v_lshl_add_u64 v[40:41], v[80:81], 0, s[10:11]
	v_readfirstlane_b32 s10, v42
	s_ashr_i32 s11, s10, 31
	s_lshl_b64 s[10:11], s[10:11], 10
	s_waitcnt lgkmcnt(0)
	v_add_f32_e32 v2, v2, v43
	s_nop 1
	v_mov_b32_dpp v42, v2 row_shl:4 row_mask:0xf bank_mask:0x5
	v_mov_b32_dpp v42, v2 row_shr:4 row_mask:0xf bank_mask:0xa
	ds_bpermute_b32 v43, v105, v97
	global_load_dwordx4 v[52:55], v[70:71], off
	global_load_dwordx4 v[48:51], v[40:41], off
	v_lshl_add_u64 v[40:41], v[80:81], 0, s[10:11]
	s_waitcnt lgkmcnt(1)
	v_add_f32_e32 v2, v2, v42
	s_nop 1
	v_mov_b32_dpp v44, v2 row_shl:8 row_mask:0xf bank_mask:0x3
	v_mov_b32_dpp v44, v2 row_shr:8 row_mask:0xf bank_mask:0xc
	s_waitcnt lgkmcnt(0)
	v_readfirstlane_b32 s10, v43
	s_ashr_i32 s11, s10, 31
	s_lshl_b64 s[10:11], s[10:11], 10
	v_lshl_add_u64 v[42:43], v[80:81], 0, s[10:11]
	s_waitcnt lgkmcnt(0)
	v_add_f32_e32 v2, v2, v44
	ds_bpermute_b32 v56, v103, v2
	s_add_i32 s10, s89, s6
	s_ashr_i32 s11, s10, 31
	s_lshl_b64 s[12:13], s[10:11], 11
	v_lshl_add_u64 v[88:89], v[82:83], 0, s[12:13]
	global_load_dwordx4 v[44:47], v[40:41], off
	s_nop 0
	global_load_dwordx4 v[40:43], v[42:43], off
	s_waitcnt lgkmcnt(0)
	v_add_f32_e32 v2, v2, v56
	global_load_dwordx4 v[56:59], v[88:89], off offset:16
	global_load_dwordx4 v[60:63], v[88:89], off
	ds_bpermute_b32 v64, v104, v2
	s_mov_b64 s[12:13], -1
	s_waitcnt lgkmcnt(0)
	v_add_f32_e32 v92, v2, v64
	v_fmamk_f32 v73, v92, 0xba800000, v73
	v_fmac_f32_e32 v72, 0xba800000, v92
	v_fmamk_f32 v67, v92, 0xba800000, v67
	v_fmac_f32_e32 v66, 0xba800000, v92
	v_pk_mul_f32 v[64:65], v[66:67], v[66:67]
	v_pk_mul_f32 v[68:69], v[72:73], v[72:73]
	v_fmamk_f32 v77, v92, 0xba800000, v77
	v_pk_mov_b32 v[70:71], v[68:69], v[64:65] op_sel:[1,0]
	v_mov_b32_e32 v69, v65
	v_fmac_f32_e32 v76, 0xba800000, v92
	v_fmamk_f32 v75, v92, 0xba800000, v75
	v_fmac_f32_e32 v74, 0xba800000, v92
	v_pk_add_f32 v[64:65], v[70:71], v[68:69]
	v_pk_mul_f32 v[68:69], v[74:75], v[74:75]
	v_pk_mul_f32 v[70:71], v[76:77], v[76:77]
	v_fmac_f32_e32 v106, 0xba800000, v92
	v_pk_mov_b32 v[112:113], v[70:71], v[68:69] op_sel:[1,0]
	v_mov_b32_e32 v71, v69
	v_fmamk_f32 v107, v92, 0xba800000, v107
	v_fmac_f32_e32 v78, 0xba800000, v92
	v_mul_f32_e32 v2, v106, v106
	v_pk_add_f32 v[68:69], v[112:113], v[70:71]
	v_fmamk_f32 v79, v92, 0xba800000, v79
	v_pk_fma_f32 v[70:71], v[106:107], v[106:107], v[2:3] op_sel_hi:[1,1,0]
	v_mul_f32_e32 v2, v78, v78
	v_pk_add_f32 v[64:65], v[64:65], v[64:65] op_sel_hi:[0,1]
	v_pk_add_f32 v[68:69], v[68:69], v[68:69] op_sel_hi:[0,1]
	v_pk_fma_f32 v[112:113], v[78:79], v[78:79], v[2:3] op_sel_hi:[1,1,0]
	v_fmamk_f32 v109, v92, 0xba800000, v109
	v_fmac_f32_e32 v108, 0xba800000, v92
	v_fmamk_f32 v111, v92, 0xba800000, v111
	v_fmac_f32_e32 v110, 0xba800000, v92
	v_mul_f32_e32 v70, v110, v110
	v_mul_f32_e32 v112, v111, v111
	v_mul_f32_e32 v64, v108, v108
	v_mul_f32_e32 v68, v109, v109
	v_pk_add_f32 v[70:71], v[70:71], v[112:113]
	v_pk_add_f32 v[64:65], v[64:65], v[68:69]
	ds_bpermute_b32 v92, v105, v38
	v_pk_add_f32 v[64:65], v[70:71], v[64:65]
	s_nop 0
	v_add_f32_e32 v2, v64, v65
	s_nop 1
	v_mov_b32_dpp v64, v2 quad_perm:[1,0,3,2] row_mask:0xf bank_mask:0xf
	s_waitcnt lgkmcnt(0)
	v_add_f32_e32 v2, v2, v64
	s_nop 1
	v_mov_b32_dpp v64, v2 quad_perm:[2,3,0,1] row_mask:0xf bank_mask:0xf
	s_waitcnt lgkmcnt(0)
	v_add_f32_e32 v2, v2, v64
	s_nop 1
	v_mov_b32_dpp v64, v2 row_shl:4 row_mask:0xf bank_mask:0x5
	v_mov_b32_dpp v64, v2 row_shr:4 row_mask:0xf bank_mask:0xa
	s_waitcnt lgkmcnt(0)
	v_add_f32_e32 v2, v2, v64
	s_nop 1
	v_mov_b32_dpp v64, v2 row_shl:8 row_mask:0xf bank_mask:0x3
	v_mov_b32_dpp v64, v2 row_shr:8 row_mask:0xf bank_mask:0xc
	s_waitcnt lgkmcnt(0)
	v_add_f32_e32 v2, v2, v64
	ds_bpermute_b32 v64, v103, v2
	s_waitcnt lgkmcnt(0)
	v_add_f32_e32 v2, v2, v64
	ds_bpermute_b32 v64, v104, v2
	s_waitcnt lgkmcnt(0)
	v_add_f32_e32 v2, v2, v64
	v_fmamk_f32 v2, v2, 0x3a800000, v241
	v_rsq_f32_e32 v112, v2
	ds_bpermute_b32 v2, v105, v39
	v_pk_mul_f32 v[64:65], v[72:73], v[112:113] op_sel_hi:[1,0]
	v_pk_mul_f32 v[66:67], v[66:67], v[112:113] op_sel_hi:[1,0]
	v_pk_mul_f32 v[68:69], v[76:77], v[112:113] op_sel_hi:[1,0]
	v_pk_mul_f32 v[70:71], v[74:75], v[112:113] op_sel_hi:[1,0]
	v_pk_mul_f32 v[72:73], v[106:107], v[112:113] op_sel_hi:[1,0]
	v_pk_mul_f32 v[74:75], v[78:79], v[112:113] op_sel_hi:[1,0]
	v_pk_mul_f32 v[76:77], v[110:111], v[112:113] op_sel_hi:[1,0]
	v_pk_mul_f32 v[78:79], v[108:109], v[112:113] op_sel_hi:[1,0]
	v_pk_fma_f32 v[66:67], v[18:19], v[66:67], v[34:35]
	v_pk_fma_f32 v[64:65], v[16:17], v[64:65], v[32:33]
	v_pk_fma_f32 v[70:71], v[14:15], v[70:71], v[30:31]
	v_pk_fma_f32 v[68:69], v[12:13], v[68:69], v[28:29]
	v_pk_fma_f32 v[74:75], v[10:11], v[74:75], v[26:27]
	v_pk_fma_f32 v[72:73], v[8:9], v[72:73], v[24:25]
	v_pk_fma_f32 v[78:79], v[6:7], v[78:79], v[22:23]
	v_pk_fma_f32 v[76:77], v[4:5], v[76:77], v[20:21]
	s_cbranch_vccz .LBB0_1062
	v_cvt_pk_bf16_f32 v106, v64, v65
	v_cvt_pk_bf16_f32 v107, v66, v67
	v_cvt_pk_bf16_f32 v108, v68, v69
	v_cvt_pk_bf16_f32 v109, v70, v71
	v_cvt_pk_bf16_f32 v110, v72, v73
	v_cvt_pk_bf16_f32 v111, v74, v75
	v_cvt_pk_bf16_f32 v112, v76, v77
	v_cvt_pk_bf16_f32 v113, v78, v79
	global_store_dwordx4 v[90:91], v[106:109], off
	global_store_dwordx4 v[90:91], v[110:113], off offset:16
	s_lshl_b64 s[12:13], s[6:7], 10
	v_mov_b32_e32 v106, v3
	v_mov_b32_e32 v107, v3
	v_mov_b32_e32 v108, v3
	v_mov_b32_e32 v109, v3
	v_cvt_pk_fp8_f32 v106, v64, v65
	v_cvt_pk_fp8_f32 v107, v68, v69
	v_cvt_pk_fp8_f32 v108, v72, v73
	v_cvt_pk_fp8_f32 v109, v76, v77
	v_cvt_pk_fp8_f32 v106, v66, v67 op_sel:[0,0,1]
	v_cvt_pk_fp8_f32 v107, v70, v71 op_sel:[0,0,1]
	v_cvt_pk_fp8_f32 v108, v74, v75 op_sel:[0,0,1]
	v_cvt_pk_fp8_f32 v109, v78, v79 op_sel:[0,0,1]
	v_lshl_add_u64 v[90:91], v[84:85], 0, s[12:13]
	s_mov_b64 s[12:13], 0
	global_store_dwordx4 v[90:91], v[106:109], off

.LBB0_1064:
	s_waitcnt vmcnt(5)
	v_cvt_pk_f32_fp8_e32 v[74:75], v52
	s_waitcnt vmcnt(0)
	v_lshlrev_b32_e32 v64, 16, v60
	v_and_b32_e32 v65, 0xffff0000, v60
	v_cvt_pk_f32_fp8_sdwa v[72:73], v52 src0_sel:WORD_1
	v_pk_mul_f32 v[74:75], v[96:97], v[74:75] op_sel_hi:[0,1]
	v_cvt_pk_f32_fp8_sdwa v[76:77], v53 src0_sel:WORD_1
	v_cvt_pk_f32_fp8_e32 v[52:53], v53
	v_pk_fma_f32 v[64:65], v[64:65], s[92:93], v[74:75] op_sel_hi:[1,0,1]
	v_cvt_pk_f32_fp8_sdwa v[74:75], v54 src0_sel:WORD_1
	v_lshlrev_b32_e32 v60, 16, v61
	v_and_b32_e32 v61, 0xffff0000, v61
	v_lshlrev_b32_e32 v66, 16, v62
	v_and_b32_e32 v67, 0xffff0000, v62
	v_pk_mul_f32 v[72:73], v[96:97], v[72:73] op_sel_hi:[0,1]
	v_pk_mul_f32 v[52:53], v[96:97], v[52:53] op_sel_hi:[0,1]
	v_pk_fma_f32 v[60:61], v[60:61], s[92:93], v[72:73] op_sel_hi:[1,0,1]
	v_pk_mul_f32 v[72:73], v[96:97], v[76:77] op_sel_hi:[0,1]
	v_cvt_pk_f32_fp8_e32 v[76:77], v54
	v_pk_fma_f32 v[52:53], v[66:67], s[92:93], v[52:53] op_sel_hi:[1,0,1]
	v_pk_mul_f32 v[66:67], v[96:97], v[74:75] op_sel_hi:[0,1]
	v_cvt_pk_f32_fp8_sdwa v[74:75], v55 src0_sel:WORD_1
	v_cvt_pk_f32_fp8_e32 v[54:55], v55
	v_lshlrev_b32_e32 v62, 16, v63
	v_and_b32_e32 v63, 0xffff0000, v63
	v_lshlrev_b32_e32 v68, 16, v56
	v_and_b32_e32 v69, 0xffff0000, v56
	v_lshlrev_b32_e32 v56, 16, v57
	v_and_b32_e32 v57, 0xffff0000, v57
	v_lshlrev_b32_e32 v70, 16, v58
	v_and_b32_e32 v71, 0xffff0000, v58
	v_lshlrev_b32_e32 v58, 16, v59
	v_and_b32_e32 v59, 0xffff0000, v59
	v_pk_fma_f32 v[62:63], v[62:63], s[92:93], v[72:73] op_sel_hi:[1,0,1]
	v_pk_mul_f32 v[72:73], v[96:97], v[76:77] op_sel_hi:[0,1]
	v_pk_fma_f32 v[56:57], v[56:57], s[92:93], v[66:67] op_sel_hi:[1,0,1]
	v_pk_mul_f32 v[66:67], v[96:97], v[74:75] op_sel_hi:[0,1]
	v_pk_mul_f32 v[54:55], v[96:97], v[54:55] op_sel_hi:[0,1]
	v_pk_fma_f32 v[68:69], v[68:69], s[92:93], v[72:73] op_sel_hi:[1,0,1]
	v_pk_fma_f32 v[54:55], v[70:71], s[92:93], v[54:55] op_sel_hi:[1,0,1]
	v_pk_fma_f32 v[58:59], v[58:59], s[92:93], v[66:67] op_sel_hi:[1,0,1]
	v_cvt_pk_f32_fp8_sdwa v[66:67], v48 src0_sel:WORD_1
	v_cvt_pk_f32_fp8_e32 v[70:71], v48
	v_cvt_pk_f32_fp8_sdwa v[72:73], v49 src0_sel:WORD_1
	v_cvt_pk_f32_fp8_e32 v[48:49], v49
	v_pk_fma_f32 v[60:61], v[94:95], v[66:67], v[60:61] op_sel_hi:[0,1,1]
	v_pk_fma_f32 v[64:65], v[94:95], v[70:71], v[64:65] op_sel_hi:[0,1,1]
	v_cvt_pk_f32_fp8_e32 v[66:67], v50
	v_pk_fma_f32 v[48:49], v[94:95], v[48:49], v[52:53] op_sel_hi:[0,1,1]
	v_cvt_pk_f32_fp8_sdwa v[52:53], v50 src0_sel:WORD_1
	v_cvt_pk_f32_fp8_sdwa v[70:71], v51 src0_sel:WORD_1
	v_cvt_pk_f32_fp8_e32 v[50:51], v51
	v_pk_fma_f32 v[62:63], v[94:95], v[72:73], v[62:63] op_sel_hi:[0,1,1]
	v_pk_fma_f32 v[52:53], v[94:95], v[52:53], v[56:57] op_sel_hi:[0,1,1]
	v_pk_fma_f32 v[56:57], v[94:95], v[66:67], v[68:69] op_sel_hi:[0,1,1]
	v_pk_fma_f32 v[50:51], v[94:95], v[50:51], v[54:55] op_sel_hi:[0,1,1]
	v_cvt_pk_f32_fp8_e32 v[54:55], v44
	v_cvt_pk_f32_fp8_sdwa v[66:67], v44 src0_sel:WORD_1
	v_cvt_pk_f32_fp8_e32 v[68:69], v45
	v_cvt_pk_f32_fp8_sdwa v[44:45], v45 src0_sel:WORD_1
	v_pk_fma_f32 v[54:55], v[92:93], v[54:55], v[64:65] op_sel_hi:[0,1,1]
	v_pk_fma_f32 v[60:61], v[92:93], v[66:67], v[60:61] op_sel_hi:[0,1,1]
	v_cvt_pk_f32_fp8_sdwa v[64:65], v46 src0_sel:WORD_1
	v_pk_fma_f32 v[44:45], v[92:93], v[44:45], v[62:63] op_sel_hi:[0,1,1]
	v_cvt_pk_f32_fp8_e32 v[62:63], v46
	v_cvt_pk_f32_fp8_e32 v[66:67], v47
	v_cvt_pk_f32_fp8_sdwa v[46:47], v47 src0_sel:WORD_1
	v_pk_fma_f32 v[58:59], v[94:95], v[70:71], v[58:59] op_sel_hi:[0,1,1]
	v_pk_fma_f32 v[56:57], v[92:93], v[62:63], v[56:57] op_sel_hi:[0,1,1]
	v_pk_fma_f32 v[52:53], v[92:93], v[64:65], v[52:53] op_sel_hi:[0,1,1]
	v_pk_fma_f32 v[46:47], v[92:93], v[46:47], v[58:59] op_sel_hi:[0,1,1]
	v_cvt_pk_f32_fp8_sdwa v[58:59], v40 src0_sel:WORD_1
	v_cvt_pk_f32_fp8_e32 v[62:63], v40
	v_cvt_pk_f32_fp8_sdwa v[64:65], v41 src0_sel:WORD_1
	v_cvt_pk_f32_fp8_e32 v[40:41], v41
	v_pk_fma_f32 v[48:49], v[92:93], v[68:69], v[48:49] op_sel_hi:[0,1,1]
	s_waitcnt lgkmcnt(0)
	v_pk_fma_f32 v[58:59], v[2:3], v[58:59], v[60:61] op_sel_hi:[0,1,1]
	v_pk_fma_f32 v[54:55], v[2:3], v[62:63], v[54:55] op_sel_hi:[0,1,1]
	v_pk_fma_f32 v[48:49], v[2:3], v[40:41], v[48:49] op_sel_hi:[0,1,1]
	v_cvt_pk_f32_fp8_sdwa v[40:41], v42 src0_sel:WORD_1
	v_cvt_pk_f32_fp8_e32 v[60:61], v42
	v_cvt_pk_f32_fp8_sdwa v[62:63], v43 src0_sel:WORD_1
	v_cvt_pk_f32_fp8_e32 v[42:43], v43
	v_pk_fma_f32 v[50:51], v[92:93], v[66:67], v[50:51] op_sel_hi:[0,1,1]
	v_pk_fma_f32 v[44:45], v[2:3], v[64:65], v[44:45] op_sel_hi:[0,1,1]
	v_pk_fma_f32 v[52:53], v[2:3], v[40:41], v[52:53] op_sel_hi:[0,1,1]
	v_pk_fma_f32 v[56:57], v[2:3], v[60:61], v[56:57] op_sel_hi:[0,1,1]
	v_pk_fma_f32 v[60:61], v[2:3], v[62:63], v[46:47] op_sel_hi:[0,1,1]
	v_pk_fma_f32 v[62:63], v[2:3], v[42:43], v[50:51] op_sel_hi:[0,1,1]
	v_pk_mov_b32 v[40:41], v[54:55], v[58:59] op_sel:[1,0]
	v_mov_b32_e32 v42, v54
	v_mov_b32_e32 v43, v59
	v_pk_add_f32 v[40:41], v[40:41], v[42:43]
	v_pk_mov_b32 v[42:43], v[48:49], v[44:45] op_sel:[1,0]
	v_mov_b32_e32 v46, v48
	v_mov_b32_e32 v47, v45
	v_pk_add_f32 v[42:43], v[42:43], v[46:47]
	v_add_f32_e32 v2, v40, v41
	v_pk_add_f32 v[42:43], v[42:43], v[42:43] op_sel:[0,1] op_sel_hi:[1,0]
	v_add_f32_e32 v40, 0, v2
	v_add_f32_e32 v46, v56, v57
	v_add_f32_e32 v50, v52, v53
	v_mov_b32_e32 v41, v62
	v_mov_b32_e32 v43, v63
	v_mov_b32_e32 v47, v60
	v_mov_b32_e32 v51, v61
	v_pk_add_f32 v[40:41], v[40:41], v[42:43]
	v_pk_add_f32 v[42:43], v[46:47], v[50:51]
	s_andn2_b64 vcc, exec, s[8:9]
	v_pk_add_f32 v[40:41], v[40:41], v[42:43]
	s_mov_b64 s[12:13], -1
	v_add_f32_e32 v2, v40, v41
	s_nop 1
	v_mov_b32_dpp v40, v2 quad_perm:[1,0,3,2] row_mask:0xf bank_mask:0xf
	s_waitcnt lgkmcnt(0)
	v_add_f32_e32 v2, v2, v40
	s_nop 1
	v_mov_b32_dpp v40, v2 quad_perm:[2,3,0,1] row_mask:0xf bank_mask:0xf
	s_waitcnt lgkmcnt(0)
	v_add_f32_e32 v2, v2, v40
	s_nop 1
	v_mov_b32_dpp v40, v2 row_shl:4 row_mask:0xf bank_mask:0x5
	v_mov_b32_dpp v40, v2 row_shr:4 row_mask:0xf bank_mask:0xa
	s_waitcnt lgkmcnt(0)
	v_add_f32_e32 v2, v2, v40
	s_nop 1
	v_mov_b32_dpp v40, v2 row_shl:8 row_mask:0xf bank_mask:0x3
	v_mov_b32_dpp v40, v2 row_shr:8 row_mask:0xf bank_mask:0xc
	s_waitcnt lgkmcnt(0)
	v_add_f32_e32 v2, v2, v40
	ds_bpermute_b32 v40, v103, v2
	s_waitcnt lgkmcnt(0)
	v_add_f32_e32 v2, v2, v40
	ds_bpermute_b32 v40, v104, v2
	s_waitcnt lgkmcnt(0)
	v_add_f32_e32 v64, v2, v40
	v_fmamk_f32 v55, v64, 0xba800000, v55
	v_fmac_f32_e32 v54, 0xba800000, v64
	v_fmamk_f32 v59, v64, 0xba800000, v59
	v_fmac_f32_e32 v58, 0xba800000, v64
	v_pk_mul_f32 v[40:41], v[58:59], v[58:59]
	v_pk_mul_f32 v[42:43], v[54:55], v[54:55]
	v_fmamk_f32 v49, v64, 0xba800000, v49
	v_pk_mov_b32 v[46:47], v[42:43], v[40:41] op_sel:[1,0]
	v_mov_b32_e32 v43, v41
	v_fmac_f32_e32 v48, 0xba800000, v64
	v_fmamk_f32 v45, v64, 0xba800000, v45
	v_fmac_f32_e32 v44, 0xba800000, v64
	v_pk_add_f32 v[40:41], v[46:47], v[42:43]
	v_pk_mul_f32 v[42:43], v[44:45], v[44:45]
	v_pk_mul_f32 v[46:47], v[48:49], v[48:49]
	v_fmac_f32_e32 v56, 0xba800000, v64
	v_pk_mov_b32 v[50:51], v[46:47], v[42:43] op_sel:[1,0]
	v_mov_b32_e32 v47, v43
	v_fmamk_f32 v57, v64, 0xba800000, v57
	v_fmac_f32_e32 v52, 0xba800000, v64
	v_mul_f32_e32 v2, v56, v56
	v_pk_add_f32 v[42:43], v[50:51], v[46:47]
	v_fmamk_f32 v53, v64, 0xba800000, v53
	v_pk_fma_f32 v[46:47], v[56:57], v[56:57], v[2:3] op_sel_hi:[1,1,0]
	v_mul_f32_e32 v2, v52, v52
	v_pk_add_f32 v[40:41], v[40:41], v[40:41] op_sel_hi:[0,1]
	v_pk_add_f32 v[42:43], v[42:43], v[42:43] op_sel_hi:[0,1]
	v_pk_fma_f32 v[50:51], v[52:53], v[52:53], v[2:3] op_sel_hi:[1,1,0]
	v_fmamk_f32 v61, v64, 0xba800000, v61
	v_fmac_f32_e32 v60, 0xba800000, v64
	v_fmamk_f32 v63, v64, 0xba800000, v63
	v_fmac_f32_e32 v62, 0xba800000, v64
	v_mul_f32_e32 v46, v62, v62
	v_mul_f32_e32 v50, v63, v63
	v_mul_f32_e32 v40, v60, v60
	v_mul_f32_e32 v42, v61, v61
	v_pk_add_f32 v[46:47], v[46:47], v[50:51]
	v_pk_add_f32 v[40:41], v[40:41], v[42:43]
	s_nop 0
	v_pk_add_f32 v[40:41], v[46:47], v[40:41]
	s_nop 0
	v_add_f32_e32 v2, v40, v41
	s_nop 1
	v_mov_b32_dpp v40, v2 quad_perm:[1,0,3,2] row_mask:0xf bank_mask:0xf
	s_waitcnt lgkmcnt(0)
	v_add_f32_e32 v2, v2, v40
	s_nop 1
	v_mov_b32_dpp v40, v2 quad_perm:[2,3,0,1] row_mask:0xf bank_mask:0xf
	s_waitcnt lgkmcnt(0)
	v_add_f32_e32 v2, v2, v40
	s_nop 1
	v_mov_b32_dpp v40, v2 row_shl:4 row_mask:0xf bank_mask:0x5
	v_mov_b32_dpp v40, v2 row_shr:4 row_mask:0xf bank_mask:0xa
	s_waitcnt lgkmcnt(0)
	v_add_f32_e32 v2, v2, v40
	s_nop 1
	v_mov_b32_dpp v40, v2 row_shl:8 row_mask:0xf bank_mask:0x3
	v_mov_b32_dpp v40, v2 row_shr:8 row_mask:0xf bank_mask:0xc
	s_waitcnt lgkmcnt(0)
	v_add_f32_e32 v2, v2, v40
	ds_bpermute_b32 v40, v103, v2
	s_waitcnt lgkmcnt(0)
	v_add_f32_e32 v2, v2, v40
	ds_bpermute_b32 v40, v104, v2
	s_waitcnt lgkmcnt(0)
	v_add_f32_e32 v2, v2, v40
	v_fmamk_f32 v2, v2, 0x3a800000, v241
	v_rsq_f32_e32 v2, v2
	s_nop 0
	v_pk_mul_f32 v[48:49], v[48:49], v[2:3] op_sel_hi:[1,0]
	v_pk_mul_f32 v[44:45], v[44:45], v[2:3] op_sel_hi:[1,0]
	v_pk_mul_f32 v[40:41], v[54:55], v[2:3] op_sel_hi:[1,0]
	v_pk_mul_f32 v[42:43], v[58:59], v[2:3] op_sel_hi:[1,0]
	v_pk_fma_f32 v[46:47], v[14:15], v[44:45], v[30:31]
	v_pk_fma_f32 v[44:45], v[12:13], v[48:49], v[28:29]
	v_pk_mul_f32 v[48:49], v[56:57], v[2:3] op_sel_hi:[1,0]
	v_pk_mul_f32 v[50:51], v[52:53], v[2:3] op_sel_hi:[1,0]
	v_pk_mul_f32 v[52:53], v[62:63], v[2:3] op_sel_hi:[1,0]
	v_pk_mul_f32 v[54:55], v[60:61], v[2:3] op_sel_hi:[1,0]
	v_pk_fma_f32 v[42:43], v[18:19], v[42:43], v[34:35]
	v_pk_fma_f32 v[40:41], v[16:17], v[40:41], v[32:33]
	v_pk_fma_f32 v[50:51], v[10:11], v[50:51], v[26:27]
	v_pk_fma_f32 v[48:49], v[8:9], v[48:49], v[24:25]
	v_pk_fma_f32 v[54:55], v[6:7], v[54:55], v[22:23]
	v_pk_fma_f32 v[52:53], v[4:5], v[52:53], v[20:21]
	s_cbranch_vccnz .LBB0_1066
	v_cvt_pk_bf16_f32 v56, v40, v41
	v_cvt_pk_bf16_f32 v57, v42, v43
	v_cvt_pk_bf16_f32 v58, v44, v45
	v_cvt_pk_bf16_f32 v59, v46, v47
	v_cvt_pk_bf16_f32 v60, v48, v49
	v_cvt_pk_bf16_f32 v61, v50, v51
	v_cvt_pk_bf16_f32 v62, v52, v53
	v_cvt_pk_bf16_f32 v63, v54, v55
	global_store_dwordx4 v[88:89], v[56:59], off
	global_store_dwordx4 v[88:89], v[60:63], off offset:16
	s_lshl_b64 s[12:13], s[10:11], 10
	v_mov_b32_e32 v56, v3
	v_mov_b32_e32 v57, v3
	v_mov_b32_e32 v58, v3
	v_mov_b32_e32 v59, v3
	v_cvt_pk_fp8_f32 v56, v40, v41
	v_cvt_pk_fp8_f32 v57, v44, v45
	v_cvt_pk_fp8_f32 v58, v48, v49
	v_cvt_pk_fp8_f32 v59, v52, v53
	v_cvt_pk_fp8_f32 v56, v42, v43 op_sel:[0,0,1]
	v_cvt_pk_fp8_f32 v57, v46, v47 op_sel:[0,0,1]
	v_cvt_pk_fp8_f32 v58, v50, v51 op_sel:[0,0,1]
	v_cvt_pk_fp8_f32 v59, v54, v55 op_sel:[0,0,1]
	v_lshl_add_u64 v[60:61], v[84:85], 0, s[12:13]
	s_mov_b64 s[12:13], 0
	global_store_dwordx4 v[60:61], v[56:59], off
